# P3 epilogues: 16 ssp quads loaded up front (vmcnt(14) per block); attention epilogue: lane^1/lane^2 exchanges via DPP quad_perm instead of ds_bpermute
# speedup vs baseline: 1.0027x; 1.0027x over previous
; __device__ __forceinline__ u32x4 pack8(f32x4 a, f32x4 b) { u32x4 w; w.x = cvtpk(a[0], a[1]); w.y = cvtpk(a[2], a[3]); w.z = cvtpk(b[0], b[1]); w.w = cvtpk(b[2], b[3]); return w; }
; __device__ __forceinline__ float latent_rstd(const float* ssp, int row, int which) {
;     const f32x4 a = *(const f32x4*)(ssp + ((size_t)row * 2 + which) * 8), b = *(const f32x4*)(ssp + ((size_t)row * 2 + which) * 8 + 4);
;     return 1.0f / sqrtf((((a[0] + a[1]) + (a[2] + a[3])) + ((b[0] + b[1]) + (b[2] + b[3]))) * (1.0f / 512.0f) + 1e-6f);
; }
;     __device__ __forceinline__ void operator()(const Acc& acc, const Unit& u, int wr, int wc, int fr, int fq) const {
;         const int row0 = u.row0 + wr * 64 + fr, col0 = u.col0 + wc * 32 + 8 * fq;
; #pragma unroll
;         for (int ai = 0; ai < 2; ++ai)
; #pragma unroll
;             for (int m = 0; m < 4; ++m) { const int row = row0 + ai * HALF + m * 16, pos = row & (SEQ - 1); const float rs = latent_rstd(ssp, row, 0); bf16_t* rowp = O + (size_t)row * ldc + col0;
; #pragma unroll
;                 for (int bj = 0; bj < 2; ++bj) { f32x4 v0 = acc[ai][bj][m][0] * rs, v1 = acc[ai][bj][m][1] * rs; const int d = (col0 + bj * HALF) % 192;
;                     if (d >= 128) { const int jj = (d - 128) >> 1; const f32x4 c01 = rope[pos * 16 + (jj >> 1)], c23 = rope[pos * 16 + (jj >> 1) + 1];
;                         f32x4 w0, w1;
;                         w0[0] = v0[0] * c01[0] - v0[1] * c01[1]; w0[1] = v0[0] * c01[1] + v0[1] * c01[0];
;                         w0[2] = v0[2] * c01[2] - v0[3] * c01[3]; w0[3] = v0[2] * c01[3] + v0[3] * c01[2];
;                         w1[0] = v1[0] * c23[0] - v1[1] * c23[1]; w1[1] = v1[0] * c23[1] + v1[1] * c23[0];
;                         w1[2] = v1[2] * c23[2] - v1[3] * c23[3]; w1[3] = v1[2] * c23[3] + v1[3] * c23[2];
;                         v0 = w0; v1 = w1; }
;                     *(u32x4*)(rowp + bj * HALF) = pack8(v0, v1); } }
.LBB0_1265:
	v_mbcnt_lo_u32_b32 v130, -1, 0
	v_mbcnt_hi_u32_b32 v130, -1, v130
	s_add_i32 s4, s26, s65
	v_and_b32_e32 v132, 15, v130
	v_add_u32_e32 v134, s4, v132
	v_ashrrev_i32_e32 v135, 31, v134
	v_lshlrev_b64 v[132:133], 6, v[134:135]
	v_lshl_add_u64 v[132:133], s[10:11], 0, v[132:133]
	v_lshlrev_b32_e32 v250, 6, v134
	global_load_dwordx4 v[182:185], v250, s[10:11]
	global_load_dwordx4 v[186:189], v250, s[10:11] offset:16
	v_add_u32_e32 v250, 16, v134
	v_lshlrev_b32_e32 v250, 6, v250
	global_load_dwordx4 v[190:193], v250, s[10:11]
	global_load_dwordx4 v[194:197], v250, s[10:11] offset:16
	v_add_u32_e32 v250, 32, v134
	v_lshlrev_b32_e32 v250, 6, v250
	global_load_dwordx4 v[200:203], v250, s[10:11]
	global_load_dwordx4 v[204:207], v250, s[10:11] offset:16
	v_add_u32_e32 v250, 48, v134
	v_lshlrev_b32_e32 v250, 6, v250
	global_load_dwordx4 v[208:211], v250, s[10:11]
	global_load_dwordx4 v[212:215], v250, s[10:11] offset:16
	v_add_u32_e32 v250, 128, v134
	v_lshlrev_b32_e32 v250, 6, v250
	global_load_dwordx4 v[216:219], v250, s[10:11]
	global_load_dwordx4 v[220:223], v250, s[10:11] offset:16
	v_add_u32_e32 v250, 144, v134
	v_lshlrev_b32_e32 v250, 6, v250
	global_load_dwordx4 v[224:227], v250, s[10:11]
	global_load_dwordx4 v[228:231], v250, s[10:11] offset:16
	v_add_u32_e32 v250, 160, v134
	v_lshlrev_b32_e32 v250, 6, v250
	global_load_dwordx4 v[232:235], v250, s[10:11]
	global_load_dwordx4 v[236:239], v250, s[10:11] offset:16
	v_add_u32_e32 v250, 176, v134
	v_lshlrev_b32_e32 v250, 6, v250
	global_load_dwordx4 v[240:243], v250, s[10:11]
	global_load_dwordx4 v[244:247], v250, s[10:11] offset:16
	v_ashrrev_i32_e32 v130, 1, v130
	s_add_i32 s3, s3, s66
	v_and_b32_e32 v130, -8, v130
	v_add_u32_e32 v132, s3, v130
	v_lshlrev_b32_e32 v130, 4, v134
	v_and_b32_e32 v157, 0xfff0, v130
	v_mul_hi_i32 v130, v132, s88
	v_lshrrev_b32_e32 v133, 31, v130
	v_lshrrev_b32_e32 v130, 5, v130
	v_add_u32_e32 v130, v130, v133
	v_mul_lo_u32 v130, v130, s90
	v_sub_u32_e32 v130, v132, v130
	v_cmp_lt_i32_e64 s[4:5], s91, v130
	v_add_u32_e32 v130, 0xffffff80, v130
	s_waitcnt vmcnt(14)
	v_mov_b32_e32 v136, v182
	v_mov_b32_e32 v137, v183
	v_mov_b32_e32 v138, v184
	v_mov_b32_e32 v139, v185
	v_mov_b32_e32 v162, v136
	v_mov_b32_e32 v158, v186
	v_mov_b32_e32 v159, v187
	v_mov_b32_e32 v160, v188
	v_mov_b32_e32 v161, v189
	v_mov_b32_e32 v163, v158
	v_mov_b32_e32 v158, v137
	v_mov_b32_e32 v136, v138
	v_mov_b32_e32 v137, v160
	v_mov_b32_e32 v160, v139
	v_pk_add_f32 v[138:139], v[162:163], v[158:159]
	v_pk_add_f32 v[136:137], v[136:137], v[160:161]
	s_nop 0
	v_pk_add_f32 v[136:137], v[138:139], v[136:137]
	s_nop 0
	v_add_f32_e32 v133, v136, v137
	v_fmamk_f32 v133, v133, 0x3b000000, v155
	v_mul_f32_e32 v135, 0x4f800000, v133
	v_cmp_gt_f32_e32 vcc, s89, v133
	s_nop 1
	v_cndmask_b32_e32 v133, v133, v135, vcc
	v_sqrt_f32_e32 v135, v133
	s_nop 0
	v_add_u32_e32 v136, -1, v135
	v_add_u32_e32 v137, 1, v135
	v_fma_f32 v138, -v136, v135, v133
	v_fma_f32 v139, -v137, v135, v133
	v_cmp_ge_f32_e64 s[6:7], 0, v138
	s_nop 1
	v_cndmask_b32_e64 v135, v135, v136, s[6:7]
	v_cmp_lt_f32_e64 s[6:7], 0, v139
	s_nop 1
	v_cndmask_b32_e64 v135, v135, v137, s[6:7]
	v_mul_f32_e32 v136, 0x37800000, v135
	v_cndmask_b32_e32 v135, v135, v136, vcc
	v_cmp_class_f32_e32 vcc, v133, v156
	s_nop 1
	v_cndmask_b32_e32 v133, v135, v133, vcc
	v_div_scale_f32 v135, s[6:7], v133, v133, 1.0
	v_rcp_f32_e32 v136, v135
	v_div_scale_f32 v137, vcc, 1.0, v133, 1.0
	v_fma_f32 v138, -v135, v136, 1.0
	v_fmac_f32_e32 v136, v138, v136
	v_mul_f32_e32 v138, v137, v136
	v_fma_f32 v139, -v135, v138, v137
	v_fmac_f32_e32 v138, v139, v136
	v_fma_f32 v135, -v135, v138, v137
	v_div_fmas_f32 v135, v135, v136, v138
	v_div_fixup_f32 v136, v135, v133, 1.0
	v_pk_mul_f32 v[138:139], v[128:129], v[136:137] op_sel_hi:[1,0]
	v_pk_mul_f32 v[126:127], v[126:127], v[136:137] op_sel_hi:[1,0]
	v_pk_mul_f32 v[128:129], v[124:125], v[136:137] op_sel_hi:[1,0]
	v_pk_mul_f32 v[124:125], v[122:123], v[136:137] op_sel_hi:[1,0]
	v_lshrrev_b32_e32 v135, 2, v130
	s_and_saveexec_b64 s[6:7], s[4:5]
	s_cbranch_execz .LBB0_1267
	v_add_u32_e32 v130, v135, v157
	v_lshl_add_u64 v[122:123], v[130:131], 4, s[38:39]
	global_load_dwordx4 v[158:161], v[122:123], off
	global_load_dwordx4 v[168:171], v[122:123], off offset:16
	s_waitcnt vmcnt(1)
	v_pk_mul_f32 v[162:163], v[126:127], v[158:159] op_sel:[1,1] op_sel_hi:[1,0]
	v_mul_f32_e32 v130, v139, v161
	v_mul_f32_e32 v172, v139, v160
	s_waitcnt vmcnt(0)
	v_pk_mul_f32 v[176:177], v[124:125], v[168:169] op_sel:[1,1] op_sel_hi:[1,0]
	v_mul_f32_e32 v178, v129, v171
	v_mul_f32_e32 v180, v129, v170
	v_pk_mul_f32 v[122:123], v[126:127], v[158:159]
	v_pk_mul_f32 v[174:175], v[124:125], v[168:169]
	v_pk_fma_f32 v[126:127], v[126:127], v[158:159], v[162:163] op_sel_hi:[0,1,1]
	v_pk_fma_f32 v[158:159], v[138:139], v[160:161], v[130:131] op_sel_hi:[1,1,0] neg_lo:[0,0,1] neg_hi:[0,0,1]
	v_pk_fma_f32 v[160:161], v[138:139], v[160:161], v[172:173] op_sel:[0,1,0] op_sel_hi:[1,0,0]
	v_pk_fma_f32 v[124:125], v[124:125], v[168:169], v[176:177] op_sel_hi:[0,1,1]
	v_pk_fma_f32 v[168:169], v[128:129], v[170:171], v[178:179] op_sel_hi:[1,1,0] neg_lo:[0,0,1] neg_hi:[0,0,1]
	v_pk_fma_f32 v[170:171], v[128:129], v[170:171], v[180:181] op_sel:[0,1,0] op_sel_hi:[1,0,0]
	v_sub_f32_e32 v126, v122, v162
	v_sub_f32_e32 v124, v174, v176
	v_mov_b32_e32 v138, v158
	v_mov_b32_e32 v139, v160
	v_mov_b32_e32 v128, v168
	v_mov_b32_e32 v129, v170

; __device__ __forceinline__ u32x4 pack8(f32x4 a, f32x4 b) { u32x4 w; w.x = cvtpk(a[0], a[1]); w.y = cvtpk(a[2], a[3]); w.z = cvtpk(b[0], b[1]); w.w = cvtpk(b[2], b[3]); return w; }
; __device__ __forceinline__ float latent_rstd(const float* ssp, int row, int which) {
;     const f32x4 a = *(const f32x4*)(ssp + ((size_t)row * 2 + which) * 8), b = *(const f32x4*)(ssp + ((size_t)row * 2 + which) * 8 + 4);
;     return 1.0f / sqrtf((((a[0] + a[1]) + (a[2] + a[3])) + ((b[0] + b[1]) + (b[2] + b[3]))) * (1.0f / 512.0f) + 1e-6f);
; }
;     __device__ __forceinline__ void operator()(const Acc& acc, const Unit& u, int wr, int wc, int fr, int fq) const {
;     ...
;             for (int m = 0; m < 4; ++m) { const int row = row0 + ai * HALF + m * 16, pos = row & (SEQ - 1); const float rs = latent_rstd(ssp, row, 0); bf16_t* rowp = O + (size_t)row * ldc + col0;
; #pragma unroll
;                 for (int bj = 0; bj < 2; ++bj) { f32x4 v0 = acc[ai][bj][m][0] * rs, v1 = acc[ai][bj][m][1] * rs; const int d = (col0 + bj * HALF) % 192;
;                     if (d >= 128) { const int jj = (d - 128) >> 1; const f32x4 c01 = rope[pos * 16 + (jj >> 1)], c23 = rope[pos * 16 + (jj >> 1) + 1];
;                         f32x4 w0, w1;
;                         w0[0] = v0[0] * c01[0] - v0[1] * c01[1]; w0[1] = v0[0] * c01[1] + v0[1] * c01[0];
;                         w0[2] = v0[2] * c01[2] - v0[3] * c01[3]; w0[3] = v0[2] * c01[3] + v0[3] * c01[2];
;                         w1[0] = v1[0] * c23[0] - v1[1] * c23[1]; w1[1] = v1[0] * c23[1] + v1[1] * c23[0];
;                         w1[2] = v1[2] * c23[2] - v1[3] * c23[3]; w1[3] = v1[2] * c23[3] + v1[3] * c23[2];
;                         v0 = w0; v1 = w1; }
;                     *(u32x4*)(rowp + bj * HALF) = pack8(v0, v1); } }
.LBB0_1269:
	s_or_b64 exec, exec, s[8:9]
	v_cvt_pk_bf16_f32 v118, v118, v119
	v_cvt_pk_bf16_f32 v119, v120, v121
	v_cvt_pk_bf16_f32 v120, v114, v115
	v_add_u32_e32 v114, 16, v134
	v_ashrrev_i32_e32 v115, 31, v114
	v_cvt_pk_bf16_f32 v121, v116, v117
	v_lshlrev_b64 v[116:117], 6, v[114:115]
	global_store_dwordx4 v[122:123], v[118:121], off offset:256
	s_nop 1
	v_lshl_add_u64 v[120:121], s[10:11], 0, v[116:117]
	s_nop 0
	s_waitcnt vmcnt(14)
	v_mov_b32_e32 v116, v190
	v_mov_b32_e32 v117, v191
	v_mov_b32_e32 v118, v192
	v_mov_b32_e32 v119, v193
	v_mov_b32_e32 v126, v116
	v_mov_b32_e32 v120, v194
	v_mov_b32_e32 v121, v195
	v_mov_b32_e32 v122, v196
	v_mov_b32_e32 v123, v197
	v_mov_b32_e32 v127, v120
	v_mov_b32_e32 v120, v117
	v_mov_b32_e32 v116, v118
	v_mov_b32_e32 v117, v122
	v_mov_b32_e32 v122, v119
	v_pk_add_f32 v[118:119], v[126:127], v[120:121]
	v_pk_add_f32 v[116:117], v[116:117], v[122:123]
	s_nop 0
	v_pk_add_f32 v[116:117], v[118:119], v[116:117]
	s_nop 0
	v_add_f32_e32 v115, v116, v117
	v_fmamk_f32 v115, v115, 0x3b000000, v155
	v_mul_f32_e32 v116, 0x4f800000, v115
	v_cmp_gt_f32_e32 vcc, s89, v115
	v_lshlrev_b32_e32 v117, 4, v114
	s_nop 0
	v_cndmask_b32_e32 v115, v115, v116, vcc
	v_sqrt_f32_e32 v116, v115
	s_nop 0
	v_add_u32_e32 v118, -1, v116
	v_add_u32_e32 v119, 1, v116
	v_fma_f32 v120, -v118, v116, v115
	v_fma_f32 v121, -v119, v116, v115
	v_cmp_ge_f32_e64 s[8:9], 0, v120
	s_nop 1
	v_cndmask_b32_e64 v116, v116, v118, s[8:9]
	v_cmp_lt_f32_e64 s[8:9], 0, v121
	s_nop 1
	v_cndmask_b32_e64 v116, v116, v119, s[8:9]
	v_mul_f32_e32 v118, 0x37800000, v116
	v_cndmask_b32_e32 v116, v116, v118, vcc
	v_cmp_class_f32_e32 vcc, v115, v156
	s_nop 1
	v_cndmask_b32_e32 v116, v116, v115, vcc
	v_div_scale_f32 v118, s[8:9], v116, v116, 1.0
	v_rcp_f32_e32 v119, v118
	v_and_b32_e32 v115, 0xfff0, v117
	v_div_scale_f32 v117, vcc, 1.0, v116, 1.0
	v_fma_f32 v120, -v118, v119, 1.0
	v_fmac_f32_e32 v119, v120, v119
	v_mul_f32_e32 v120, v117, v119
	v_fma_f32 v121, -v118, v120, v117
	v_fmac_f32_e32 v120, v121, v119
	v_fma_f32 v117, -v118, v120, v117
	v_div_fmas_f32 v117, v117, v119, v120
	v_div_fixup_f32 v116, v117, v116, 1.0
	v_pk_mul_f32 v[112:113], v[112:113], v[116:117] op_sel_hi:[1,0]
	v_pk_mul_f32 v[110:111], v[110:111], v[116:117] op_sel_hi:[1,0]
	v_pk_mul_f32 v[118:119], v[108:109], v[116:117] op_sel_hi:[1,0]
	v_pk_mul_f32 v[108:109], v[106:107], v[116:117] op_sel_hi:[1,0]
	s_and_saveexec_b64 s[8:9], s[4:5]
	s_cbranch_execz .LBB0_1271
	v_add_u32_e32 v130, v135, v115
	v_lshl_add_u64 v[106:107], v[130:131], 4, s[38:39]
	global_load_dwordx4 v[120:123], v[106:107], off
	global_load_dwordx4 v[126:129], v[106:107], off offset:16
	s_waitcnt vmcnt(1)
	v_pk_mul_f32 v[136:137], v[110:111], v[120:121] op_sel:[1,1] op_sel_hi:[1,0]
	v_mul_f32_e32 v130, v113, v123
	v_mul_f32_e32 v138, v113, v122
	s_waitcnt vmcnt(0)
	v_pk_mul_f32 v[160:161], v[108:109], v[126:127] op_sel:[1,1] op_sel_hi:[1,0]
	v_mul_f32_e32 v162, v119, v129
	v_mul_f32_e32 v168, v119, v128
	v_pk_mul_f32 v[106:107], v[110:111], v[120:121]
	v_pk_mul_f32 v[158:159], v[108:109], v[126:127]
	v_pk_fma_f32 v[110:111], v[110:111], v[120:121], v[136:137] op_sel_hi:[0,1,1]
	v_pk_fma_f32 v[120:121], v[112:113], v[122:123], v[130:131] op_sel_hi:[1,1,0] neg_lo:[0,0,1] neg_hi:[0,0,1]
	v_pk_fma_f32 v[122:123], v[112:113], v[122:123], v[138:139] op_sel:[0,1,0] op_sel_hi:[1,0,0]
	v_pk_fma_f32 v[108:109], v[108:109], v[126:127], v[160:161] op_sel_hi:[0,1,1]
	v_pk_fma_f32 v[126:127], v[118:119], v[128:129], v[162:163] op_sel_hi:[1,1,0] neg_lo:[0,0,1] neg_hi:[0,0,1]
	v_pk_fma_f32 v[128:129], v[118:119], v[128:129], v[168:169] op_sel:[0,1,0] op_sel_hi:[1,0,0]
	v_sub_f32_e32 v110, v106, v136
	v_sub_f32_e32 v108, v158, v160
	v_mov_b32_e32 v112, v120
	v_mov_b32_e32 v113, v122
	v_mov_b32_e32 v118, v126
	v_mov_b32_e32 v119, v128

; __device__ __forceinline__ u32x4 pack8(f32x4 a, f32x4 b) { u32x4 w; w.x = cvtpk(a[0], a[1]); w.y = cvtpk(a[2], a[3]); w.z = cvtpk(b[0], b[1]); w.w = cvtpk(b[2], b[3]); return w; }
; __device__ __forceinline__ float latent_rstd(const float* ssp, int row, int which) {
;     const f32x4 a = *(const f32x4*)(ssp + ((size_t)row * 2 + which) * 8), b = *(const f32x4*)(ssp + ((size_t)row * 2 + which) * 8 + 4);
;     return 1.0f / sqrtf((((a[0] + a[1]) + (a[2] + a[3])) + ((b[0] + b[1]) + (b[2] + b[3]))) * (1.0f / 512.0f) + 1e-6f);
; }
;     __device__ __forceinline__ void operator()(const Acc& acc, const Unit& u, int wr, int wc, int fr, int fq) const {
;     ...
;             for (int m = 0; m < 4; ++m) { const int row = row0 + ai * HALF + m * 16, pos = row & (SEQ - 1); const float rs = latent_rstd(ssp, row, 0); bf16_t* rowp = O + (size_t)row * ldc + col0;
; #pragma unroll
;                 for (int bj = 0; bj < 2; ++bj) { f32x4 v0 = acc[ai][bj][m][0] * rs, v1 = acc[ai][bj][m][1] * rs; const int d = (col0 + bj * HALF) % 192;
;                     if (d >= 128) { const int jj = (d - 128) >> 1; const f32x4 c01 = rope[pos * 16 + (jj >> 1)], c23 = rope[pos * 16 + (jj >> 1) + 1];
;                         f32x4 w0, w1;
;                         w0[0] = v0[0] * c01[0] - v0[1] * c01[1]; w0[1] = v0[0] * c01[1] + v0[1] * c01[0];
;                         w0[2] = v0[2] * c01[2] - v0[3] * c01[3]; w0[3] = v0[2] * c01[3] + v0[3] * c01[2];
;                         w1[0] = v1[0] * c23[0] - v1[1] * c23[1]; w1[1] = v1[0] * c23[1] + v1[1] * c23[0];
;                         w1[2] = v1[2] * c23[2] - v1[3] * c23[3]; w1[3] = v1[2] * c23[3] + v1[3] * c23[2];
;                         v0 = w0; v1 = w1; }
;                     *(u32x4*)(rowp + bj * HALF) = pack8(v0, v1); } }
.LBB0_1273:
	s_or_b64 exec, exec, s[8:9]
	v_cvt_pk_bf16_f32 v102, v102, v103
	v_cvt_pk_bf16_f32 v103, v104, v105
	v_cvt_pk_bf16_f32 v104, v98, v99
	v_add_u32_e32 v98, 32, v134
	v_ashrrev_i32_e32 v99, 31, v98
	v_cvt_pk_bf16_f32 v105, v100, v101
	v_lshlrev_b64 v[100:101], 6, v[98:99]
	global_store_dwordx4 v[106:107], v[102:105], off offset:256
	s_nop 1
	v_lshl_add_u64 v[104:105], s[10:11], 0, v[100:101]
	s_nop 0
	s_waitcnt vmcnt(14)
	v_mov_b32_e32 v100, v200
	v_mov_b32_e32 v101, v201
	v_mov_b32_e32 v102, v202
	v_mov_b32_e32 v103, v203
	v_mov_b32_e32 v108, v100
	v_mov_b32_e32 v104, v204
	v_mov_b32_e32 v105, v205
	v_mov_b32_e32 v106, v206
	v_mov_b32_e32 v107, v207
	v_mov_b32_e32 v109, v104
	v_mov_b32_e32 v104, v101
	v_mov_b32_e32 v100, v102
	v_mov_b32_e32 v101, v106
	v_mov_b32_e32 v106, v103
	v_pk_add_f32 v[102:103], v[108:109], v[104:105]
	v_pk_add_f32 v[100:101], v[100:101], v[106:107]
	s_nop 0
	v_pk_add_f32 v[100:101], v[102:103], v[100:101]
	s_nop 0
	v_add_f32_e32 v99, v100, v101
	v_fmamk_f32 v99, v99, 0x3b000000, v155
	v_mul_f32_e32 v100, 0x4f800000, v99
	v_cmp_gt_f32_e32 vcc, s89, v99
	v_lshlrev_b32_e32 v101, 4, v98
	s_nop 0
	v_cndmask_b32_e32 v99, v99, v100, vcc
	v_sqrt_f32_e32 v100, v99
	s_nop 0
	v_add_u32_e32 v102, -1, v100
	v_add_u32_e32 v103, 1, v100
	v_fma_f32 v104, -v102, v100, v99
	v_fma_f32 v105, -v103, v100, v99
	v_cmp_ge_f32_e64 s[8:9], 0, v104
	s_nop 1
	v_cndmask_b32_e64 v100, v100, v102, s[8:9]
	v_cmp_lt_f32_e64 s[8:9], 0, v105
	s_nop 1
	v_cndmask_b32_e64 v100, v100, v103, s[8:9]
	v_mul_f32_e32 v102, 0x37800000, v100
	v_cndmask_b32_e32 v100, v100, v102, vcc
	v_cmp_class_f32_e32 vcc, v99, v156
	s_nop 1
	v_cndmask_b32_e32 v100, v100, v99, vcc
	v_div_scale_f32 v102, s[8:9], v100, v100, 1.0
	v_rcp_f32_e32 v103, v102
	v_and_b32_e32 v99, 0xfff0, v101
	v_div_scale_f32 v101, vcc, 1.0, v100, 1.0
	v_fma_f32 v104, -v102, v103, 1.0
	v_fmac_f32_e32 v103, v104, v103
	v_mul_f32_e32 v104, v101, v103
	v_fma_f32 v105, -v102, v104, v101
	v_fmac_f32_e32 v104, v105, v103
	v_fma_f32 v101, -v102, v104, v101
	v_div_fmas_f32 v101, v101, v103, v104
	v_div_fixup_f32 v100, v101, v100, 1.0
	v_pk_mul_f32 v[96:97], v[96:97], v[100:101] op_sel_hi:[1,0]
	v_pk_mul_f32 v[94:95], v[94:95], v[100:101] op_sel_hi:[1,0]
	v_pk_mul_f32 v[102:103], v[92:93], v[100:101] op_sel_hi:[1,0]
	v_pk_mul_f32 v[92:93], v[90:91], v[100:101] op_sel_hi:[1,0]
	s_and_saveexec_b64 s[8:9], s[4:5]
	s_cbranch_execz .LBB0_1275
	v_add_u32_e32 v130, v135, v99
	v_lshl_add_u64 v[90:91], v[130:131], 4, s[38:39]
	global_load_dwordx4 v[104:107], v[90:91], off
	global_load_dwordx4 v[108:111], v[90:91], off offset:16
	s_waitcnt vmcnt(1)
	v_pk_mul_f32 v[112:113], v[94:95], v[104:105] op_sel:[1,1] op_sel_hi:[1,0]
	v_mul_f32_e32 v114, v97, v107
	v_mul_f32_e32 v116, v97, v106
	s_waitcnt vmcnt(0)
	v_pk_mul_f32 v[120:121], v[92:93], v[108:109] op_sel:[1,1] op_sel_hi:[1,0]
	v_mul_f32_e32 v122, v103, v111
	v_mul_f32_e32 v126, v103, v110
	v_pk_mul_f32 v[90:91], v[94:95], v[104:105]
	v_pk_mul_f32 v[118:119], v[92:93], v[108:109]
	v_pk_fma_f32 v[94:95], v[94:95], v[104:105], v[112:113] op_sel_hi:[0,1,1]
	v_pk_fma_f32 v[104:105], v[96:97], v[106:107], v[114:115] op_sel_hi:[1,1,0] neg_lo:[0,0,1] neg_hi:[0,0,1]
	v_pk_fma_f32 v[106:107], v[96:97], v[106:107], v[116:117] op_sel:[0,1,0] op_sel_hi:[1,0,0]
	v_pk_fma_f32 v[92:93], v[92:93], v[108:109], v[120:121] op_sel_hi:[0,1,1]
	v_pk_fma_f32 v[108:109], v[102:103], v[110:111], v[122:123] op_sel_hi:[1,1,0] neg_lo:[0,0,1] neg_hi:[0,0,1]
	v_pk_fma_f32 v[110:111], v[102:103], v[110:111], v[126:127] op_sel:[0,1,0] op_sel_hi:[1,0,0]
	v_sub_f32_e32 v94, v90, v112
	v_sub_f32_e32 v92, v118, v120
	v_mov_b32_e32 v96, v104
	v_mov_b32_e32 v97, v106
	v_mov_b32_e32 v102, v108
	v_mov_b32_e32 v103, v110

; __device__ __forceinline__ u32x4 pack8(f32x4 a, f32x4 b) { u32x4 w; w.x = cvtpk(a[0], a[1]); w.y = cvtpk(a[2], a[3]); w.z = cvtpk(b[0], b[1]); w.w = cvtpk(b[2], b[3]); return w; }
; __device__ __forceinline__ float latent_rstd(const float* ssp, int row, int which) {
;     const f32x4 a = *(const f32x4*)(ssp + ((size_t)row * 2 + which) * 8), b = *(const f32x4*)(ssp + ((size_t)row * 2 + which) * 8 + 4);
;     return 1.0f / sqrtf((((a[0] + a[1]) + (a[2] + a[3])) + ((b[0] + b[1]) + (b[2] + b[3]))) * (1.0f / 512.0f) + 1e-6f);
; }
;     __device__ __forceinline__ void operator()(const Acc& acc, const Unit& u, int wr, int wc, int fr, int fq) const {
;     ...
;             for (int m = 0; m < 4; ++m) { const int row = row0 + ai * HALF + m * 16, pos = row & (SEQ - 1); const float rs = latent_rstd(ssp, row, 0); bf16_t* rowp = O + (size_t)row * ldc + col0;
; #pragma unroll
;                 for (int bj = 0; bj < 2; ++bj) { f32x4 v0 = acc[ai][bj][m][0] * rs, v1 = acc[ai][bj][m][1] * rs; const int d = (col0 + bj * HALF) % 192;
;                     if (d >= 128) { const int jj = (d - 128) >> 1; const f32x4 c01 = rope[pos * 16 + (jj >> 1)], c23 = rope[pos * 16 + (jj >> 1) + 1];
;                         f32x4 w0, w1;
;                         w0[0] = v0[0] * c01[0] - v0[1] * c01[1]; w0[1] = v0[0] * c01[1] + v0[1] * c01[0];
;                         w0[2] = v0[2] * c01[2] - v0[3] * c01[3]; w0[3] = v0[2] * c01[3] + v0[3] * c01[2];
;                         w1[0] = v1[0] * c23[0] - v1[1] * c23[1]; w1[1] = v1[0] * c23[1] + v1[1] * c23[0];
;                         w1[2] = v1[2] * c23[2] - v1[3] * c23[3]; w1[3] = v1[2] * c23[3] + v1[3] * c23[2];
;                         v0 = w0; v1 = w1; }
;                     *(u32x4*)(rowp + bj * HALF) = pack8(v0, v1); } }
.LBB0_1277:
	s_or_b64 exec, exec, s[8:9]
	v_cvt_pk_bf16_f32 v86, v86, v87
	v_cvt_pk_bf16_f32 v87, v88, v89
	v_cvt_pk_bf16_f32 v88, v82, v83
	v_add_u32_e32 v82, 48, v134
	v_ashrrev_i32_e32 v83, 31, v82
	v_cvt_pk_bf16_f32 v89, v84, v85
	v_lshlrev_b64 v[84:85], 6, v[82:83]
	global_store_dwordx4 v[90:91], v[86:89], off offset:256
	s_nop 1
	v_lshl_add_u64 v[88:89], s[10:11], 0, v[84:85]
	s_nop 0
	s_waitcnt vmcnt(14)
	v_mov_b32_e32 v84, v208
	v_mov_b32_e32 v85, v209
	v_mov_b32_e32 v86, v210
	v_mov_b32_e32 v87, v211
	v_mov_b32_e32 v92, v84
	v_mov_b32_e32 v88, v212
	v_mov_b32_e32 v89, v213
	v_mov_b32_e32 v90, v214
	v_mov_b32_e32 v91, v215
	v_mov_b32_e32 v93, v88
	v_mov_b32_e32 v88, v85
	v_mov_b32_e32 v84, v86
	v_mov_b32_e32 v85, v90
	v_mov_b32_e32 v90, v87
	v_pk_add_f32 v[86:87], v[92:93], v[88:89]
	v_pk_add_f32 v[84:85], v[84:85], v[90:91]
	s_nop 0
	v_pk_add_f32 v[84:85], v[86:87], v[84:85]
	s_nop 0
	v_add_f32_e32 v83, v84, v85
	v_fmamk_f32 v83, v83, 0x3b000000, v155
	v_mul_f32_e32 v84, 0x4f800000, v83
	v_cmp_gt_f32_e32 vcc, s89, v83
	v_lshlrev_b32_e32 v85, 4, v82
	s_nop 0
	v_cndmask_b32_e32 v83, v83, v84, vcc
	v_sqrt_f32_e32 v84, v83
	s_nop 0
	v_add_u32_e32 v86, -1, v84
	v_add_u32_e32 v87, 1, v84
	v_fma_f32 v88, -v86, v84, v83
	v_fma_f32 v89, -v87, v84, v83
	v_cmp_ge_f32_e64 s[8:9], 0, v88
	s_nop 1
	v_cndmask_b32_e64 v84, v84, v86, s[8:9]
	v_cmp_lt_f32_e64 s[8:9], 0, v89
	s_nop 1
	v_cndmask_b32_e64 v84, v84, v87, s[8:9]
	v_mul_f32_e32 v86, 0x37800000, v84
	v_cndmask_b32_e32 v84, v84, v86, vcc
	v_cmp_class_f32_e32 vcc, v83, v156
	s_nop 1
	v_cndmask_b32_e32 v84, v84, v83, vcc
	v_div_scale_f32 v86, s[8:9], v84, v84, 1.0
	v_rcp_f32_e32 v87, v86
	v_and_b32_e32 v83, 0xfff0, v85
	v_div_scale_f32 v85, vcc, 1.0, v84, 1.0
	v_fma_f32 v88, -v86, v87, 1.0
	v_fmac_f32_e32 v87, v88, v87
	v_mul_f32_e32 v88, v85, v87
	v_fma_f32 v89, -v86, v88, v85
	v_fmac_f32_e32 v88, v89, v87
	v_fma_f32 v85, -v86, v88, v85
	v_div_fmas_f32 v85, v85, v87, v88
	v_div_fixup_f32 v84, v85, v84, 1.0
	v_pk_mul_f32 v[80:81], v[80:81], v[84:85] op_sel_hi:[1,0]
	v_pk_mul_f32 v[78:79], v[78:79], v[84:85] op_sel_hi:[1,0]
	v_pk_mul_f32 v[86:87], v[76:77], v[84:85] op_sel_hi:[1,0]
	v_pk_mul_f32 v[76:77], v[74:75], v[84:85] op_sel_hi:[1,0]
	s_and_saveexec_b64 s[8:9], s[4:5]
	s_cbranch_execz .LBB0_1279
	v_add_u32_e32 v130, v135, v83
	v_lshl_add_u64 v[74:75], v[130:131], 4, s[38:39]
	global_load_dwordx4 v[88:91], v[74:75], off
	global_load_dwordx4 v[92:95], v[74:75], off offset:16
	s_waitcnt vmcnt(1)
	v_pk_mul_f32 v[96:97], v[78:79], v[88:89] op_sel:[1,1] op_sel_hi:[1,0]
	v_mul_f32_e32 v98, v81, v91
	v_mul_f32_e32 v100, v81, v90
	s_waitcnt vmcnt(0)
	v_pk_mul_f32 v[104:105], v[76:77], v[92:93] op_sel:[1,1] op_sel_hi:[1,0]
	v_mul_f32_e32 v106, v87, v95
	v_mul_f32_e32 v108, v87, v94
	v_pk_mul_f32 v[74:75], v[78:79], v[88:89]
	v_pk_mul_f32 v[102:103], v[76:77], v[92:93]
	v_pk_fma_f32 v[78:79], v[78:79], v[88:89], v[96:97] op_sel_hi:[0,1,1]
	v_pk_fma_f32 v[88:89], v[80:81], v[90:91], v[98:99] op_sel_hi:[1,1,0] neg_lo:[0,0,1] neg_hi:[0,0,1]
	v_pk_fma_f32 v[90:91], v[80:81], v[90:91], v[100:101] op_sel:[0,1,0] op_sel_hi:[1,0,0]
	v_pk_fma_f32 v[76:77], v[76:77], v[92:93], v[104:105] op_sel_hi:[0,1,1]
	v_pk_fma_f32 v[92:93], v[86:87], v[94:95], v[106:107] op_sel_hi:[1,1,0] neg_lo:[0,0,1] neg_hi:[0,0,1]
	v_pk_fma_f32 v[94:95], v[86:87], v[94:95], v[108:109] op_sel:[0,1,0] op_sel_hi:[1,0,0]
	v_sub_f32_e32 v78, v74, v96
	v_sub_f32_e32 v76, v102, v104
	v_mov_b32_e32 v80, v88
	v_mov_b32_e32 v81, v90
	v_mov_b32_e32 v86, v92
	v_mov_b32_e32 v87, v94

; __device__ __forceinline__ u32x4 pack8(f32x4 a, f32x4 b) { u32x4 w; w.x = cvtpk(a[0], a[1]); w.y = cvtpk(a[2], a[3]); w.z = cvtpk(b[0], b[1]); w.w = cvtpk(b[2], b[3]); return w; }
; __device__ __forceinline__ float latent_rstd(const float* ssp, int row, int which) {
;     const f32x4 a = *(const f32x4*)(ssp + ((size_t)row * 2 + which) * 8), b = *(const f32x4*)(ssp + ((size_t)row * 2 + which) * 8 + 4);
;     return 1.0f / sqrtf((((a[0] + a[1]) + (a[2] + a[3])) + ((b[0] + b[1]) + (b[2] + b[3]))) * (1.0f / 512.0f) + 1e-6f);
; }
;     __device__ __forceinline__ void operator()(const Acc& acc, const Unit& u, int wr, int wc, int fr, int fq) const {
;     ...
;             for (int m = 0; m < 4; ++m) { const int row = row0 + ai * HALF + m * 16, pos = row & (SEQ - 1); const float rs = latent_rstd(ssp, row, 0); bf16_t* rowp = O + (size_t)row * ldc + col0;
; #pragma unroll
;                 for (int bj = 0; bj < 2; ++bj) { f32x4 v0 = acc[ai][bj][m][0] * rs, v1 = acc[ai][bj][m][1] * rs; const int d = (col0 + bj * HALF) % 192;
;                     if (d >= 128) { const int jj = (d - 128) >> 1; const f32x4 c01 = rope[pos * 16 + (jj >> 1)], c23 = rope[pos * 16 + (jj >> 1) + 1];
;                         f32x4 w0, w1;
;                         w0[0] = v0[0] * c01[0] - v0[1] * c01[1]; w0[1] = v0[0] * c01[1] + v0[1] * c01[0];
;                         w0[2] = v0[2] * c01[2] - v0[3] * c01[3]; w0[3] = v0[2] * c01[3] + v0[3] * c01[2];
;                         w1[0] = v1[0] * c23[0] - v1[1] * c23[1]; w1[1] = v1[0] * c23[1] + v1[1] * c23[0];
;                         w1[2] = v1[2] * c23[2] - v1[3] * c23[3]; w1[3] = v1[2] * c23[3] + v1[3] * c23[2];
;                         v0 = w0; v1 = w1; }
;                     *(u32x4*)(rowp + bj * HALF) = pack8(v0, v1); } }
.LBB0_1281:
	s_or_b64 exec, exec, s[8:9]
	v_cvt_pk_bf16_f32 v70, v70, v71
	v_cvt_pk_bf16_f32 v71, v72, v73
	v_cvt_pk_bf16_f32 v72, v66, v67
	v_add_u32_e32 v66, 0x80, v134
	v_ashrrev_i32_e32 v67, 31, v66
	v_cvt_pk_bf16_f32 v73, v68, v69
	v_lshlrev_b64 v[68:69], 6, v[66:67]
	global_store_dwordx4 v[74:75], v[70:73], off offset:256
	s_nop 1
	v_lshl_add_u64 v[72:73], s[10:11], 0, v[68:69]
	s_nop 0
	s_waitcnt vmcnt(14)
	v_mov_b32_e32 v68, v216
	v_mov_b32_e32 v69, v217
	v_mov_b32_e32 v70, v218
	v_mov_b32_e32 v71, v219
	v_mov_b32_e32 v76, v68
	v_mov_b32_e32 v72, v220
	v_mov_b32_e32 v73, v221
	v_mov_b32_e32 v74, v222
	v_mov_b32_e32 v75, v223
	v_mov_b32_e32 v77, v72
	v_mov_b32_e32 v72, v69
	v_mov_b32_e32 v68, v70
	v_mov_b32_e32 v69, v74
	v_mov_b32_e32 v74, v71
	v_pk_add_f32 v[70:71], v[76:77], v[72:73]
	v_pk_add_f32 v[68:69], v[68:69], v[74:75]
	s_nop 0
	v_pk_add_f32 v[68:69], v[70:71], v[68:69]
	s_nop 0
	v_add_f32_e32 v67, v68, v69
	v_fmamk_f32 v67, v67, 0x3b000000, v155
	v_mul_f32_e32 v68, 0x4f800000, v67
	v_cmp_gt_f32_e32 vcc, s89, v67
	v_lshlrev_b32_e32 v69, 4, v66
	s_nop 0
	v_cndmask_b32_e32 v67, v67, v68, vcc
	v_sqrt_f32_e32 v68, v67
	s_nop 0
	v_add_u32_e32 v70, -1, v68
	v_add_u32_e32 v71, 1, v68
	v_fma_f32 v72, -v70, v68, v67
	v_fma_f32 v73, -v71, v68, v67
	v_cmp_ge_f32_e64 s[8:9], 0, v72
	s_nop 1
	v_cndmask_b32_e64 v68, v68, v70, s[8:9]
	v_cmp_lt_f32_e64 s[8:9], 0, v73
	s_nop 1
	v_cndmask_b32_e64 v68, v68, v71, s[8:9]
	v_mul_f32_e32 v70, 0x37800000, v68
	v_cndmask_b32_e32 v68, v68, v70, vcc
	v_cmp_class_f32_e32 vcc, v67, v156
	s_nop 1
	v_cndmask_b32_e32 v68, v68, v67, vcc
	v_div_scale_f32 v70, s[8:9], v68, v68, 1.0
	v_rcp_f32_e32 v71, v70
	v_and_b32_e32 v67, 0xfff0, v69
	v_div_scale_f32 v69, vcc, 1.0, v68, 1.0
	v_fma_f32 v72, -v70, v71, 1.0
	v_fmac_f32_e32 v71, v72, v71
	v_mul_f32_e32 v72, v69, v71
	v_fma_f32 v73, -v70, v72, v69
	v_fmac_f32_e32 v72, v73, v71
	v_fma_f32 v69, -v70, v72, v69
	v_div_fmas_f32 v69, v69, v71, v72
	v_div_fixup_f32 v68, v69, v68, 1.0
	v_pk_mul_f32 v[64:65], v[64:65], v[68:69] op_sel_hi:[1,0]
	v_pk_mul_f32 v[62:63], v[62:63], v[68:69] op_sel_hi:[1,0]
	v_pk_mul_f32 v[70:71], v[60:61], v[68:69] op_sel_hi:[1,0]
	v_pk_mul_f32 v[60:61], v[58:59], v[68:69] op_sel_hi:[1,0]
	s_and_saveexec_b64 s[8:9], s[4:5]
	s_cbranch_execz .LBB0_1283
	v_add_u32_e32 v130, v135, v67
	v_lshl_add_u64 v[58:59], v[130:131], 4, s[38:39]
	global_load_dwordx4 v[72:75], v[58:59], off
	global_load_dwordx4 v[76:79], v[58:59], off offset:16
	s_waitcnt vmcnt(1)
	v_pk_mul_f32 v[80:81], v[62:63], v[72:73] op_sel:[1,1] op_sel_hi:[1,0]
	v_mul_f32_e32 v82, v65, v75
	v_mul_f32_e32 v84, v65, v74
	s_waitcnt vmcnt(0)
	v_pk_mul_f32 v[88:89], v[60:61], v[76:77] op_sel:[1,1] op_sel_hi:[1,0]
	v_mul_f32_e32 v90, v71, v79
	v_mul_f32_e32 v92, v71, v78
	v_pk_mul_f32 v[58:59], v[62:63], v[72:73]
	v_pk_mul_f32 v[86:87], v[60:61], v[76:77]
	v_pk_fma_f32 v[62:63], v[62:63], v[72:73], v[80:81] op_sel_hi:[0,1,1]
	v_pk_fma_f32 v[72:73], v[64:65], v[74:75], v[82:83] op_sel_hi:[1,1,0] neg_lo:[0,0,1] neg_hi:[0,0,1]
	v_pk_fma_f32 v[74:75], v[64:65], v[74:75], v[84:85] op_sel:[0,1,0] op_sel_hi:[1,0,0]
	v_pk_fma_f32 v[60:61], v[60:61], v[76:77], v[88:89] op_sel_hi:[0,1,1]
	v_pk_fma_f32 v[76:77], v[70:71], v[78:79], v[90:91] op_sel_hi:[1,1,0] neg_lo:[0,0,1] neg_hi:[0,0,1]
	v_pk_fma_f32 v[78:79], v[70:71], v[78:79], v[92:93] op_sel:[0,1,0] op_sel_hi:[1,0,0]
	v_sub_f32_e32 v62, v58, v80
	v_sub_f32_e32 v60, v86, v88
	v_mov_b32_e32 v64, v72
	v_mov_b32_e32 v65, v74
	v_mov_b32_e32 v70, v76
	v_mov_b32_e32 v71, v78

; __device__ __forceinline__ u32x4 pack8(f32x4 a, f32x4 b) { u32x4 w; w.x = cvtpk(a[0], a[1]); w.y = cvtpk(a[2], a[3]); w.z = cvtpk(b[0], b[1]); w.w = cvtpk(b[2], b[3]); return w; }
; __device__ __forceinline__ float latent_rstd(const float* ssp, int row, int which) {
;     const f32x4 a = *(const f32x4*)(ssp + ((size_t)row * 2 + which) * 8), b = *(const f32x4*)(ssp + ((size_t)row * 2 + which) * 8 + 4);
;     return 1.0f / sqrtf((((a[0] + a[1]) + (a[2] + a[3])) + ((b[0] + b[1]) + (b[2] + b[3]))) * (1.0f / 512.0f) + 1e-6f);
; }
;     __device__ __forceinline__ void operator()(const Acc& acc, const Unit& u, int wr, int wc, int fr, int fq) const {
;     ...
;             for (int m = 0; m < 4; ++m) { const int row = row0 + ai * HALF + m * 16, pos = row & (SEQ - 1); const float rs = latent_rstd(ssp, row, 0); bf16_t* rowp = O + (size_t)row * ldc + col0;
; #pragma unroll
;                 for (int bj = 0; bj < 2; ++bj) { f32x4 v0 = acc[ai][bj][m][0] * rs, v1 = acc[ai][bj][m][1] * rs; const int d = (col0 + bj * HALF) % 192;
;                     if (d >= 128) { const int jj = (d - 128) >> 1; const f32x4 c01 = rope[pos * 16 + (jj >> 1)], c23 = rope[pos * 16 + (jj >> 1) + 1];
;                         f32x4 w0, w1;
;                         w0[0] = v0[0] * c01[0] - v0[1] * c01[1]; w0[1] = v0[0] * c01[1] + v0[1] * c01[0];
;                         w0[2] = v0[2] * c01[2] - v0[3] * c01[3]; w0[3] = v0[2] * c01[3] + v0[3] * c01[2];
;                         w1[0] = v1[0] * c23[0] - v1[1] * c23[1]; w1[1] = v1[0] * c23[1] + v1[1] * c23[0];
;                         w1[2] = v1[2] * c23[2] - v1[3] * c23[3]; w1[3] = v1[2] * c23[3] + v1[3] * c23[2];
;                         v0 = w0; v1 = w1; }
;                     *(u32x4*)(rowp + bj * HALF) = pack8(v0, v1); } }
.LBB0_1285:
	s_or_b64 exec, exec, s[8:9]
	v_cvt_pk_bf16_f32 v54, v54, v55
	v_cvt_pk_bf16_f32 v55, v56, v57
	v_cvt_pk_bf16_f32 v56, v50, v51
	v_add_u32_e32 v50, 0x90, v134
	v_ashrrev_i32_e32 v51, 31, v50
	v_cvt_pk_bf16_f32 v57, v52, v53
	v_lshlrev_b64 v[52:53], 6, v[50:51]
	global_store_dwordx4 v[58:59], v[54:57], off offset:256
	s_nop 1
	v_lshl_add_u64 v[56:57], s[10:11], 0, v[52:53]
	s_nop 0
	s_waitcnt vmcnt(14)
	v_mov_b32_e32 v52, v224
	v_mov_b32_e32 v53, v225
	v_mov_b32_e32 v54, v226
	v_mov_b32_e32 v55, v227
	v_mov_b32_e32 v60, v52
	v_mov_b32_e32 v56, v228
	v_mov_b32_e32 v57, v229
	v_mov_b32_e32 v58, v230
	v_mov_b32_e32 v59, v231
	v_mov_b32_e32 v61, v56
	v_mov_b32_e32 v56, v53
	v_mov_b32_e32 v52, v54
	v_mov_b32_e32 v53, v58
	v_mov_b32_e32 v58, v55
	v_pk_add_f32 v[54:55], v[60:61], v[56:57]
	v_pk_add_f32 v[52:53], v[52:53], v[58:59]
	s_nop 0
	v_pk_add_f32 v[52:53], v[54:55], v[52:53]
	s_nop 0
	v_add_f32_e32 v51, v52, v53
	v_fmamk_f32 v51, v51, 0x3b000000, v155
	v_mul_f32_e32 v52, 0x4f800000, v51
	v_cmp_gt_f32_e32 vcc, s89, v51
	v_lshlrev_b32_e32 v53, 4, v50
	s_nop 0
	v_cndmask_b32_e32 v51, v51, v52, vcc
	v_sqrt_f32_e32 v52, v51
	s_nop 0
	v_add_u32_e32 v54, -1, v52
	v_add_u32_e32 v55, 1, v52
	v_fma_f32 v56, -v54, v52, v51
	v_fma_f32 v57, -v55, v52, v51
	v_cmp_ge_f32_e64 s[8:9], 0, v56
	s_nop 1
	v_cndmask_b32_e64 v52, v52, v54, s[8:9]
	v_cmp_lt_f32_e64 s[8:9], 0, v57
	s_nop 1
	v_cndmask_b32_e64 v52, v52, v55, s[8:9]
	v_mul_f32_e32 v54, 0x37800000, v52
	v_cndmask_b32_e32 v52, v52, v54, vcc
	v_cmp_class_f32_e32 vcc, v51, v156
	s_nop 1
	v_cndmask_b32_e32 v52, v52, v51, vcc
	v_div_scale_f32 v54, s[8:9], v52, v52, 1.0
	v_rcp_f32_e32 v55, v54
	v_and_b32_e32 v51, 0xfff0, v53
	v_div_scale_f32 v53, vcc, 1.0, v52, 1.0
	v_fma_f32 v56, -v54, v55, 1.0
	v_fmac_f32_e32 v55, v56, v55
	v_mul_f32_e32 v56, v53, v55
	v_fma_f32 v57, -v54, v56, v53
	v_fmac_f32_e32 v56, v57, v55
	v_fma_f32 v53, -v54, v56, v53
	v_div_fmas_f32 v53, v53, v55, v56
	v_div_fixup_f32 v52, v53, v52, 1.0
	v_pk_mul_f32 v[48:49], v[48:49], v[52:53] op_sel_hi:[1,0]
	v_pk_mul_f32 v[46:47], v[46:47], v[52:53] op_sel_hi:[1,0]
	v_pk_mul_f32 v[54:55], v[44:45], v[52:53] op_sel_hi:[1,0]
	v_pk_mul_f32 v[44:45], v[42:43], v[52:53] op_sel_hi:[1,0]
	s_and_saveexec_b64 s[8:9], s[4:5]
	s_cbranch_execz .LBB0_1287
	v_add_u32_e32 v130, v135, v51
	v_lshl_add_u64 v[42:43], v[130:131], 4, s[38:39]
	global_load_dwordx4 v[56:59], v[42:43], off
	global_load_dwordx4 v[60:63], v[42:43], off offset:16
	s_waitcnt vmcnt(1)
	v_pk_mul_f32 v[64:65], v[46:47], v[56:57] op_sel:[1,1] op_sel_hi:[1,0]
	v_mul_f32_e32 v66, v49, v59
	v_mul_f32_e32 v68, v49, v58
	s_waitcnt vmcnt(0)
	v_pk_mul_f32 v[72:73], v[44:45], v[60:61] op_sel:[1,1] op_sel_hi:[1,0]
	v_mul_f32_e32 v74, v55, v63
	v_mul_f32_e32 v76, v55, v62
	v_pk_mul_f32 v[42:43], v[46:47], v[56:57]
	v_pk_mul_f32 v[70:71], v[44:45], v[60:61]
	v_pk_fma_f32 v[46:47], v[46:47], v[56:57], v[64:65] op_sel_hi:[0,1,1]
	v_pk_fma_f32 v[56:57], v[48:49], v[58:59], v[66:67] op_sel_hi:[1,1,0] neg_lo:[0,0,1] neg_hi:[0,0,1]
	v_pk_fma_f32 v[58:59], v[48:49], v[58:59], v[68:69] op_sel:[0,1,0] op_sel_hi:[1,0,0]
	v_pk_fma_f32 v[44:45], v[44:45], v[60:61], v[72:73] op_sel_hi:[0,1,1]
	v_pk_fma_f32 v[60:61], v[54:55], v[62:63], v[74:75] op_sel_hi:[1,1,0] neg_lo:[0,0,1] neg_hi:[0,0,1]
	v_pk_fma_f32 v[62:63], v[54:55], v[62:63], v[76:77] op_sel:[0,1,0] op_sel_hi:[1,0,0]
	v_sub_f32_e32 v46, v42, v64
	v_sub_f32_e32 v44, v70, v72
	v_mov_b32_e32 v48, v56
	v_mov_b32_e32 v49, v58
	v_mov_b32_e32 v54, v60
	v_mov_b32_e32 v55, v62

; __device__ __forceinline__ u32x4 pack8(f32x4 a, f32x4 b) { u32x4 w; w.x = cvtpk(a[0], a[1]); w.y = cvtpk(a[2], a[3]); w.z = cvtpk(b[0], b[1]); w.w = cvtpk(b[2], b[3]); return w; }
; __device__ __forceinline__ float latent_rstd(const float* ssp, int row, int which) {
;     const f32x4 a = *(const f32x4*)(ssp + ((size_t)row * 2 + which) * 8), b = *(const f32x4*)(ssp + ((size_t)row * 2 + which) * 8 + 4);
;     return 1.0f / sqrtf((((a[0] + a[1]) + (a[2] + a[3])) + ((b[0] + b[1]) + (b[2] + b[3]))) * (1.0f / 512.0f) + 1e-6f);
; }
;     __device__ __forceinline__ void operator()(const Acc& acc, const Unit& u, int wr, int wc, int fr, int fq) const {
;     ...
;             for (int m = 0; m < 4; ++m) { const int row = row0 + ai * HALF + m * 16, pos = row & (SEQ - 1); const float rs = latent_rstd(ssp, row, 0); bf16_t* rowp = O + (size_t)row * ldc + col0;
; #pragma unroll
;                 for (int bj = 0; bj < 2; ++bj) { f32x4 v0 = acc[ai][bj][m][0] * rs, v1 = acc[ai][bj][m][1] * rs; const int d = (col0 + bj * HALF) % 192;
;                     if (d >= 128) { const int jj = (d - 128) >> 1; const f32x4 c01 = rope[pos * 16 + (jj >> 1)], c23 = rope[pos * 16 + (jj >> 1) + 1];
;                         f32x4 w0, w1;
;                         w0[0] = v0[0] * c01[0] - v0[1] * c01[1]; w0[1] = v0[0] * c01[1] + v0[1] * c01[0];
;                         w0[2] = v0[2] * c01[2] - v0[3] * c01[3]; w0[3] = v0[2] * c01[3] + v0[3] * c01[2];
;                         w1[0] = v1[0] * c23[0] - v1[1] * c23[1]; w1[1] = v1[0] * c23[1] + v1[1] * c23[0];
;                         w1[2] = v1[2] * c23[2] - v1[3] * c23[3]; w1[3] = v1[2] * c23[3] + v1[3] * c23[2];
;                         v0 = w0; v1 = w1; }
;                     *(u32x4*)(rowp + bj * HALF) = pack8(v0, v1); } }
.LBB0_1289:
	s_or_b64 exec, exec, s[8:9]
	v_cvt_pk_bf16_f32 v38, v38, v39
	v_cvt_pk_bf16_f32 v39, v40, v41
	v_cvt_pk_bf16_f32 v40, v34, v35
	v_add_u32_e32 v34, 0xa0, v134
	v_ashrrev_i32_e32 v35, 31, v34
	v_cvt_pk_bf16_f32 v41, v36, v37
	v_lshlrev_b64 v[36:37], 6, v[34:35]
	global_store_dwordx4 v[42:43], v[38:41], off offset:256
	s_nop 1
	v_lshl_add_u64 v[40:41], s[10:11], 0, v[36:37]
	s_nop 0
	s_waitcnt vmcnt(14)
	v_mov_b32_e32 v36, v232
	v_mov_b32_e32 v37, v233
	v_mov_b32_e32 v38, v234
	v_mov_b32_e32 v39, v235
	v_mov_b32_e32 v44, v36
	v_mov_b32_e32 v40, v236
	v_mov_b32_e32 v41, v237
	v_mov_b32_e32 v42, v238
	v_mov_b32_e32 v43, v239
	v_mov_b32_e32 v45, v40
	v_mov_b32_e32 v40, v37
	v_mov_b32_e32 v36, v38
	v_mov_b32_e32 v37, v42
	v_mov_b32_e32 v42, v39
	v_pk_add_f32 v[38:39], v[44:45], v[40:41]
	v_pk_add_f32 v[36:37], v[36:37], v[42:43]
	s_nop 0
	v_pk_add_f32 v[36:37], v[38:39], v[36:37]
	s_nop 0
	v_add_f32_e32 v35, v36, v37
	v_fmamk_f32 v35, v35, 0x3b000000, v155
	v_mul_f32_e32 v36, 0x4f800000, v35
	v_cmp_gt_f32_e32 vcc, s89, v35
	v_lshlrev_b32_e32 v37, 4, v34
	s_nop 0
	v_cndmask_b32_e32 v35, v35, v36, vcc
	v_sqrt_f32_e32 v36, v35
	s_nop 0
	v_add_u32_e32 v38, -1, v36
	v_add_u32_e32 v39, 1, v36
	v_fma_f32 v40, -v38, v36, v35
	v_fma_f32 v41, -v39, v36, v35
	v_cmp_ge_f32_e64 s[8:9], 0, v40
	s_nop 1
	v_cndmask_b32_e64 v36, v36, v38, s[8:9]
	v_cmp_lt_f32_e64 s[8:9], 0, v41
	s_nop 1
	v_cndmask_b32_e64 v36, v36, v39, s[8:9]
	v_mul_f32_e32 v38, 0x37800000, v36
	v_cndmask_b32_e32 v36, v36, v38, vcc
	v_cmp_class_f32_e32 vcc, v35, v156
	s_nop 1
	v_cndmask_b32_e32 v36, v36, v35, vcc
	v_div_scale_f32 v38, s[8:9], v36, v36, 1.0
	v_rcp_f32_e32 v39, v38
	v_and_b32_e32 v35, 0xfff0, v37
	v_div_scale_f32 v37, vcc, 1.0, v36, 1.0
	v_fma_f32 v40, -v38, v39, 1.0
	v_fmac_f32_e32 v39, v40, v39
	v_mul_f32_e32 v40, v37, v39
	v_fma_f32 v41, -v38, v40, v37
	v_fmac_f32_e32 v40, v41, v39
	v_fma_f32 v37, -v38, v40, v37
	v_div_fmas_f32 v37, v37, v39, v40
	v_div_fixup_f32 v36, v37, v36, 1.0
	v_pk_mul_f32 v[32:33], v[32:33], v[36:37] op_sel_hi:[1,0]
	v_pk_mul_f32 v[30:31], v[30:31], v[36:37] op_sel_hi:[1,0]
	v_pk_mul_f32 v[38:39], v[28:29], v[36:37] op_sel_hi:[1,0]
	v_pk_mul_f32 v[28:29], v[26:27], v[36:37] op_sel_hi:[1,0]
	s_and_saveexec_b64 s[8:9], s[4:5]
	s_cbranch_execz .LBB0_1291
	v_add_u32_e32 v130, v135, v35
	v_lshl_add_u64 v[26:27], v[130:131], 4, s[38:39]
	global_load_dwordx4 v[40:43], v[26:27], off
	global_load_dwordx4 v[44:47], v[26:27], off offset:16
	s_waitcnt vmcnt(1)
	v_pk_mul_f32 v[48:49], v[30:31], v[40:41] op_sel:[1,1] op_sel_hi:[1,0]
	v_mul_f32_e32 v50, v33, v43
	v_mul_f32_e32 v52, v33, v42
	s_waitcnt vmcnt(0)
	v_pk_mul_f32 v[56:57], v[28:29], v[44:45] op_sel:[1,1] op_sel_hi:[1,0]
	v_mul_f32_e32 v58, v39, v47
	v_mul_f32_e32 v60, v39, v46
	v_pk_mul_f32 v[26:27], v[30:31], v[40:41]
	v_pk_mul_f32 v[54:55], v[28:29], v[44:45]
	v_pk_fma_f32 v[30:31], v[30:31], v[40:41], v[48:49] op_sel_hi:[0,1,1]
	v_pk_fma_f32 v[40:41], v[32:33], v[42:43], v[50:51] op_sel_hi:[1,1,0] neg_lo:[0,0,1] neg_hi:[0,0,1]
	v_pk_fma_f32 v[42:43], v[32:33], v[42:43], v[52:53] op_sel:[0,1,0] op_sel_hi:[1,0,0]
	v_pk_fma_f32 v[28:29], v[28:29], v[44:45], v[56:57] op_sel_hi:[0,1,1]
	v_pk_fma_f32 v[44:45], v[38:39], v[46:47], v[58:59] op_sel_hi:[1,1,0] neg_lo:[0,0,1] neg_hi:[0,0,1]
	v_pk_fma_f32 v[46:47], v[38:39], v[46:47], v[60:61] op_sel:[0,1,0] op_sel_hi:[1,0,0]
	v_sub_f32_e32 v30, v26, v48
	v_sub_f32_e32 v28, v54, v56
	v_mov_b32_e32 v32, v40
	v_mov_b32_e32 v33, v42
	v_mov_b32_e32 v38, v44
	v_mov_b32_e32 v39, v46

; __device__ __forceinline__ u32x4 pack8(f32x4 a, f32x4 b) { u32x4 w; w.x = cvtpk(a[0], a[1]); w.y = cvtpk(a[2], a[3]); w.z = cvtpk(b[0], b[1]); w.w = cvtpk(b[2], b[3]); return w; }
; __device__ __forceinline__ float latent_rstd(const float* ssp, int row, int which) {
;     const f32x4 a = *(const f32x4*)(ssp + ((size_t)row * 2 + which) * 8), b = *(const f32x4*)(ssp + ((size_t)row * 2 + which) * 8 + 4);
;     return 1.0f / sqrtf((((a[0] + a[1]) + (a[2] + a[3])) + ((b[0] + b[1]) + (b[2] + b[3]))) * (1.0f / 512.0f) + 1e-6f);
; }
;     __device__ __forceinline__ void operator()(const Acc& acc, const Unit& u, int wr, int wc, int fr, int fq) const {
;     ...
;             for (int m = 0; m < 4; ++m) { const int row = row0 + ai * HALF + m * 16, pos = row & (SEQ - 1); const float rs = latent_rstd(ssp, row, 0); bf16_t* rowp = O + (size_t)row * ldc + col0;
; #pragma unroll
;                 for (int bj = 0; bj < 2; ++bj) { f32x4 v0 = acc[ai][bj][m][0] * rs, v1 = acc[ai][bj][m][1] * rs; const int d = (col0 + bj * HALF) % 192;
;                     if (d >= 128) { const int jj = (d - 128) >> 1; const f32x4 c01 = rope[pos * 16 + (jj >> 1)], c23 = rope[pos * 16 + (jj >> 1) + 1];
;                         f32x4 w0, w1;
;                         w0[0] = v0[0] * c01[0] - v0[1] * c01[1]; w0[1] = v0[0] * c01[1] + v0[1] * c01[0];
;                         w0[2] = v0[2] * c01[2] - v0[3] * c01[3]; w0[3] = v0[2] * c01[3] + v0[3] * c01[2];
;                         w1[0] = v1[0] * c23[0] - v1[1] * c23[1]; w1[1] = v1[0] * c23[1] + v1[1] * c23[0];
;                         w1[2] = v1[2] * c23[2] - v1[3] * c23[3]; w1[3] = v1[2] * c23[3] + v1[3] * c23[2];
;                         v0 = w0; v1 = w1; }
;                     *(u32x4*)(rowp + bj * HALF) = pack8(v0, v1); } }
.LBB0_1293:
	s_or_b64 exec, exec, s[8:9]
	v_cvt_pk_bf16_f32 v22, v22, v23
	v_cvt_pk_bf16_f32 v23, v24, v25
	v_cvt_pk_bf16_f32 v24, v18, v19
	v_add_u32_e32 v18, 0xb0, v134
	v_ashrrev_i32_e32 v19, 31, v18
	v_cvt_pk_bf16_f32 v25, v20, v21
	v_lshlrev_b64 v[20:21], 6, v[18:19]
	global_store_dwordx4 v[26:27], v[22:25], off offset:256
	s_nop 1
	v_lshl_add_u64 v[24:25], s[10:11], 0, v[20:21]
	s_nop 0
	s_waitcnt vmcnt(14)
	v_mov_b32_e32 v20, v240
	v_mov_b32_e32 v21, v241
	v_mov_b32_e32 v22, v242
	v_mov_b32_e32 v23, v243
	v_mov_b32_e32 v28, v20
	v_mov_b32_e32 v24, v244
	v_mov_b32_e32 v25, v245
	v_mov_b32_e32 v26, v246
	v_mov_b32_e32 v27, v247
	v_mov_b32_e32 v29, v24
	v_mov_b32_e32 v24, v21
	v_mov_b32_e32 v20, v22
	v_mov_b32_e32 v21, v26
	v_mov_b32_e32 v26, v23
	v_pk_add_f32 v[22:23], v[28:29], v[24:25]
	v_pk_add_f32 v[20:21], v[20:21], v[26:27]
	s_nop 0
	v_pk_add_f32 v[20:21], v[22:23], v[20:21]
	s_nop 0
	v_add_f32_e32 v19, v20, v21
	v_fmamk_f32 v19, v19, 0x3b000000, v155
	v_mul_f32_e32 v20, 0x4f800000, v19
	v_cmp_gt_f32_e32 vcc, s89, v19
	v_lshlrev_b32_e32 v21, 4, v18
	s_nop 0
	v_cndmask_b32_e32 v19, v19, v20, vcc
	v_sqrt_f32_e32 v20, v19
	s_nop 0
	v_add_u32_e32 v22, -1, v20
	v_add_u32_e32 v23, 1, v20
	v_fma_f32 v24, -v22, v20, v19
	v_fma_f32 v25, -v23, v20, v19
	v_cmp_ge_f32_e64 s[8:9], 0, v24
	s_nop 1
	v_cndmask_b32_e64 v20, v20, v22, s[8:9]
	v_cmp_lt_f32_e64 s[8:9], 0, v25
	s_nop 1
	v_cndmask_b32_e64 v20, v20, v23, s[8:9]
	v_mul_f32_e32 v22, 0x37800000, v20
	v_cndmask_b32_e32 v20, v20, v22, vcc
	v_cmp_class_f32_e32 vcc, v19, v156
	s_nop 1
	v_cndmask_b32_e32 v20, v20, v19, vcc
	v_div_scale_f32 v22, s[8:9], v20, v20, 1.0
	v_rcp_f32_e32 v23, v22
	v_and_b32_e32 v19, 0xfff0, v21
	v_div_scale_f32 v21, vcc, 1.0, v20, 1.0
	v_fma_f32 v24, -v22, v23, 1.0
	v_fmac_f32_e32 v23, v24, v23
	v_mul_f32_e32 v24, v21, v23
	v_fma_f32 v25, -v22, v24, v21
	v_fmac_f32_e32 v24, v25, v23
	v_fma_f32 v21, -v22, v24, v21
	v_div_fmas_f32 v21, v21, v23, v24
	v_div_fixup_f32 v20, v21, v20, 1.0
	v_pk_mul_f32 v[16:17], v[16:17], v[20:21] op_sel_hi:[1,0]
	v_pk_mul_f32 v[14:15], v[14:15], v[20:21] op_sel_hi:[1,0]
	v_pk_mul_f32 v[22:23], v[12:13], v[20:21] op_sel_hi:[1,0]
	v_pk_mul_f32 v[12:13], v[10:11], v[20:21] op_sel_hi:[1,0]
	s_and_saveexec_b64 s[8:9], s[4:5]
	s_cbranch_execz .LBB0_1295
	v_add_u32_e32 v130, v135, v19
	v_lshl_add_u64 v[10:11], v[130:131], 4, s[38:39]
	global_load_dwordx4 v[24:27], v[10:11], off
	global_load_dwordx4 v[28:31], v[10:11], off offset:16
	s_waitcnt vmcnt(1)
	v_pk_mul_f32 v[32:33], v[14:15], v[24:25] op_sel:[1,1] op_sel_hi:[1,0]
	v_mul_f32_e32 v34, v17, v27
	v_mul_f32_e32 v36, v17, v26
	s_waitcnt vmcnt(0)
	v_pk_mul_f32 v[40:41], v[12:13], v[28:29] op_sel:[1,1] op_sel_hi:[1,0]
	v_mul_f32_e32 v42, v23, v31
	v_mul_f32_e32 v44, v23, v30
	v_pk_mul_f32 v[10:11], v[14:15], v[24:25]
	v_pk_mul_f32 v[38:39], v[12:13], v[28:29]
	v_pk_fma_f32 v[14:15], v[14:15], v[24:25], v[32:33] op_sel_hi:[0,1,1]
	v_pk_fma_f32 v[24:25], v[16:17], v[26:27], v[34:35] op_sel_hi:[1,1,0] neg_lo:[0,0,1] neg_hi:[0,0,1]
	v_pk_fma_f32 v[26:27], v[16:17], v[26:27], v[36:37] op_sel:[0,1,0] op_sel_hi:[1,0,0]
	v_pk_fma_f32 v[12:13], v[12:13], v[28:29], v[40:41] op_sel_hi:[0,1,1]
	v_pk_fma_f32 v[28:29], v[22:23], v[30:31], v[42:43] op_sel_hi:[1,1,0] neg_lo:[0,0,1] neg_hi:[0,0,1]
	v_pk_fma_f32 v[30:31], v[22:23], v[30:31], v[44:45] op_sel:[0,1,0] op_sel_hi:[1,0,0]
	v_sub_f32_e32 v14, v10, v32
	v_sub_f32_e32 v12, v38, v40
	v_mov_b32_e32 v16, v24
	v_mov_b32_e32 v17, v26
	v_mov_b32_e32 v22, v28
	v_mov_b32_e32 v23, v30

; __device__ __forceinline__ u32x4 pack8(f32x4 a, f32x4 b) { u32x4 w; w.x = cvtpk(a[0], a[1]); w.y = cvtpk(a[2], a[3]); w.z = cvtpk(b[0], b[1]); w.w = cvtpk(b[2], b[3]); return w; }
; __device__ __forceinline__ float latent_rstd(const float* ssp, int row, int which) {
;     const f32x4 a = *(const f32x4*)(ssp + ((size_t)row * 2 + which) * 8), b = *(const f32x4*)(ssp + ((size_t)row * 2 + which) * 8 + 4);
;     return 1.0f / sqrtf((((a[0] + a[1]) + (a[2] + a[3])) + ((b[0] + b[1]) + (b[2] + b[3]))) * (1.0f / 512.0f) + 1e-6f);
; }
;     __device__ __forceinline__ void operator()(const Acc& acc, const Unit& u, int wr, int wc, int fr, int fq) const {
;         const int row0 = u.row0 + wr * 64 + fr, col0 = u.col0 + wc * 32 + 8 * fq;
; #pragma unroll
;         for (int ai = 0; ai < 2; ++ai)
; #pragma unroll
;             for (int m = 0; m < 4; ++m) { const int row = row0 + ai * HALF + m * 16; const float rs = latent_rstd(ssp, row, 1); bf16_t* rowp = O + (size_t)row * ldc + col0;
; #pragma unroll
;                 for (int bj = 0; bj < 2; ++bj) *(u32x4*)(rowp + bj * HALF) = pack8(acc[ai][bj][m][0] * rs, acc[ai][bj][m][1] * rs); }
;     }
.LBB0_1321:
	v_mbcnt_lo_u32_b32 v147, -1, 0
	v_mbcnt_hi_u32_b32 v147, -1, v147
	s_add_i32 s4, s79, s62
	v_and_b32_e32 v130, 15, v147
	v_add_u32_e32 v132, s4, v130
	v_ashrrev_i32_e32 v133, 31, v132
	v_lshlrev_b64 v[130:131], 6, v[132:133]
	v_lshl_add_u64 v[130:131], s[10:11], 0, v[130:131]
	v_lshlrev_b32_e32 v250, 6, v132
	global_load_dwordx4 v[182:185], v250, s[10:11] offset:32
	global_load_dwordx4 v[186:189], v250, s[10:11] offset:48
	v_add_u32_e32 v250, 16, v132
	v_lshlrev_b32_e32 v250, 6, v250
	global_load_dwordx4 v[190:193], v250, s[10:11] offset:32
	global_load_dwordx4 v[194:197], v250, s[10:11] offset:48
	v_add_u32_e32 v250, 32, v132
	v_lshlrev_b32_e32 v250, 6, v250
	global_load_dwordx4 v[200:203], v250, s[10:11] offset:32
	global_load_dwordx4 v[204:207], v250, s[10:11] offset:48
	v_add_u32_e32 v250, 48, v132
	v_lshlrev_b32_e32 v250, 6, v250
	global_load_dwordx4 v[208:211], v250, s[10:11] offset:32
	global_load_dwordx4 v[212:215], v250, s[10:11] offset:48
	v_add_u32_e32 v250, 128, v132
	v_lshlrev_b32_e32 v250, 6, v250
	global_load_dwordx4 v[216:219], v250, s[10:11] offset:32
	global_load_dwordx4 v[220:223], v250, s[10:11] offset:48
	v_add_u32_e32 v250, 144, v132
	v_lshlrev_b32_e32 v250, 6, v250
	global_load_dwordx4 v[224:227], v250, s[10:11] offset:32
	global_load_dwordx4 v[228:231], v250, s[10:11] offset:48
	v_add_u32_e32 v250, 160, v132
	v_lshlrev_b32_e32 v250, 6, v250
	global_load_dwordx4 v[232:235], v250, s[10:11] offset:32
	global_load_dwordx4 v[236:239], v250, s[10:11] offset:48
	v_add_u32_e32 v250, 176, v132
	v_lshlrev_b32_e32 v250, 6, v250
	global_load_dwordx4 v[240:243], v250, s[10:11] offset:32
	global_load_dwordx4 v[244:247], v250, s[10:11] offset:48
	v_lshlrev_b64 v[158:159], 12, v[132:133]
	v_ashrrev_i32_e32 v130, 1, v147
	s_add_i32 s4, s88, s63
	v_and_b32_e32 v130, -8, v130
	v_add_u32_e32 v130, s4, v130
	v_add_u32_e32 v156, 16, v132
	v_ashrrev_i32_e32 v131, 31, v130
	v_ashrrev_i32_e32 v157, 31, v156
	v_lshl_add_u64 v[158:159], s[12:13], 0, v[158:159]
	v_lshlrev_b64 v[130:131], 1, v[130:131]
	s_waitcnt vmcnt(14)
	v_mov_b32_e32 v148, v182
	v_mov_b32_e32 v149, v183
	v_mov_b32_e32 v150, v184
	v_mov_b32_e32 v151, v185
	v_mov_b32_e32 v160, v148
	v_mov_b32_e32 v152, v186
	v_mov_b32_e32 v153, v187
	v_mov_b32_e32 v154, v188
	v_mov_b32_e32 v155, v189
	v_mov_b32_e32 v161, v152
	v_mov_b32_e32 v152, v149
	v_mov_b32_e32 v148, v150
	v_mov_b32_e32 v149, v154
	v_mov_b32_e32 v154, v151
	v_pk_add_f32 v[150:151], v[160:161], v[152:153]
	v_pk_add_f32 v[148:149], v[148:149], v[154:155]
	s_nop 0
	v_pk_add_f32 v[148:149], v[150:151], v[148:149]
	v_lshl_add_u64 v[150:151], v[158:159], 0, v[130:131]
	v_add_f32_e32 v133, v148, v149
	v_fmamk_f32 v133, v133, 0x3b000000, v139
	v_mul_f32_e32 v147, 0x4f800000, v133
	v_cmp_gt_f32_e32 vcc, s72, v133
	v_lshlrev_b64 v[148:149], 6, v[156:157]
	v_lshl_add_u64 v[148:149], s[10:11], 0, v[148:149]
	v_cndmask_b32_e32 v133, v133, v147, vcc
	v_sqrt_f32_e32 v147, v133
	s_nop 0
	v_add_u32_e32 v152, -1, v147
	v_add_u32_e32 v153, 1, v147
	v_fma_f32 v154, -v152, v147, v133
	v_fma_f32 v155, -v153, v147, v133
	v_cmp_ge_f32_e64 s[4:5], 0, v154
	s_nop 1
	v_cndmask_b32_e64 v147, v147, v152, s[4:5]
	v_cmp_lt_f32_e64 s[4:5], 0, v155
	s_nop 1
	v_cndmask_b32_e64 v147, v147, v153, s[4:5]
	v_mul_f32_e32 v152, 0x37800000, v147
	v_cndmask_b32_e32 v147, v147, v152, vcc
	v_cmp_class_f32_e32 vcc, v133, v146
	s_nop 1
	v_cndmask_b32_e32 v133, v147, v133, vcc
	v_div_scale_f32 v147, s[4:5], v133, v133, 1.0
	v_rcp_f32_e32 v152, v147
	v_div_scale_f32 v153, vcc, 1.0, v133, 1.0
	v_fma_f32 v154, -v147, v152, 1.0
	v_fmac_f32_e32 v152, v154, v152
	v_mul_f32_e32 v154, v153, v152
	v_fma_f32 v155, -v147, v154, v153
	v_fmac_f32_e32 v154, v155, v152
	v_fma_f32 v147, -v147, v154, v153
	v_div_fmas_f32 v147, v147, v152, v154
	v_div_fixup_f32 v152, v147, v133, 1.0
	v_pk_mul_f32 v[128:129], v[128:129], v[152:153] op_sel_hi:[1,0]
	v_pk_mul_f32 v[126:127], v[126:127], v[152:153] op_sel_hi:[1,0]
	v_pk_mul_f32 v[124:125], v[124:125], v[152:153] op_sel_hi:[1,0]
	v_pk_mul_f32 v[122:123], v[122:123], v[152:153] op_sel_hi:[1,0]
	v_pk_mul_f32 v[120:121], v[120:121], v[152:153] op_sel_hi:[1,0]
	v_pk_mul_f32 v[118:119], v[118:119], v[152:153] op_sel_hi:[1,0]
	v_pk_mul_f32 v[154:155], v[116:117], v[152:153] op_sel_hi:[1,0]
	v_pk_mul_f32 v[152:153], v[114:115], v[152:153] op_sel_hi:[1,0]
	v_cvt_pk_bf16_f32 v114, v126, v127
	v_cvt_pk_bf16_f32 v115, v128, v129
	v_cvt_pk_bf16_f32 v116, v122, v123
	v_cvt_pk_bf16_f32 v117, v124, v125
	global_store_dwordx4 v[150:151], v[114:117], off
	v_lshlrev_b64 v[124:125], 12, v[156:157]
	v_add_u32_e32 v122, 32, v132
	v_cvt_pk_bf16_f32 v114, v118, v119
	v_cvt_pk_bf16_f32 v115, v120, v121
	v_cvt_pk_bf16_f32 v116, v152, v153
	v_cvt_pk_bf16_f32 v117, v154, v155
	global_store_dwordx4 v[150:151], v[114:117], off offset:256
	s_nop 0
	v_ashrrev_i32_e32 v123, 31, v122
	s_waitcnt vmcnt(14)
; __device__ __forceinline__ u32x4 pack8(f32x4 a, f32x4 b) { u32x4 w; w.x = cvtpk(a[0], a[1]); w.y = cvtpk(a[2], a[3]); w.z = cvtpk(b[0], b[1]); w.w = cvtpk(b[2], b[3]); return w; }
; __device__ __forceinline__ float latent_rstd(const float* ssp, int row, int which) {
;     const f32x4 a = *(const f32x4*)(ssp + ((size_t)row * 2 + which) * 8), b = *(const f32x4*)(ssp + ((size_t)row * 2 + which) * 8 + 4);
;     return 1.0f / sqrtf((((a[0] + a[1]) + (a[2] + a[3])) + ((b[0] + b[1]) + (b[2] + b[3]))) * (1.0f / 512.0f) + 1e-6f);
; }
;     __device__ __forceinline__ void operator()(const Acc& acc, const Unit& u, int wr, int wc, int fr, int fq) const {
;         const int row0 = u.row0 + wr * 64 + fr, col0 = u.col0 + wc * 32 + 8 * fq;
; #pragma unroll
;         for (int ai = 0; ai < 2; ++ai)
; #pragma unroll
;             for (int m = 0; m < 4; ++m) { const int row = row0 + ai * HALF + m * 16; const float rs = latent_rstd(ssp, row, 1); bf16_t* rowp = O + (size_t)row * ldc + col0;
; #pragma unroll
;                 for (int bj = 0; bj < 2; ++bj) *(u32x4*)(rowp + bj * HALF) = pack8(acc[ai][bj][m][0] * rs, acc[ai][bj][m][1] * rs); }
;     }
	v_mov_b32_e32 v114, v190
	v_mov_b32_e32 v115, v191
	v_mov_b32_e32 v116, v192
	v_mov_b32_e32 v117, v193
	v_mov_b32_e32 v126, v114
	v_mov_b32_e32 v118, v194
	v_mov_b32_e32 v119, v195
	v_mov_b32_e32 v120, v196
	v_mov_b32_e32 v121, v197
	v_mov_b32_e32 v127, v118
	v_mov_b32_e32 v118, v115
	v_mov_b32_e32 v114, v116
	v_mov_b32_e32 v115, v120
	v_mov_b32_e32 v120, v117
	v_pk_add_f32 v[116:117], v[126:127], v[118:119]
	v_pk_add_f32 v[114:115], v[114:115], v[120:121]
	s_nop 0
	v_pk_add_f32 v[114:115], v[116:117], v[114:115]
	v_lshl_add_u64 v[116:117], s[12:13], 0, v[124:125]
	v_add_f32_e32 v114, v114, v115
	v_fmamk_f32 v114, v114, 0x3b000000, v139
	v_mul_f32_e32 v115, 0x4f800000, v114
	v_cmp_gt_f32_e32 vcc, s72, v114
	v_lshl_add_u64 v[116:117], v[116:117], 0, v[130:131]
	s_nop 0
	v_cndmask_b32_e32 v118, v114, v115, vcc
	v_sqrt_f32_e32 v119, v118
	v_lshlrev_b64 v[114:115], 6, v[122:123]
	v_lshl_add_u64 v[114:115], s[10:11], 0, v[114:115]
	v_add_u32_e32 v120, -1, v119
	v_add_u32_e32 v121, 1, v119
	v_fma_f32 v124, -v120, v119, v118
	v_fma_f32 v125, -v121, v119, v118
	v_cmp_ge_f32_e64 s[4:5], 0, v124
	s_nop 1
	v_cndmask_b32_e64 v119, v119, v120, s[4:5]
	v_cmp_lt_f32_e64 s[4:5], 0, v125
	s_nop 1
	v_cndmask_b32_e64 v119, v119, v121, s[4:5]
	v_mul_f32_e32 v120, 0x37800000, v119
	v_cndmask_b32_e32 v119, v119, v120, vcc
	v_cmp_class_f32_e32 vcc, v118, v146
	s_nop 1
	v_cndmask_b32_e32 v118, v119, v118, vcc
	v_div_scale_f32 v119, s[4:5], v118, v118, 1.0
	v_rcp_f32_e32 v120, v119
	v_div_scale_f32 v121, vcc, 1.0, v118, 1.0
	v_fma_f32 v124, -v119, v120, 1.0
	v_fmac_f32_e32 v120, v124, v120
	v_mul_f32_e32 v124, v121, v120
	v_fma_f32 v125, -v119, v124, v121
	v_fmac_f32_e32 v124, v125, v120
	v_fma_f32 v119, -v119, v124, v121
	v_div_fmas_f32 v119, v119, v120, v124
	v_div_fixup_f32 v118, v119, v118, 1.0
	v_pk_mul_f32 v[112:113], v[112:113], v[118:119] op_sel_hi:[1,0]
	v_pk_mul_f32 v[110:111], v[110:111], v[118:119] op_sel_hi:[1,0]
	v_pk_mul_f32 v[108:109], v[108:109], v[118:119] op_sel_hi:[1,0]
	v_pk_mul_f32 v[106:107], v[106:107], v[118:119] op_sel_hi:[1,0]
	v_pk_mul_f32 v[104:105], v[104:105], v[118:119] op_sel_hi:[1,0]
	v_pk_mul_f32 v[102:103], v[102:103], v[118:119] op_sel_hi:[1,0]
	v_pk_mul_f32 v[120:121], v[100:101], v[118:119] op_sel_hi:[1,0]
	v_pk_mul_f32 v[118:119], v[98:99], v[118:119] op_sel_hi:[1,0]
	v_cvt_pk_bf16_f32 v98, v110, v111
	v_cvt_pk_bf16_f32 v99, v112, v113
	v_cvt_pk_bf16_f32 v100, v106, v107
	v_cvt_pk_bf16_f32 v101, v108, v109
	global_store_dwordx4 v[116:117], v[98:101], off
	v_lshlrev_b64 v[108:109], 12, v[122:123]
	v_add_u32_e32 v106, 48, v132
	v_cvt_pk_bf16_f32 v98, v102, v103
	v_cvt_pk_bf16_f32 v99, v104, v105
	v_cvt_pk_bf16_f32 v100, v118, v119
	v_cvt_pk_bf16_f32 v101, v120, v121
	global_store_dwordx4 v[116:117], v[98:101], off offset:256
	s_nop 0
	v_ashrrev_i32_e32 v107, 31, v106
	s_waitcnt vmcnt(14)
	v_mov_b32_e32 v98, v200
	v_mov_b32_e32 v99, v201
	v_mov_b32_e32 v100, v202
	v_mov_b32_e32 v101, v203
	v_mov_b32_e32 v110, v98
	v_mov_b32_e32 v102, v204
	v_mov_b32_e32 v103, v205
	v_mov_b32_e32 v104, v206
	v_mov_b32_e32 v105, v207
	v_mov_b32_e32 v111, v102
	v_mov_b32_e32 v102, v99
	v_mov_b32_e32 v98, v100
	v_mov_b32_e32 v99, v104
	v_mov_b32_e32 v104, v101
	v_pk_add_f32 v[100:101], v[110:111], v[102:103]
	v_pk_add_f32 v[98:99], v[98:99], v[104:105]
	s_nop 0
	v_pk_add_f32 v[98:99], v[100:101], v[98:99]
	v_lshl_add_u64 v[100:101], s[12:13], 0, v[108:109]
	v_add_f32_e32 v98, v98, v99
	v_fmamk_f32 v98, v98, 0x3b000000, v139
	v_mul_f32_e32 v99, 0x4f800000, v98
	v_cmp_gt_f32_e32 vcc, s72, v98
	v_lshl_add_u64 v[100:101], v[100:101], 0, v[130:131]
	s_nop 0
	v_cndmask_b32_e32 v102, v98, v99, vcc
	v_sqrt_f32_e32 v103, v102
	v_lshlrev_b64 v[98:99], 6, v[106:107]
	v_lshl_add_u64 v[98:99], s[10:11], 0, v[98:99]
	v_add_u32_e32 v104, -1, v103
	v_add_u32_e32 v105, 1, v103
	v_fma_f32 v108, -v104, v103, v102
	v_fma_f32 v109, -v105, v103, v102
	v_cmp_ge_f32_e64 s[4:5], 0, v108
	s_nop 1
	v_cndmask_b32_e64 v103, v103, v104, s[4:5]
	v_cmp_lt_f32_e64 s[4:5], 0, v109
	s_nop 1
	v_cndmask_b32_e64 v103, v103, v105, s[4:5]
	v_mul_f32_e32 v104, 0x37800000, v103
	v_cndmask_b32_e32 v103, v103, v104, vcc
	v_cmp_class_f32_e32 vcc, v102, v146
	s_nop 1
	v_cndmask_b32_e32 v102, v103, v102, vcc
	v_div_scale_f32 v103, s[4:5], v102, v102, 1.0
	v_rcp_f32_e32 v104, v103
	v_div_scale_f32 v105, vcc, 1.0, v102, 1.0
	v_fma_f32 v108, -v103, v104, 1.0
	v_fmac_f32_e32 v104, v108, v104
	v_mul_f32_e32 v108, v105, v104
	v_fma_f32 v109, -v103, v108, v105
	v_fmac_f32_e32 v108, v109, v104
	v_fma_f32 v103, -v103, v108, v105
	v_div_fmas_f32 v103, v103, v104, v108
	v_div_fixup_f32 v102, v103, v102, 1.0
	v_pk_mul_f32 v[96:97], v[96:97], v[102:103] op_sel_hi:[1,0]
	v_pk_mul_f32 v[94:95], v[94:95], v[102:103] op_sel_hi:[1,0]
	v_pk_mul_f32 v[92:93], v[92:93], v[102:103] op_sel_hi:[1,0]
	v_pk_mul_f32 v[90:91], v[90:91], v[102:103] op_sel_hi:[1,0]
	v_pk_mul_f32 v[88:89], v[88:89], v[102:103] op_sel_hi:[1,0]
	v_pk_mul_f32 v[86:87], v[86:87], v[102:103] op_sel_hi:[1,0]
	v_pk_mul_f32 v[104:105], v[84:85], v[102:103] op_sel_hi:[1,0]
	v_pk_mul_f32 v[102:103], v[82:83], v[102:103] op_sel_hi:[1,0]
	v_cvt_pk_bf16_f32 v82, v94, v95
	v_cvt_pk_bf16_f32 v83, v96, v97
	v_cvt_pk_bf16_f32 v84, v90, v91
	v_cvt_pk_bf16_f32 v85, v92, v93
	global_store_dwordx4 v[100:101], v[82:85], off
	v_lshlrev_b64 v[92:93], 12, v[106:107]
	v_add_u32_e32 v90, 0x80, v132
	v_cvt_pk_bf16_f32 v82, v86, v87
	v_cvt_pk_bf16_f32 v83, v88, v89
	v_cvt_pk_bf16_f32 v84, v102, v103
	v_cvt_pk_bf16_f32 v85, v104, v105
	global_store_dwordx4 v[100:101], v[82:85], off offset:256
	s_nop 0
	v_ashrrev_i32_e32 v91, 31, v90
	s_waitcnt vmcnt(14)
; __device__ __forceinline__ u32x4 pack8(f32x4 a, f32x4 b) { u32x4 w; w.x = cvtpk(a[0], a[1]); w.y = cvtpk(a[2], a[3]); w.z = cvtpk(b[0], b[1]); w.w = cvtpk(b[2], b[3]); return w; }
; __device__ __forceinline__ float latent_rstd(const float* ssp, int row, int which) {
;     const f32x4 a = *(const f32x4*)(ssp + ((size_t)row * 2 + which) * 8), b = *(const f32x4*)(ssp + ((size_t)row * 2 + which) * 8 + 4);
;     return 1.0f / sqrtf((((a[0] + a[1]) + (a[2] + a[3])) + ((b[0] + b[1]) + (b[2] + b[3]))) * (1.0f / 512.0f) + 1e-6f);
; }
;     __device__ __forceinline__ void operator()(const Acc& acc, const Unit& u, int wr, int wc, int fr, int fq) const {
;         const int row0 = u.row0 + wr * 64 + fr, col0 = u.col0 + wc * 32 + 8 * fq;
; #pragma unroll
;         for (int ai = 0; ai < 2; ++ai)
; #pragma unroll
;             for (int m = 0; m < 4; ++m) { const int row = row0 + ai * HALF + m * 16; const float rs = latent_rstd(ssp, row, 1); bf16_t* rowp = O + (size_t)row * ldc + col0;
; #pragma unroll
;                 for (int bj = 0; bj < 2; ++bj) *(u32x4*)(rowp + bj * HALF) = pack8(acc[ai][bj][m][0] * rs, acc[ai][bj][m][1] * rs); }
;     }
	v_mov_b32_e32 v82, v208
	v_mov_b32_e32 v83, v209
	v_mov_b32_e32 v84, v210
	v_mov_b32_e32 v85, v211
	v_mov_b32_e32 v94, v82
	v_mov_b32_e32 v86, v212
	v_mov_b32_e32 v87, v213
	v_mov_b32_e32 v88, v214
	v_mov_b32_e32 v89, v215
	v_mov_b32_e32 v95, v86
	v_mov_b32_e32 v86, v83
	v_mov_b32_e32 v82, v84
	v_mov_b32_e32 v83, v88
	v_mov_b32_e32 v88, v85
	v_pk_add_f32 v[84:85], v[94:95], v[86:87]
	v_pk_add_f32 v[82:83], v[82:83], v[88:89]
	s_nop 0
	v_pk_add_f32 v[82:83], v[84:85], v[82:83]
	v_lshl_add_u64 v[84:85], s[12:13], 0, v[92:93]
	v_add_f32_e32 v82, v82, v83
	v_fmamk_f32 v82, v82, 0x3b000000, v139
	v_mul_f32_e32 v83, 0x4f800000, v82
	v_cmp_gt_f32_e32 vcc, s72, v82
	v_lshl_add_u64 v[84:85], v[84:85], 0, v[130:131]
	s_nop 0
	v_cndmask_b32_e32 v86, v82, v83, vcc
	v_sqrt_f32_e32 v87, v86
	v_lshlrev_b64 v[82:83], 6, v[90:91]
	v_lshl_add_u64 v[82:83], s[10:11], 0, v[82:83]
	v_add_u32_e32 v88, -1, v87
	v_add_u32_e32 v89, 1, v87
	v_fma_f32 v92, -v88, v87, v86
	v_fma_f32 v93, -v89, v87, v86
	v_cmp_ge_f32_e64 s[4:5], 0, v92
	s_nop 1
	v_cndmask_b32_e64 v87, v87, v88, s[4:5]
	v_cmp_lt_f32_e64 s[4:5], 0, v93
	s_nop 1
	v_cndmask_b32_e64 v87, v87, v89, s[4:5]
	v_mul_f32_e32 v88, 0x37800000, v87
	v_cndmask_b32_e32 v87, v87, v88, vcc
	v_cmp_class_f32_e32 vcc, v86, v146
	s_nop 1
	v_cndmask_b32_e32 v86, v87, v86, vcc
	v_div_scale_f32 v87, s[4:5], v86, v86, 1.0
	v_rcp_f32_e32 v88, v87
	v_div_scale_f32 v89, vcc, 1.0, v86, 1.0
	v_fma_f32 v92, -v87, v88, 1.0
	v_fmac_f32_e32 v88, v92, v88
	v_mul_f32_e32 v92, v89, v88
	v_fma_f32 v93, -v87, v92, v89
	v_fmac_f32_e32 v92, v93, v88
	v_fma_f32 v87, -v87, v92, v89
	v_div_fmas_f32 v87, v87, v88, v92
	v_div_fixup_f32 v86, v87, v86, 1.0
	v_pk_mul_f32 v[80:81], v[80:81], v[86:87] op_sel_hi:[1,0]
	v_pk_mul_f32 v[78:79], v[78:79], v[86:87] op_sel_hi:[1,0]
	v_pk_mul_f32 v[76:77], v[76:77], v[86:87] op_sel_hi:[1,0]
	v_pk_mul_f32 v[74:75], v[74:75], v[86:87] op_sel_hi:[1,0]
	v_pk_mul_f32 v[72:73], v[72:73], v[86:87] op_sel_hi:[1,0]
	v_pk_mul_f32 v[70:71], v[70:71], v[86:87] op_sel_hi:[1,0]
	v_pk_mul_f32 v[88:89], v[68:69], v[86:87] op_sel_hi:[1,0]
	v_pk_mul_f32 v[86:87], v[66:67], v[86:87] op_sel_hi:[1,0]
	v_cvt_pk_bf16_f32 v66, v78, v79
	v_cvt_pk_bf16_f32 v67, v80, v81
	v_cvt_pk_bf16_f32 v68, v74, v75
	v_cvt_pk_bf16_f32 v69, v76, v77
	global_store_dwordx4 v[84:85], v[66:69], off
	v_lshlrev_b64 v[76:77], 12, v[90:91]
	v_add_u32_e32 v74, 0x90, v132
	v_cvt_pk_bf16_f32 v66, v70, v71
	v_cvt_pk_bf16_f32 v67, v72, v73
	v_cvt_pk_bf16_f32 v68, v86, v87
	v_cvt_pk_bf16_f32 v69, v88, v89
	global_store_dwordx4 v[84:85], v[66:69], off offset:256
	s_nop 0
	v_ashrrev_i32_e32 v75, 31, v74
	s_waitcnt vmcnt(14)
	v_mov_b32_e32 v66, v216
	v_mov_b32_e32 v67, v217
	v_mov_b32_e32 v68, v218
	v_mov_b32_e32 v69, v219
	v_mov_b32_e32 v78, v66
	v_mov_b32_e32 v70, v220
	v_mov_b32_e32 v71, v221
	v_mov_b32_e32 v72, v222
	v_mov_b32_e32 v73, v223
	v_mov_b32_e32 v79, v70
	v_mov_b32_e32 v70, v67
	v_mov_b32_e32 v66, v68
	v_mov_b32_e32 v67, v72
	v_mov_b32_e32 v72, v69
	v_pk_add_f32 v[68:69], v[78:79], v[70:71]
	v_pk_add_f32 v[66:67], v[66:67], v[72:73]
	s_nop 0
	v_pk_add_f32 v[66:67], v[68:69], v[66:67]
	v_lshl_add_u64 v[68:69], s[12:13], 0, v[76:77]
	v_add_f32_e32 v66, v66, v67
	v_fmamk_f32 v66, v66, 0x3b000000, v139
	v_mul_f32_e32 v67, 0x4f800000, v66
	v_cmp_gt_f32_e32 vcc, s72, v66
	v_lshl_add_u64 v[68:69], v[68:69], 0, v[130:131]
	s_nop 0
	v_cndmask_b32_e32 v70, v66, v67, vcc
	v_sqrt_f32_e32 v71, v70
	v_lshlrev_b64 v[66:67], 6, v[74:75]
	v_lshl_add_u64 v[66:67], s[10:11], 0, v[66:67]
	v_add_u32_e32 v72, -1, v71
	v_add_u32_e32 v73, 1, v71
	v_fma_f32 v76, -v72, v71, v70
	v_fma_f32 v77, -v73, v71, v70
	v_cmp_ge_f32_e64 s[4:5], 0, v76
	s_nop 1
	v_cndmask_b32_e64 v71, v71, v72, s[4:5]
	v_cmp_lt_f32_e64 s[4:5], 0, v77
	s_nop 1
	v_cndmask_b32_e64 v71, v71, v73, s[4:5]
	v_mul_f32_e32 v72, 0x37800000, v71
	v_cndmask_b32_e32 v71, v71, v72, vcc
	v_cmp_class_f32_e32 vcc, v70, v146
	s_nop 1
	v_cndmask_b32_e32 v70, v71, v70, vcc
	v_div_scale_f32 v71, s[4:5], v70, v70, 1.0
	v_rcp_f32_e32 v72, v71
	v_div_scale_f32 v73, vcc, 1.0, v70, 1.0
	v_fma_f32 v76, -v71, v72, 1.0
	v_fmac_f32_e32 v72, v76, v72
	v_mul_f32_e32 v76, v73, v72
	v_fma_f32 v77, -v71, v76, v73
	v_fmac_f32_e32 v76, v77, v72
	v_fma_f32 v71, -v71, v76, v73
	v_div_fmas_f32 v71, v71, v72, v76
	v_div_fixup_f32 v70, v71, v70, 1.0
	v_pk_mul_f32 v[64:65], v[64:65], v[70:71] op_sel_hi:[1,0]
	v_pk_mul_f32 v[62:63], v[62:63], v[70:71] op_sel_hi:[1,0]
	v_pk_mul_f32 v[60:61], v[60:61], v[70:71] op_sel_hi:[1,0]
	v_pk_mul_f32 v[58:59], v[58:59], v[70:71] op_sel_hi:[1,0]
	v_pk_mul_f32 v[56:57], v[56:57], v[70:71] op_sel_hi:[1,0]
	v_pk_mul_f32 v[54:55], v[54:55], v[70:71] op_sel_hi:[1,0]
	v_pk_mul_f32 v[72:73], v[52:53], v[70:71] op_sel_hi:[1,0]
	v_pk_mul_f32 v[70:71], v[50:51], v[70:71] op_sel_hi:[1,0]
	v_cvt_pk_bf16_f32 v50, v62, v63
	v_cvt_pk_bf16_f32 v51, v64, v65
	v_cvt_pk_bf16_f32 v52, v58, v59
	v_cvt_pk_bf16_f32 v53, v60, v61
	global_store_dwordx4 v[68:69], v[50:53], off
	v_lshlrev_b64 v[60:61], 12, v[74:75]
	v_add_u32_e32 v58, 0xa0, v132
	v_cvt_pk_bf16_f32 v50, v54, v55
	v_cvt_pk_bf16_f32 v51, v56, v57
	v_cvt_pk_bf16_f32 v52, v70, v71
	v_cvt_pk_bf16_f32 v53, v72, v73
	global_store_dwordx4 v[68:69], v[50:53], off offset:256
	s_nop 0
	v_ashrrev_i32_e32 v59, 31, v58
	s_waitcnt vmcnt(14)
; __device__ __forceinline__ u32x4 pack8(f32x4 a, f32x4 b) { u32x4 w; w.x = cvtpk(a[0], a[1]); w.y = cvtpk(a[2], a[3]); w.z = cvtpk(b[0], b[1]); w.w = cvtpk(b[2], b[3]); return w; }
; __device__ __forceinline__ float latent_rstd(const float* ssp, int row, int which) {
;     const f32x4 a = *(const f32x4*)(ssp + ((size_t)row * 2 + which) * 8), b = *(const f32x4*)(ssp + ((size_t)row * 2 + which) * 8 + 4);
;     return 1.0f / sqrtf((((a[0] + a[1]) + (a[2] + a[3])) + ((b[0] + b[1]) + (b[2] + b[3]))) * (1.0f / 512.0f) + 1e-6f);
; }
;     __device__ __forceinline__ void operator()(const Acc& acc, const Unit& u, int wr, int wc, int fr, int fq) const {
;         const int row0 = u.row0 + wr * 64 + fr, col0 = u.col0 + wc * 32 + 8 * fq;
; #pragma unroll
;         for (int ai = 0; ai < 2; ++ai)
; #pragma unroll
;             for (int m = 0; m < 4; ++m) { const int row = row0 + ai * HALF + m * 16; const float rs = latent_rstd(ssp, row, 1); bf16_t* rowp = O + (size_t)row * ldc + col0;
; #pragma unroll
;                 for (int bj = 0; bj < 2; ++bj) *(u32x4*)(rowp + bj * HALF) = pack8(acc[ai][bj][m][0] * rs, acc[ai][bj][m][1] * rs); }
;     }
	v_mov_b32_e32 v50, v224
	v_mov_b32_e32 v51, v225
	v_mov_b32_e32 v52, v226
	v_mov_b32_e32 v53, v227
	v_mov_b32_e32 v62, v50
	v_mov_b32_e32 v54, v228
	v_mov_b32_e32 v55, v229
	v_mov_b32_e32 v56, v230
	v_mov_b32_e32 v57, v231
	v_mov_b32_e32 v63, v54
	v_mov_b32_e32 v54, v51
	v_mov_b32_e32 v50, v52
	v_mov_b32_e32 v51, v56
	v_mov_b32_e32 v56, v53
	v_pk_add_f32 v[52:53], v[62:63], v[54:55]
	v_pk_add_f32 v[50:51], v[50:51], v[56:57]
	s_nop 0
	v_pk_add_f32 v[50:51], v[52:53], v[50:51]
	v_lshl_add_u64 v[52:53], s[12:13], 0, v[60:61]
	v_add_f32_e32 v50, v50, v51
	v_fmamk_f32 v50, v50, 0x3b000000, v139
	v_mul_f32_e32 v51, 0x4f800000, v50
	v_cmp_gt_f32_e32 vcc, s72, v50
	v_lshl_add_u64 v[52:53], v[52:53], 0, v[130:131]
	s_nop 0
	v_cndmask_b32_e32 v54, v50, v51, vcc
	v_sqrt_f32_e32 v55, v54
	v_lshlrev_b64 v[50:51], 6, v[58:59]
	v_lshl_add_u64 v[50:51], s[10:11], 0, v[50:51]
	v_add_u32_e32 v56, -1, v55
	v_add_u32_e32 v57, 1, v55
	v_fma_f32 v60, -v56, v55, v54
	v_fma_f32 v61, -v57, v55, v54
	v_cmp_ge_f32_e64 s[4:5], 0, v60
	s_nop 1
	v_cndmask_b32_e64 v55, v55, v56, s[4:5]
	v_cmp_lt_f32_e64 s[4:5], 0, v61
	s_nop 1
	v_cndmask_b32_e64 v55, v55, v57, s[4:5]
	v_mul_f32_e32 v56, 0x37800000, v55
	v_cndmask_b32_e32 v55, v55, v56, vcc
	v_cmp_class_f32_e32 vcc, v54, v146
	s_nop 1
	v_cndmask_b32_e32 v54, v55, v54, vcc
	v_div_scale_f32 v55, s[4:5], v54, v54, 1.0
	v_rcp_f32_e32 v56, v55
	v_div_scale_f32 v57, vcc, 1.0, v54, 1.0
	v_fma_f32 v60, -v55, v56, 1.0
	v_fmac_f32_e32 v56, v60, v56
	v_mul_f32_e32 v60, v57, v56
	v_fma_f32 v61, -v55, v60, v57
	v_fmac_f32_e32 v60, v61, v56
	v_fma_f32 v55, -v55, v60, v57
	v_div_fmas_f32 v55, v55, v56, v60
	v_div_fixup_f32 v54, v55, v54, 1.0
	v_pk_mul_f32 v[48:49], v[48:49], v[54:55] op_sel_hi:[1,0]
	v_pk_mul_f32 v[46:47], v[46:47], v[54:55] op_sel_hi:[1,0]
	v_pk_mul_f32 v[44:45], v[44:45], v[54:55] op_sel_hi:[1,0]
	v_pk_mul_f32 v[42:43], v[42:43], v[54:55] op_sel_hi:[1,0]
	v_pk_mul_f32 v[40:41], v[40:41], v[54:55] op_sel_hi:[1,0]
	v_pk_mul_f32 v[38:39], v[38:39], v[54:55] op_sel_hi:[1,0]
	v_pk_mul_f32 v[56:57], v[36:37], v[54:55] op_sel_hi:[1,0]
	v_pk_mul_f32 v[54:55], v[34:35], v[54:55] op_sel_hi:[1,0]
	v_cvt_pk_bf16_f32 v34, v46, v47
	v_cvt_pk_bf16_f32 v35, v48, v49
	v_cvt_pk_bf16_f32 v36, v42, v43
	v_cvt_pk_bf16_f32 v37, v44, v45
	global_store_dwordx4 v[52:53], v[34:37], off
	v_lshlrev_b64 v[44:45], 12, v[58:59]
	v_add_u32_e32 v42, 0xb0, v132
	v_cvt_pk_bf16_f32 v34, v38, v39
	v_cvt_pk_bf16_f32 v35, v40, v41
	v_cvt_pk_bf16_f32 v36, v54, v55
	v_cvt_pk_bf16_f32 v37, v56, v57
	global_store_dwordx4 v[52:53], v[34:37], off offset:256
	s_nop 0
	v_ashrrev_i32_e32 v43, 31, v42
	s_waitcnt vmcnt(14)
; __device__ __forceinline__ u32x4 pack8(f32x4 a, f32x4 b) { u32x4 w; w.x = cvtpk(a[0], a[1]); w.y = cvtpk(a[2], a[3]); w.z = cvtpk(b[0], b[1]); w.w = cvtpk(b[2], b[3]); return w; }
; #define PG8_BAR __builtin_amdgcn_s_barrier()
; __device__ __forceinline__ float latent_rstd(const float* ssp, int row, int which) {
;     const f32x4 a = *(const f32x4*)(ssp + ((size_t)row * 2 + which) * 8), b = *(const f32x4*)(ssp + ((size_t)row * 2 + which) * 8 + 4);
;     return 1.0f / sqrtf((((a[0] + a[1]) + (a[2] + a[3])) + ((b[0] + b[1]) + (b[2] + b[3]))) * (1.0f / 512.0f) + 1e-6f);
; }
;     __device__ __forceinline__ void operator()(const Acc& acc, const Unit& u, int wr, int wc, int fr, int fq) const {
;         const int row0 = u.row0 + wr * 64 + fr, col0 = u.col0 + wc * 32 + 8 * fq;
; #pragma unroll
;         for (int ai = 0; ai < 2; ++ai)
; #pragma unroll
;             for (int m = 0; m < 4; ++m) { const int row = row0 + ai * HALF + m * 16; const float rs = latent_rstd(ssp, row, 1); bf16_t* rowp = O + (size_t)row * ldc + col0;
; #pragma unroll
;                 for (int bj = 0; bj < 2; ++bj) *(u32x4*)(rowp + bj * HALF) = pack8(acc[ai][bj][m][0] * rs, acc[ai][bj][m][1] * rs); }
;     }
; template <class Epi, class Sched, bool F8 = false, bool MID = false, bool GATHER = false>
; __device__ __forceinline__ void gemm_phase(LAS unsigned char* lds, const Gemm g, const Sched& S, const Epi& E) {
;     ...
;         if (!has_next) break;
; #pragma unroll
;         for (int a = 0; a < 2; ++a)
; #pragma unroll
;             for (int b = 0; b < 2; ++b)
; #pragma unroll
;                 for (int m = 0; m < 4; ++m)
; #pragma unroll
;                     for (int n = 0; n < 2; ++n) acc[a][b][m][n] = (f32x4){0.f, 0.f, 0.f, 0.f};
;         cur = nxt; cA = nA; cB = nB; ++ui;
;         if constexpr (GATHER) {
; #pragma unroll
;             for (int i = 0; i < 2; ++i) { voffA[i] = nvA0[i]; voffA1[i] = nvA1[i]; } }
;         if (wr == 1) PG8_BAR;
;     }
	v_mov_b32_e32 v34, v232
	v_mov_b32_e32 v35, v233
	v_mov_b32_e32 v36, v234
	v_mov_b32_e32 v37, v235
	v_mov_b32_e32 v46, v34
	v_mov_b32_e32 v38, v236
	v_mov_b32_e32 v39, v237
	v_mov_b32_e32 v40, v238
	v_mov_b32_e32 v41, v239
	v_mov_b32_e32 v47, v38
	v_mov_b32_e32 v38, v35
	v_mov_b32_e32 v34, v36
	v_mov_b32_e32 v35, v40
	v_mov_b32_e32 v40, v37
	v_pk_add_f32 v[36:37], v[46:47], v[38:39]
	v_pk_add_f32 v[34:35], v[34:35], v[40:41]
	s_nop 0
	v_pk_add_f32 v[34:35], v[36:37], v[34:35]
	v_lshl_add_u64 v[36:37], s[12:13], 0, v[44:45]
	v_add_f32_e32 v34, v34, v35
	v_fmamk_f32 v34, v34, 0x3b000000, v139
	v_mul_f32_e32 v35, 0x4f800000, v34
	v_cmp_gt_f32_e32 vcc, s72, v34
	v_lshl_add_u64 v[36:37], v[36:37], 0, v[130:131]
	s_nop 0
	v_cndmask_b32_e32 v38, v34, v35, vcc
	v_sqrt_f32_e32 v39, v38
	v_lshlrev_b64 v[34:35], 6, v[42:43]
	v_lshl_add_u64 v[34:35], s[10:11], 0, v[34:35]
	v_add_u32_e32 v40, -1, v39
	v_add_u32_e32 v41, 1, v39
	v_fma_f32 v44, -v40, v39, v38
	v_fma_f32 v45, -v41, v39, v38
	v_cmp_ge_f32_e64 s[4:5], 0, v44
	s_nop 1
	v_cndmask_b32_e64 v39, v39, v40, s[4:5]
	v_cmp_lt_f32_e64 s[4:5], 0, v45
	s_nop 1
	v_cndmask_b32_e64 v39, v39, v41, s[4:5]
	v_mul_f32_e32 v40, 0x37800000, v39
	v_cndmask_b32_e32 v39, v39, v40, vcc
	v_cmp_class_f32_e32 vcc, v38, v146
	s_nop 1
	v_cndmask_b32_e32 v38, v39, v38, vcc
	v_div_scale_f32 v39, s[4:5], v38, v38, 1.0
	v_rcp_f32_e32 v40, v39
	v_div_scale_f32 v41, vcc, 1.0, v38, 1.0
	v_fma_f32 v44, -v39, v40, 1.0
	v_fmac_f32_e32 v40, v44, v40
	v_mul_f32_e32 v44, v41, v40
	v_fma_f32 v45, -v39, v44, v41
	v_fmac_f32_e32 v44, v45, v40
	v_fma_f32 v39, -v39, v44, v41
	v_div_fmas_f32 v39, v39, v40, v44
	v_div_fixup_f32 v38, v39, v38, 1.0
	v_pk_mul_f32 v[40:41], v[20:21], v[38:39] op_sel_hi:[1,0]
	v_pk_mul_f32 v[20:21], v[18:19], v[38:39] op_sel_hi:[1,0]
	v_pk_mul_f32 v[24:25], v[24:25], v[38:39] op_sel_hi:[1,0]
	v_pk_mul_f32 v[22:23], v[22:23], v[38:39] op_sel_hi:[1,0]
	v_pk_mul_f32 v[28:29], v[28:29], v[38:39] op_sel_hi:[1,0]
	v_cvt_pk_bf16_f32 v18, v22, v23
	v_cvt_pk_bf16_f32 v19, v24, v25
	v_cvt_pk_bf16_f32 v20, v20, v21
	v_cvt_pk_bf16_f32 v21, v40, v41
	v_pk_mul_f32 v[26:27], v[26:27], v[38:39] op_sel_hi:[1,0]
	v_pk_mul_f32 v[32:33], v[32:33], v[38:39] op_sel_hi:[1,0]
	v_pk_mul_f32 v[30:31], v[30:31], v[38:39] op_sel_hi:[1,0]
	global_store_dwordx4 v[36:37], v[18:21], off
	s_nop 1
	v_cvt_pk_bf16_f32 v18, v26, v27
	v_cvt_pk_bf16_f32 v19, v28, v29
	v_cvt_pk_bf16_f32 v20, v30, v31
	v_cvt_pk_bf16_f32 v21, v32, v33
	global_store_dwordx4 v[36:37], v[18:21], off offset:256
	s_nop 0
	s_waitcnt vmcnt(14)
	v_mov_b32_e32 v18, v240
	v_mov_b32_e32 v19, v241
	v_mov_b32_e32 v20, v242
	v_mov_b32_e32 v21, v243
	v_mov_b32_e32 v26, v18
	v_mov_b32_e32 v22, v244
	v_mov_b32_e32 v23, v245
	v_mov_b32_e32 v24, v246
	v_mov_b32_e32 v25, v247
	v_mov_b32_e32 v27, v22
	v_mov_b32_e32 v22, v19
	v_mov_b32_e32 v18, v20
	v_mov_b32_e32 v19, v24
	v_mov_b32_e32 v24, v21
	v_pk_add_f32 v[20:21], v[26:27], v[22:23]
	v_pk_add_f32 v[18:19], v[18:19], v[24:25]
	s_nop 0
	v_pk_add_f32 v[18:19], v[20:21], v[18:19]
	s_nop 0
	v_add_f32_e32 v18, v18, v19
	v_fmamk_f32 v18, v18, 0x3b000000, v139
	v_mul_f32_e32 v19, 0x4f800000, v18
	v_cmp_gt_f32_e32 vcc, s72, v18
	s_nop 1
	v_cndmask_b32_e32 v20, v18, v19, vcc
	v_sqrt_f32_e32 v21, v20
	v_lshlrev_b64 v[18:19], 12, v[42:43]
	v_lshl_add_u64 v[18:19], s[12:13], 0, v[18:19]
	v_lshl_add_u64 v[18:19], v[18:19], 0, v[130:131]
	v_add_u32_e32 v22, -1, v21
	v_add_u32_e32 v23, 1, v21
	v_fma_f32 v24, -v22, v21, v20
	v_fma_f32 v25, -v23, v21, v20
	v_cmp_ge_f32_e64 s[4:5], 0, v24
	s_nop 1
	v_cndmask_b32_e64 v21, v21, v22, s[4:5]
	v_cmp_lt_f32_e64 s[4:5], 0, v25
	s_nop 1
	v_cndmask_b32_e64 v21, v21, v23, s[4:5]
	v_mul_f32_e32 v22, 0x37800000, v21
	v_cndmask_b32_e32 v21, v21, v22, vcc
	v_cmp_class_f32_e32 vcc, v20, v146
	s_nop 1
	v_cndmask_b32_e32 v20, v21, v20, vcc
	v_div_scale_f32 v21, s[4:5], v20, v20, 1.0
	v_rcp_f32_e32 v22, v21
	v_div_scale_f32 v23, vcc, 1.0, v20, 1.0
	s_mov_b64 s[4:5], -1
	v_fma_f32 v24, -v21, v22, 1.0
	v_fmac_f32_e32 v22, v24, v22
	v_mul_f32_e32 v24, v23, v22
	v_fma_f32 v25, -v21, v24, v23
	v_fmac_f32_e32 v24, v25, v22
	v_fma_f32 v21, -v21, v24, v23
	v_div_fmas_f32 v21, v21, v22, v24
	v_div_fixup_f32 v20, v21, v20, 1.0
	v_pk_mul_f32 v[22:23], v[4:5], v[20:21] op_sel_hi:[1,0]
	v_pk_mul_f32 v[4:5], v[2:3], v[20:21] op_sel_hi:[1,0]
	s_andn2_b64 vcc, exec, s[44:45]
	v_pk_mul_f32 v[8:9], v[8:9], v[20:21] op_sel_hi:[1,0]
	v_pk_mul_f32 v[6:7], v[6:7], v[20:21] op_sel_hi:[1,0]
	v_pk_mul_f32 v[12:13], v[12:13], v[20:21] op_sel_hi:[1,0]
	v_cvt_pk_bf16_f32 v2, v6, v7
	v_cvt_pk_bf16_f32 v3, v8, v9
	v_cvt_pk_bf16_f32 v4, v4, v5
	v_cvt_pk_bf16_f32 v5, v22, v23
	v_pk_mul_f32 v[10:11], v[10:11], v[20:21] op_sel_hi:[1,0]
	v_pk_mul_f32 v[16:17], v[16:17], v[20:21] op_sel_hi:[1,0]
	v_pk_mul_f32 v[14:15], v[14:15], v[20:21] op_sel_hi:[1,0]
	global_store_dwordx4 v[18:19], v[2:5], off
	s_nop 1
	v_cvt_pk_bf16_f32 v2, v10, v11
	v_cvt_pk_bf16_f32 v3, v12, v13
	v_cvt_pk_bf16_f32 v4, v14, v15
	v_cvt_pk_bf16_f32 v5, v16, v17
	global_store_dwordx4 v[18:19], v[2:5], off offset:256
	s_cbranch_vccnz .LBB0_1310
	s_andn2_b64 vcc, exec, s[6:7]
	s_cbranch_vccnz .LBB0_1309
	s_barrier
	s_branch .LBB0_1309

; #define LDS_WAIT() asm volatile("s_waitcnt lgkmcnt(0)" ::: "memory")
; __device__ __forceinline__ unsigned cvt4_fp8(float a, float b, float c, float d) { int w = 0; w = __builtin_amdgcn_cvt_pk_fp8_f32(a, b, w, false); w = __builtin_amdgcn_cvt_pk_fp8_f32(c, d, w, true); return (unsigned)w; }
; template <bool MLA>
; __device__ __forceinline__ void attn_unit(char* lds, int h, int qb, const bf16_t* Qp, int ldq, const bf16_t* Kp, int ldk, const bf16_t* KRp, const bf16_t* Vp, int ldv,
;                                           unsigned char* Op, int ldo, const float* KMp, const float* rel_bias) {
;     ...
;     if (hi == 0) li_l[r32] = l_reg; LDS_WAIT();
;     unsigned char* Ow = Op + (size_t)qlo * ldo;
; #pragma unroll
;     for (int r = 0; r < 16; ++r) { const int orow = CROWC(r) + 4 * hi; const float rl = 16.0f * __builtin_amdgcn_rcpf(li_h[CROWC(r)]);
; #pragma unroll
;         for (int d0 = 0; d0 < 4; ++d0) { const float v = o[d0][r] * rl; const float v1 = __shfl_xor(v, 1), v2 = __shfl_xor(v, 2), v3 = __shfl_xor(v1, 2);
;             if ((r32 & 3) == 0) *(unsigned*)(Ow + (size_t)orow * ldo + d0 * 32 + r32) = cvt4_fp8(v, v1, v2, v3); } }
.LBB0_1394:
	s_and_saveexec_b64 s[44:45], s[4:5]
	ds_write_b32 v173, v178
	s_or_b64 exec, exec, s[44:45]
	s_waitcnt lgkmcnt(0)
	ds_read_b32 v66, v167
	v_and_b32_e32 v68, 64, v195
	v_xor_b32_e32 v67, 1, v195
	v_add_u32_e32 v72, 64, v68
	v_cmp_lt_i32_e32 vcc, v67, v72
	s_waitcnt lgkmcnt(0)
	v_rcp_f32_e32 v66, v66
	s_lshl_b32 s10, s27, 7
	v_cndmask_b32_e32 v67, v195, v67, vcc
	v_lshlrev_b32_e32 v68, 2, v67
	v_mul_f32_e32 v69, 0x41800000, v66
	v_mul_f32_e32 v70, v34, v69
	s_nop 1
	v_mov_b32_dpp v71, v70 quad_perm:[1,0,3,2] row_mask:0xf bank_mask:0xf
	v_xor_b32_e32 v67, 2, v195
	s_add_u32 s22, s70, s43
	v_cmp_lt_i32_e32 vcc, v67, v72
	s_addc_u32 s23, s71, 0
	s_add_u32 s10, s22, s10
	v_cndmask_b32_e32 v34, v195, v67, vcc
	s_mov_b32 s43, s11
	v_lshlrev_b32_e32 v34, 2, v34
	s_addc_u32 s22, s23, 0
	s_lshl_b64 s[42:43], s[42:43], 11
	s_nop 1
	v_mov_b32_dpp v72, v70 quad_perm:[2,3,0,1] row_mask:0xf bank_mask:0xf
	s_waitcnt lgkmcnt(0)
	s_nop 1
	v_mov_b32_dpp v73, v71 quad_perm:[2,3,0,1] row_mask:0xf bank_mask:0xf
	s_add_u32 s42, s10, s42
	s_addc_u32 s43, s22, s43
	v_lshl_add_u64 v[66:67], s[42:43], 0, v[168:169]
	v_lshl_add_u64 v[66:67], v[66:67], 0, v[170:171]
	s_and_saveexec_b64 s[42:43], s[6:7]
	s_cbranch_execz .LBB0_1398
	v_mov_b32_e32 v74, v147
	v_cvt_pk_fp8_f32 v74, v70, v71
	s_waitcnt lgkmcnt(0)
	v_cvt_pk_fp8_f32 v74, v72, v73 op_sel:[0,0,1]
	global_store_dword v[66:67], v74, off
.LBB0_1398:
	s_or_b64 exec, exec, s[42:43]
	v_mul_f32_e32 v50, v50, v69
	s_nop 1
	v_mov_b32_dpp v71, v50 quad_perm:[1,0,3,2] row_mask:0xf bank_mask:0xf
	s_nop 1
	v_mov_b32_dpp v70, v50 quad_perm:[2,3,0,1] row_mask:0xf bank_mask:0xf
	s_waitcnt lgkmcnt(0)
	s_nop 1
	v_mov_b32_dpp v72, v71 quad_perm:[2,3,0,1] row_mask:0xf bank_mask:0xf
	s_and_saveexec_b64 s[42:43], s[6:7]
	s_cbranch_execz .LBB0_1400
	v_mov_b32_e32 v73, v147
	v_cvt_pk_fp8_f32 v73, v50, v71
	s_waitcnt lgkmcnt(0)
	v_cvt_pk_fp8_f32 v73, v70, v72 op_sel:[0,0,1]
	global_store_dword v[66:67], v73, off offset:32
.LBB0_1400:
	s_or_b64 exec, exec, s[42:43]
	v_mul_f32_e32 v18, v18, v69
	s_waitcnt lgkmcnt(0)
	s_nop 1
	v_mov_b32_dpp v70, v18 quad_perm:[1,0,3,2] row_mask:0xf bank_mask:0xf
	s_nop 1
	v_mov_b32_dpp v50, v18 quad_perm:[2,3,0,1] row_mask:0xf bank_mask:0xf
	s_waitcnt lgkmcnt(0)
	s_nop 1
	v_mov_b32_dpp v71, v70 quad_perm:[2,3,0,1] row_mask:0xf bank_mask:0xf
	s_and_saveexec_b64 s[42:43], s[6:7]
	s_cbranch_execz .LBB0_1402
	v_mov_b32_e32 v72, v147
	v_cvt_pk_fp8_f32 v72, v18, v70
	s_waitcnt lgkmcnt(0)
	v_cvt_pk_fp8_f32 v72, v50, v71 op_sel:[0,0,1]
	global_store_dword v[66:67], v72, off offset:64
.LBB0_1402:
	s_or_b64 exec, exec, s[42:43]
	v_mul_f32_e32 v2, v2, v69
	s_waitcnt lgkmcnt(0)
	s_nop 1
	v_mov_b32_dpp v50, v2 quad_perm:[1,0,3,2] row_mask:0xf bank_mask:0xf
	s_nop 1
	v_mov_b32_dpp v18, v2 quad_perm:[2,3,0,1] row_mask:0xf bank_mask:0xf
	s_waitcnt lgkmcnt(0)
	s_nop 1
	v_mov_b32_dpp v69, v50 quad_perm:[2,3,0,1] row_mask:0xf bank_mask:0xf
	s_and_saveexec_b64 s[42:43], s[6:7]
	s_cbranch_execz .LBB0_1404
	v_mov_b32_e32 v70, v147
	v_cvt_pk_fp8_f32 v70, v2, v50
	s_waitcnt lgkmcnt(0)
	v_cvt_pk_fp8_f32 v70, v18, v69 op_sel:[0,0,1]
	global_store_dword v[66:67], v70, off offset:96
.LBB0_1404:
	s_or_b64 exec, exec, s[42:43]
	ds_read_b32 v2, v167 offset:4
	s_waitcnt lgkmcnt(0)
	v_rcp_f32_e32 v2, v2
	s_nop 0
	v_mul_f32_e32 v2, 0x41800000, v2
	v_mul_f32_e32 v18, v35, v2
	s_nop 1
	v_mov_b32_dpp v50, v18 quad_perm:[1,0,3,2] row_mask:0xf bank_mask:0xf
	s_nop 1
	v_mov_b32_dpp v35, v18 quad_perm:[2,3,0,1] row_mask:0xf bank_mask:0xf
	s_waitcnt lgkmcnt(0)
	s_nop 1
	v_mov_b32_dpp v69, v50 quad_perm:[2,3,0,1] row_mask:0xf bank_mask:0xf
	s_and_saveexec_b64 s[42:43], s[6:7]
	s_cbranch_execz .LBB0_1406
	v_mov_b32_e32 v70, v147
	v_cvt_pk_fp8_f32 v70, v18, v50
	s_waitcnt lgkmcnt(0)
	v_cvt_pk_fp8_f32 v70, v35, v69 op_sel:[0,0,1]
	global_store_dword v[66:67], v70, off offset:2048
.LBB0_1406:
	s_or_b64 exec, exec, s[42:43]
	v_mul_f32_e32 v18, v51, v2
	s_nop 1
	v_mov_b32_dpp v50, v18 quad_perm:[1,0,3,2] row_mask:0xf bank_mask:0xf
	s_waitcnt lgkmcnt(0)
	s_nop 1
	v_mov_b32_dpp v35, v18 quad_perm:[2,3,0,1] row_mask:0xf bank_mask:0xf
	s_waitcnt lgkmcnt(0)
	s_nop 1
	v_mov_b32_dpp v51, v50 quad_perm:[2,3,0,1] row_mask:0xf bank_mask:0xf
	s_and_saveexec_b64 s[42:43], s[6:7]
	s_cbranch_execz .LBB0_1408
	v_mov_b32_e32 v69, v147
	v_cvt_pk_fp8_f32 v69, v18, v50
	s_waitcnt lgkmcnt(0)
	v_cvt_pk_fp8_f32 v69, v35, v51 op_sel:[0,0,1]
	global_store_dword v[66:67], v69, off offset:2080
.LBB0_1408:
	s_or_b64 exec, exec, s[42:43]
	v_mul_f32_e32 v18, v19, v2
	s_waitcnt lgkmcnt(0)
	s_nop 1
	v_mov_b32_dpp v35, v18 quad_perm:[1,0,3,2] row_mask:0xf bank_mask:0xf
	s_nop 1
	v_mov_b32_dpp v19, v18 quad_perm:[2,3,0,1] row_mask:0xf bank_mask:0xf
	s_waitcnt lgkmcnt(0)
	s_nop 1
	v_mov_b32_dpp v50, v35 quad_perm:[2,3,0,1] row_mask:0xf bank_mask:0xf
	s_and_saveexec_b64 s[42:43], s[6:7]
	s_cbranch_execz .LBB0_1410
	v_mov_b32_e32 v51, v147
	v_cvt_pk_fp8_f32 v51, v18, v35
	s_waitcnt lgkmcnt(0)
	v_cvt_pk_fp8_f32 v51, v19, v50 op_sel:[0,0,1]
	global_store_dword v[66:67], v51, off offset:2112
.LBB0_1410:
	s_or_b64 exec, exec, s[42:43]
	v_mul_f32_e32 v2, v3, v2
	s_nop 1
	v_mov_b32_dpp v18, v2 quad_perm:[1,0,3,2] row_mask:0xf bank_mask:0xf
	s_nop 1
	v_mov_b32_dpp v3, v2 quad_perm:[2,3,0,1] row_mask:0xf bank_mask:0xf
	s_waitcnt lgkmcnt(0)
	s_nop 1
	v_mov_b32_dpp v19, v18 quad_perm:[2,3,0,1] row_mask:0xf bank_mask:0xf
	s_and_saveexec_b64 s[42:43], s[6:7]
	s_cbranch_execz .LBB0_1412
	v_mov_b32_e32 v35, v147
	v_cvt_pk_fp8_f32 v35, v2, v18
	s_waitcnt lgkmcnt(0)
	v_cvt_pk_fp8_f32 v35, v3, v19 op_sel:[0,0,1]
	global_store_dword v[66:67], v35, off offset:2144
; #define LDS_WAIT() asm volatile("s_waitcnt lgkmcnt(0)" ::: "memory")
; __device__ __forceinline__ unsigned cvt4_fp8(float a, float b, float c, float d) { int w = 0; w = __builtin_amdgcn_cvt_pk_fp8_f32(a, b, w, false); w = __builtin_amdgcn_cvt_pk_fp8_f32(c, d, w, true); return (unsigned)w; }
; template <bool MLA>
; __device__ __forceinline__ void attn_unit(char* lds, int h, int qb, const bf16_t* Qp, int ldq, const bf16_t* Kp, int ldk, const bf16_t* KRp, const bf16_t* Vp, int ldv,
;                                           unsigned char* Op, int ldo, const float* KMp, const float* rel_bias) {
;     ...
;     if (hi == 0) li_l[r32] = l_reg; LDS_WAIT();
;     unsigned char* Ow = Op + (size_t)qlo * ldo;
; #pragma unroll
;     for (int r = 0; r < 16; ++r) { const int orow = CROWC(r) + 4 * hi; const float rl = 16.0f * __builtin_amdgcn_rcpf(li_h[CROWC(r)]);
; #pragma unroll
;         for (int d0 = 0; d0 < 4; ++d0) { const float v = o[d0][r] * rl; const float v1 = __shfl_xor(v, 1), v2 = __shfl_xor(v, 2), v3 = __shfl_xor(v1, 2);
;             if ((r32 & 3) == 0) *(unsigned*)(Ow + (size_t)orow * ldo + d0 * 32 + r32) = cvt4_fp8(v, v1, v2, v3); } }
.LBB0_1412:
	s_or_b64 exec, exec, s[42:43]
	ds_read_b32 v2, v167 offset:8
	s_waitcnt lgkmcnt(0)
	v_rcp_f32_e32 v2, v2
	s_nop 0
	v_mul_f32_e32 v2, 0x41800000, v2
	v_mul_f32_e32 v3, v36, v2
	s_nop 1
	v_mov_b32_dpp v19, v3 quad_perm:[1,0,3,2] row_mask:0xf bank_mask:0xf
	s_nop 1
	v_mov_b32_dpp v18, v3 quad_perm:[2,3,0,1] row_mask:0xf bank_mask:0xf
	s_waitcnt lgkmcnt(0)
	s_nop 1
	v_mov_b32_dpp v35, v19 quad_perm:[2,3,0,1] row_mask:0xf bank_mask:0xf
	s_and_saveexec_b64 s[42:43], s[6:7]
	s_cbranch_execz .LBB0_1414
	v_mov_b32_e32 v36, v147
	v_cvt_pk_fp8_f32 v36, v3, v19
	s_waitcnt lgkmcnt(0)
	v_cvt_pk_fp8_f32 v36, v18, v35 op_sel:[0,0,1]
	v_add_co_u32_e32 v18, vcc, 0x1000, v66
	s_nop 1
	v_addc_co_u32_e32 v19, vcc, 0, v67, vcc
	global_store_dword v[18:19], v36, off
.LBB0_1414:
	s_or_b64 exec, exec, s[42:43]
	v_mul_f32_e32 v3, v52, v2
	s_nop 1
	v_mov_b32_dpp v19, v3 quad_perm:[1,0,3,2] row_mask:0xf bank_mask:0xf
	s_waitcnt lgkmcnt(0)
	s_nop 1
	v_mov_b32_dpp v18, v3 quad_perm:[2,3,0,1] row_mask:0xf bank_mask:0xf
	s_waitcnt lgkmcnt(0)
	s_nop 1
	v_mov_b32_dpp v35, v19 quad_perm:[2,3,0,1] row_mask:0xf bank_mask:0xf
	s_and_saveexec_b64 s[42:43], s[6:7]
	s_cbranch_execz .LBB0_1416
	v_mov_b32_e32 v36, v147
	v_cvt_pk_fp8_f32 v36, v3, v19
	s_waitcnt lgkmcnt(0)
	v_cvt_pk_fp8_f32 v36, v18, v35 op_sel:[0,0,1]
	v_add_co_u32_e32 v18, vcc, 0x1000, v66
	s_nop 1
	v_addc_co_u32_e32 v19, vcc, 0, v67, vcc
	global_store_dword v[18:19], v36, off offset:32
.LBB0_1416:
	s_or_b64 exec, exec, s[42:43]
	v_mul_f32_e32 v3, v20, v2
	s_nop 1
	v_mov_b32_dpp v19, v3 quad_perm:[1,0,3,2] row_mask:0xf bank_mask:0xf
	s_waitcnt lgkmcnt(0)
	s_nop 1
	v_mov_b32_dpp v18, v3 quad_perm:[2,3,0,1] row_mask:0xf bank_mask:0xf
	s_waitcnt lgkmcnt(0)
	s_nop 1
	v_mov_b32_dpp v20, v19 quad_perm:[2,3,0,1] row_mask:0xf bank_mask:0xf
	s_and_saveexec_b64 s[42:43], s[6:7]
	s_cbranch_execz .LBB0_1418
	v_mov_b32_e32 v35, v147
	v_cvt_pk_fp8_f32 v35, v3, v19
	s_waitcnt lgkmcnt(0)
	v_cvt_pk_fp8_f32 v35, v18, v20 op_sel:[0,0,1]
	v_add_co_u32_e32 v18, vcc, 0x1000, v66
	s_nop 1
	v_addc_co_u32_e32 v19, vcc, 0, v67, vcc
	global_store_dword v[18:19], v35, off offset:64
.LBB0_1418:
	s_or_b64 exec, exec, s[42:43]
	v_mul_f32_e32 v2, v4, v2
	s_nop 1
	v_mov_b32_dpp v4, v2 quad_perm:[1,0,3,2] row_mask:0xf bank_mask:0xf
	s_nop 1
	v_mov_b32_dpp v3, v2 quad_perm:[2,3,0,1] row_mask:0xf bank_mask:0xf
	s_waitcnt lgkmcnt(0)
	s_nop 1
	v_mov_b32_dpp v18, v4 quad_perm:[2,3,0,1] row_mask:0xf bank_mask:0xf
	s_and_saveexec_b64 s[42:43], s[6:7]
	s_cbranch_execz .LBB0_1420
	v_mov_b32_e32 v19, v147
	v_cvt_pk_fp8_f32 v19, v2, v4
	v_add_co_u32_e32 v2, vcc, 0x1000, v66
	s_waitcnt lgkmcnt(0)
	v_cvt_pk_fp8_f32 v19, v3, v18 op_sel:[0,0,1]
	v_addc_co_u32_e32 v3, vcc, 0, v67, vcc
	global_store_dword v[2:3], v19, off offset:96
.LBB0_1420:
	s_or_b64 exec, exec, s[42:43]
	ds_read_b32 v2, v167 offset:12
	s_waitcnt lgkmcnt(0)
	v_rcp_f32_e32 v2, v2
	s_nop 0
	v_mul_f32_e32 v2, 0x41800000, v2
	v_mul_f32_e32 v3, v37, v2
	s_nop 1
	v_mov_b32_dpp v18, v3 quad_perm:[1,0,3,2] row_mask:0xf bank_mask:0xf
	s_nop 1
	v_mov_b32_dpp v4, v3 quad_perm:[2,3,0,1] row_mask:0xf bank_mask:0xf
	s_waitcnt lgkmcnt(0)
	s_nop 1
	v_mov_b32_dpp v19, v18 quad_perm:[2,3,0,1] row_mask:0xf bank_mask:0xf
	s_and_saveexec_b64 s[42:43], s[6:7]
	s_cbranch_execz .LBB0_1422
	v_mov_b32_e32 v20, v147
	v_cvt_pk_fp8_f32 v20, v3, v18
	v_add_co_u32_e32 v18, vcc, 0x1000, v66
	s_waitcnt lgkmcnt(0)
	v_cvt_pk_fp8_f32 v20, v4, v19 op_sel:[0,0,1]
	v_addc_co_u32_e32 v19, vcc, 0, v67, vcc
	global_store_dword v[18:19], v20, off offset:2048
.LBB0_1422:
	s_or_b64 exec, exec, s[42:43]
	v_mul_f32_e32 v3, v53, v2
	s_nop 1
	v_mov_b32_dpp v18, v3 quad_perm:[1,0,3,2] row_mask:0xf bank_mask:0xf
	s_waitcnt lgkmcnt(0)
	s_nop 1
	v_mov_b32_dpp v4, v3 quad_perm:[2,3,0,1] row_mask:0xf bank_mask:0xf
	s_waitcnt lgkmcnt(0)
	s_nop 1
	v_mov_b32_dpp v19, v18 quad_perm:[2,3,0,1] row_mask:0xf bank_mask:0xf
	s_and_saveexec_b64 s[42:43], s[6:7]
	s_cbranch_execz .LBB0_1424
	v_mov_b32_e32 v20, v147
	v_cvt_pk_fp8_f32 v20, v3, v18
	v_add_co_u32_e32 v18, vcc, 0x1000, v66
	s_waitcnt lgkmcnt(0)
	v_cvt_pk_fp8_f32 v20, v4, v19 op_sel:[0,0,1]
	v_addc_co_u32_e32 v19, vcc, 0, v67, vcc
	global_store_dword v[18:19], v20, off offset:2080
.LBB0_1424:
	s_or_b64 exec, exec, s[42:43]
	v_mul_f32_e32 v3, v21, v2
	s_nop 1
	v_mov_b32_dpp v18, v3 quad_perm:[1,0,3,2] row_mask:0xf bank_mask:0xf
	s_waitcnt lgkmcnt(0)
	s_nop 1
	v_mov_b32_dpp v4, v3 quad_perm:[2,3,0,1] row_mask:0xf bank_mask:0xf
	s_waitcnt lgkmcnt(0)
	s_nop 1
	v_mov_b32_dpp v19, v18 quad_perm:[2,3,0,1] row_mask:0xf bank_mask:0xf
	s_and_saveexec_b64 s[42:43], s[6:7]
	s_cbranch_execz .LBB0_1426
	v_mov_b32_e32 v20, v147
	v_cvt_pk_fp8_f32 v20, v3, v18
	v_add_co_u32_e32 v18, vcc, 0x1000, v66
	s_waitcnt lgkmcnt(0)
	v_cvt_pk_fp8_f32 v20, v4, v19 op_sel:[0,0,1]
	v_addc_co_u32_e32 v19, vcc, 0, v67, vcc
	global_store_dword v[18:19], v20, off offset:2112
.LBB0_1426:
	s_or_b64 exec, exec, s[42:43]
	v_mul_f32_e32 v2, v5, v2
	s_waitcnt lgkmcnt(0)
	s_nop 1
	v_mov_b32_dpp v4, v2 quad_perm:[1,0,3,2] row_mask:0xf bank_mask:0xf
	s_nop 1
	v_mov_b32_dpp v3, v2 quad_perm:[2,3,0,1] row_mask:0xf bank_mask:0xf
	s_waitcnt lgkmcnt(0)
	s_nop 1
	v_mov_b32_dpp v5, v4 quad_perm:[2,3,0,1] row_mask:0xf bank_mask:0xf
	s_and_saveexec_b64 s[42:43], s[6:7]
	s_cbranch_execz .LBB0_1428
	v_mov_b32_e32 v18, v147
	v_cvt_pk_fp8_f32 v18, v2, v4
	v_add_co_u32_e32 v2, vcc, 0x1000, v66
	s_waitcnt lgkmcnt(0)
	v_cvt_pk_fp8_f32 v18, v3, v5 op_sel:[0,0,1]
	v_addc_co_u32_e32 v3, vcc, 0, v67, vcc
	global_store_dword v[2:3], v18, off offset:2144
; #define LDS_WAIT() asm volatile("s_waitcnt lgkmcnt(0)" ::: "memory")
; __device__ __forceinline__ unsigned cvt4_fp8(float a, float b, float c, float d) { int w = 0; w = __builtin_amdgcn_cvt_pk_fp8_f32(a, b, w, false); w = __builtin_amdgcn_cvt_pk_fp8_f32(c, d, w, true); return (unsigned)w; }
; template <bool MLA>
; __device__ __forceinline__ void attn_unit(char* lds, int h, int qb, const bf16_t* Qp, int ldq, const bf16_t* Kp, int ldk, const bf16_t* KRp, const bf16_t* Vp, int ldv,
;                                           unsigned char* Op, int ldo, const float* KMp, const float* rel_bias) {
;     ...
;     if (hi == 0) li_l[r32] = l_reg; LDS_WAIT();
;     unsigned char* Ow = Op + (size_t)qlo * ldo;
; #pragma unroll
;     for (int r = 0; r < 16; ++r) { const int orow = CROWC(r) + 4 * hi; const float rl = 16.0f * __builtin_amdgcn_rcpf(li_h[CROWC(r)]);
; #pragma unroll
;         for (int d0 = 0; d0 < 4; ++d0) { const float v = o[d0][r] * rl; const float v1 = __shfl_xor(v, 1), v2 = __shfl_xor(v, 2), v3 = __shfl_xor(v1, 2);
;             if ((r32 & 3) == 0) *(unsigned*)(Ow + (size_t)orow * ldo + d0 * 32 + r32) = cvt4_fp8(v, v1, v2, v3); } }
.LBB0_1428:
	s_or_b64 exec, exec, s[42:43]
	ds_read_b32 v2, v167 offset:32
	s_waitcnt lgkmcnt(0)
	v_rcp_f32_e32 v2, v2
	s_nop 0
	v_mul_f32_e32 v2, 0x41800000, v2
	v_mul_f32_e32 v3, v38, v2
	s_nop 1
	v_mov_b32_dpp v5, v3 quad_perm:[1,0,3,2] row_mask:0xf bank_mask:0xf
	s_nop 1
	v_mov_b32_dpp v4, v3 quad_perm:[2,3,0,1] row_mask:0xf bank_mask:0xf
	s_waitcnt lgkmcnt(0)
	s_nop 1
	v_mov_b32_dpp v18, v5 quad_perm:[2,3,0,1] row_mask:0xf bank_mask:0xf
	s_and_saveexec_b64 s[42:43], s[6:7]
	s_cbranch_execz .LBB0_1430
	v_mov_b32_e32 v19, v147
	v_cvt_pk_fp8_f32 v19, v3, v5
	s_waitcnt lgkmcnt(0)
	v_cvt_pk_fp8_f32 v19, v4, v18 op_sel:[0,0,1]
	v_add_co_u32_e32 v4, vcc, 0x4000, v66
	s_nop 1
	v_addc_co_u32_e32 v5, vcc, 0, v67, vcc
	global_store_dword v[4:5], v19, off
.LBB0_1430:
	s_or_b64 exec, exec, s[42:43]
	v_mul_f32_e32 v3, v54, v2
	s_nop 1
	v_mov_b32_dpp v5, v3 quad_perm:[1,0,3,2] row_mask:0xf bank_mask:0xf
	s_waitcnt lgkmcnt(0)
	s_nop 1
	v_mov_b32_dpp v4, v3 quad_perm:[2,3,0,1] row_mask:0xf bank_mask:0xf
	s_waitcnt lgkmcnt(0)
	s_nop 1
	v_mov_b32_dpp v18, v5 quad_perm:[2,3,0,1] row_mask:0xf bank_mask:0xf
	s_and_saveexec_b64 s[42:43], s[6:7]
	s_cbranch_execz .LBB0_1432
	v_mov_b32_e32 v19, v147
	v_cvt_pk_fp8_f32 v19, v3, v5
	s_waitcnt lgkmcnt(0)
	v_cvt_pk_fp8_f32 v19, v4, v18 op_sel:[0,0,1]
	v_add_co_u32_e32 v4, vcc, 0x4000, v66
	s_nop 1
	v_addc_co_u32_e32 v5, vcc, 0, v67, vcc
	global_store_dword v[4:5], v19, off offset:32
.LBB0_1432:
	s_or_b64 exec, exec, s[42:43]
	v_mul_f32_e32 v3, v22, v2
	s_nop 1
	v_mov_b32_dpp v5, v3 quad_perm:[1,0,3,2] row_mask:0xf bank_mask:0xf
	s_waitcnt lgkmcnt(0)
	s_nop 1
	v_mov_b32_dpp v4, v3 quad_perm:[2,3,0,1] row_mask:0xf bank_mask:0xf
	s_waitcnt lgkmcnt(0)
	s_nop 1
	v_mov_b32_dpp v18, v5 quad_perm:[2,3,0,1] row_mask:0xf bank_mask:0xf
	s_and_saveexec_b64 s[42:43], s[6:7]
	s_cbranch_execz .LBB0_1434
	v_mov_b32_e32 v19, v147
	v_cvt_pk_fp8_f32 v19, v3, v5
	s_waitcnt lgkmcnt(0)
	v_cvt_pk_fp8_f32 v19, v4, v18 op_sel:[0,0,1]
	v_add_co_u32_e32 v4, vcc, 0x4000, v66
	s_nop 1
	v_addc_co_u32_e32 v5, vcc, 0, v67, vcc
	global_store_dword v[4:5], v19, off offset:64
.LBB0_1434:
	s_or_b64 exec, exec, s[42:43]
	v_mul_f32_e32 v2, v6, v2
	s_waitcnt lgkmcnt(0)
	s_nop 1
	v_mov_b32_dpp v4, v2 quad_perm:[1,0,3,2] row_mask:0xf bank_mask:0xf
	s_nop 1
	v_mov_b32_dpp v3, v2 quad_perm:[2,3,0,1] row_mask:0xf bank_mask:0xf
	s_waitcnt lgkmcnt(0)
	s_nop 1
	v_mov_b32_dpp v5, v4 quad_perm:[2,3,0,1] row_mask:0xf bank_mask:0xf
	s_and_saveexec_b64 s[42:43], s[6:7]
	s_cbranch_execz .LBB0_1436
	v_mov_b32_e32 v6, v147
	v_cvt_pk_fp8_f32 v6, v2, v4
	v_add_co_u32_e32 v2, vcc, 0x4000, v66
	s_waitcnt lgkmcnt(0)
	v_cvt_pk_fp8_f32 v6, v3, v5 op_sel:[0,0,1]
	v_addc_co_u32_e32 v3, vcc, 0, v67, vcc
	global_store_dword v[2:3], v6, off offset:96
.LBB0_1436:
	s_or_b64 exec, exec, s[42:43]
	ds_read_b32 v2, v167 offset:36
	s_waitcnt lgkmcnt(0)
	v_rcp_f32_e32 v2, v2
	s_nop 0
	v_mul_f32_e32 v2, 0x41800000, v2
	v_mul_f32_e32 v3, v39, v2
	s_nop 1
	v_mov_b32_dpp v5, v3 quad_perm:[1,0,3,2] row_mask:0xf bank_mask:0xf
	s_nop 1
	v_mov_b32_dpp v4, v3 quad_perm:[2,3,0,1] row_mask:0xf bank_mask:0xf
	s_waitcnt lgkmcnt(0)
	s_nop 1
	v_mov_b32_dpp v6, v5 quad_perm:[2,3,0,1] row_mask:0xf bank_mask:0xf
	s_and_saveexec_b64 s[42:43], s[6:7]
	s_cbranch_execz .LBB0_1438
	v_mov_b32_e32 v18, v147
	v_cvt_pk_fp8_f32 v18, v3, v5
	s_waitcnt lgkmcnt(0)
	v_cvt_pk_fp8_f32 v18, v4, v6 op_sel:[0,0,1]
	v_add_co_u32_e32 v4, vcc, 0x4000, v66
	s_nop 1
	v_addc_co_u32_e32 v5, vcc, 0, v67, vcc
	global_store_dword v[4:5], v18, off offset:2048
.LBB0_1438:
	s_or_b64 exec, exec, s[42:43]
	v_mul_f32_e32 v3, v55, v2
	s_nop 1
	v_mov_b32_dpp v5, v3 quad_perm:[1,0,3,2] row_mask:0xf bank_mask:0xf
	s_waitcnt lgkmcnt(0)
	s_nop 1
	v_mov_b32_dpp v4, v3 quad_perm:[2,3,0,1] row_mask:0xf bank_mask:0xf
	s_waitcnt lgkmcnt(0)
	s_nop 1
	v_mov_b32_dpp v6, v5 quad_perm:[2,3,0,1] row_mask:0xf bank_mask:0xf
	s_and_saveexec_b64 s[42:43], s[6:7]
	s_cbranch_execz .LBB0_1440
	v_mov_b32_e32 v18, v147
	v_cvt_pk_fp8_f32 v18, v3, v5
	s_waitcnt lgkmcnt(0)
	v_cvt_pk_fp8_f32 v18, v4, v6 op_sel:[0,0,1]
	v_add_co_u32_e32 v4, vcc, 0x4000, v66
	s_nop 1
	v_addc_co_u32_e32 v5, vcc, 0, v67, vcc
	global_store_dword v[4:5], v18, off offset:2080
.LBB0_1440:
	s_or_b64 exec, exec, s[42:43]
	v_mul_f32_e32 v3, v23, v2
	s_nop 1
	v_mov_b32_dpp v5, v3 quad_perm:[1,0,3,2] row_mask:0xf bank_mask:0xf
	s_waitcnt lgkmcnt(0)
	s_nop 1
	v_mov_b32_dpp v4, v3 quad_perm:[2,3,0,1] row_mask:0xf bank_mask:0xf
	s_waitcnt lgkmcnt(0)
	s_nop 1
	v_mov_b32_dpp v6, v5 quad_perm:[2,3,0,1] row_mask:0xf bank_mask:0xf
	s_and_saveexec_b64 s[42:43], s[6:7]
	s_cbranch_execz .LBB0_1442
	v_mov_b32_e32 v18, v147
	v_cvt_pk_fp8_f32 v18, v3, v5
	s_waitcnt lgkmcnt(0)
	v_cvt_pk_fp8_f32 v18, v4, v6 op_sel:[0,0,1]
	v_add_co_u32_e32 v4, vcc, 0x4000, v66
	s_nop 1
	v_addc_co_u32_e32 v5, vcc, 0, v67, vcc
	global_store_dword v[4:5], v18, off offset:2112
.LBB0_1442:
	s_or_b64 exec, exec, s[42:43]
	v_mul_f32_e32 v2, v7, v2
	s_waitcnt lgkmcnt(0)
	s_nop 1
	v_mov_b32_dpp v4, v2 quad_perm:[1,0,3,2] row_mask:0xf bank_mask:0xf
	s_nop 1
	v_mov_b32_dpp v3, v2 quad_perm:[2,3,0,1] row_mask:0xf bank_mask:0xf
	s_waitcnt lgkmcnt(0)
	s_nop 1
	v_mov_b32_dpp v5, v4 quad_perm:[2,3,0,1] row_mask:0xf bank_mask:0xf
	s_and_saveexec_b64 s[42:43], s[6:7]
	s_cbranch_execz .LBB0_1444
	v_mov_b32_e32 v6, v147
	v_cvt_pk_fp8_f32 v6, v2, v4
	v_add_co_u32_e32 v2, vcc, 0x4000, v66
	s_waitcnt lgkmcnt(0)
	v_cvt_pk_fp8_f32 v6, v3, v5 op_sel:[0,0,1]
	v_addc_co_u32_e32 v3, vcc, 0, v67, vcc
	global_store_dword v[2:3], v6, off offset:2144
; #define LDS_WAIT() asm volatile("s_waitcnt lgkmcnt(0)" ::: "memory")
; __device__ __forceinline__ unsigned cvt4_fp8(float a, float b, float c, float d) { int w = 0; w = __builtin_amdgcn_cvt_pk_fp8_f32(a, b, w, false); w = __builtin_amdgcn_cvt_pk_fp8_f32(c, d, w, true); return (unsigned)w; }
; template <bool MLA>
; __device__ __forceinline__ void attn_unit(char* lds, int h, int qb, const bf16_t* Qp, int ldq, const bf16_t* Kp, int ldk, const bf16_t* KRp, const bf16_t* Vp, int ldv,
;                                           unsigned char* Op, int ldo, const float* KMp, const float* rel_bias) {
;     ...
;     if (hi == 0) li_l[r32] = l_reg; LDS_WAIT();
;     unsigned char* Ow = Op + (size_t)qlo * ldo;
; #pragma unroll
;     for (int r = 0; r < 16; ++r) { const int orow = CROWC(r) + 4 * hi; const float rl = 16.0f * __builtin_amdgcn_rcpf(li_h[CROWC(r)]);
; #pragma unroll
;         for (int d0 = 0; d0 < 4; ++d0) { const float v = o[d0][r] * rl; const float v1 = __shfl_xor(v, 1), v2 = __shfl_xor(v, 2), v3 = __shfl_xor(v1, 2);
;             if ((r32 & 3) == 0) *(unsigned*)(Ow + (size_t)orow * ldo + d0 * 32 + r32) = cvt4_fp8(v, v1, v2, v3); } }
.LBB0_1444:
	s_or_b64 exec, exec, s[42:43]
	ds_read_b32 v2, v167 offset:40
	s_waitcnt lgkmcnt(0)
	v_rcp_f32_e32 v2, v2
	s_nop 0
	v_mul_f32_e32 v2, 0x41800000, v2
	v_mul_f32_e32 v3, v40, v2
	s_nop 1
	v_mov_b32_dpp v5, v3 quad_perm:[1,0,3,2] row_mask:0xf bank_mask:0xf
	s_nop 1
	v_mov_b32_dpp v4, v3 quad_perm:[2,3,0,1] row_mask:0xf bank_mask:0xf
	s_waitcnt lgkmcnt(0)
	s_nop 1
	v_mov_b32_dpp v6, v5 quad_perm:[2,3,0,1] row_mask:0xf bank_mask:0xf
	s_and_saveexec_b64 s[42:43], s[6:7]
	s_cbranch_execz .LBB0_1446
	v_mov_b32_e32 v7, v147
	v_cvt_pk_fp8_f32 v7, v3, v5
	s_waitcnt lgkmcnt(0)
	v_cvt_pk_fp8_f32 v7, v4, v6 op_sel:[0,0,1]
	v_add_co_u32_e32 v4, vcc, 0x5000, v66
	s_nop 1
	v_addc_co_u32_e32 v5, vcc, 0, v67, vcc
	global_store_dword v[4:5], v7, off
.LBB0_1446:
	s_or_b64 exec, exec, s[42:43]
	v_mul_f32_e32 v3, v56, v2
	s_nop 1
	v_mov_b32_dpp v5, v3 quad_perm:[1,0,3,2] row_mask:0xf bank_mask:0xf
	s_waitcnt lgkmcnt(0)
	s_nop 1
	v_mov_b32_dpp v4, v3 quad_perm:[2,3,0,1] row_mask:0xf bank_mask:0xf
	s_waitcnt lgkmcnt(0)
	s_nop 1
	v_mov_b32_dpp v6, v5 quad_perm:[2,3,0,1] row_mask:0xf bank_mask:0xf
	s_and_saveexec_b64 s[42:43], s[6:7]
	s_cbranch_execz .LBB0_1448
	v_mov_b32_e32 v7, v147
	v_cvt_pk_fp8_f32 v7, v3, v5
	s_waitcnt lgkmcnt(0)
	v_cvt_pk_fp8_f32 v7, v4, v6 op_sel:[0,0,1]
	v_add_co_u32_e32 v4, vcc, 0x5000, v66
	s_nop 1
	v_addc_co_u32_e32 v5, vcc, 0, v67, vcc
	global_store_dword v[4:5], v7, off offset:32
.LBB0_1448:
	s_or_b64 exec, exec, s[42:43]
	v_mul_f32_e32 v3, v24, v2
	s_nop 1
	v_mov_b32_dpp v5, v3 quad_perm:[1,0,3,2] row_mask:0xf bank_mask:0xf
	s_waitcnt lgkmcnt(0)
	s_nop 1
	v_mov_b32_dpp v4, v3 quad_perm:[2,3,0,1] row_mask:0xf bank_mask:0xf
	s_waitcnt lgkmcnt(0)
	s_nop 1
	v_mov_b32_dpp v6, v5 quad_perm:[2,3,0,1] row_mask:0xf bank_mask:0xf
	s_and_saveexec_b64 s[42:43], s[6:7]
	s_cbranch_execz .LBB0_1450
	v_mov_b32_e32 v7, v147
	v_cvt_pk_fp8_f32 v7, v3, v5
	s_waitcnt lgkmcnt(0)
	v_cvt_pk_fp8_f32 v7, v4, v6 op_sel:[0,0,1]
	v_add_co_u32_e32 v4, vcc, 0x5000, v66
	s_nop 1
	v_addc_co_u32_e32 v5, vcc, 0, v67, vcc
	global_store_dword v[4:5], v7, off offset:64
.LBB0_1450:
	s_or_b64 exec, exec, s[42:43]
	v_mul_f32_e32 v2, v8, v2
	s_waitcnt lgkmcnt(0)
	s_nop 1
	v_mov_b32_dpp v4, v2 quad_perm:[1,0,3,2] row_mask:0xf bank_mask:0xf
	s_nop 1
	v_mov_b32_dpp v3, v2 quad_perm:[2,3,0,1] row_mask:0xf bank_mask:0xf
	s_waitcnt lgkmcnt(0)
	s_nop 1
	v_mov_b32_dpp v5, v4 quad_perm:[2,3,0,1] row_mask:0xf bank_mask:0xf
	s_and_saveexec_b64 s[42:43], s[6:7]
	s_cbranch_execz .LBB0_1452
	v_mov_b32_e32 v6, v147
	v_cvt_pk_fp8_f32 v6, v2, v4
	v_add_co_u32_e32 v2, vcc, 0x5000, v66
	s_waitcnt lgkmcnt(0)
	v_cvt_pk_fp8_f32 v6, v3, v5 op_sel:[0,0,1]
	v_addc_co_u32_e32 v3, vcc, 0, v67, vcc
	global_store_dword v[2:3], v6, off offset:96
.LBB0_1452:
	s_or_b64 exec, exec, s[42:43]
	ds_read_b32 v2, v167 offset:44
	s_waitcnt lgkmcnt(0)
	v_rcp_f32_e32 v2, v2
	s_nop 0
	v_mul_f32_e32 v2, 0x41800000, v2
	v_mul_f32_e32 v3, v41, v2
	s_nop 1
	v_mov_b32_dpp v5, v3 quad_perm:[1,0,3,2] row_mask:0xf bank_mask:0xf
	s_nop 1
	v_mov_b32_dpp v4, v3 quad_perm:[2,3,0,1] row_mask:0xf bank_mask:0xf
	s_waitcnt lgkmcnt(0)
	s_nop 1
	v_mov_b32_dpp v6, v5 quad_perm:[2,3,0,1] row_mask:0xf bank_mask:0xf
	s_and_saveexec_b64 s[42:43], s[6:7]
	s_cbranch_execz .LBB0_1454
	v_mov_b32_e32 v7, v147
	v_cvt_pk_fp8_f32 v7, v3, v5
	s_waitcnt lgkmcnt(0)
	v_cvt_pk_fp8_f32 v7, v4, v6 op_sel:[0,0,1]
	v_add_co_u32_e32 v4, vcc, 0x5000, v66
	s_nop 1
	v_addc_co_u32_e32 v5, vcc, 0, v67, vcc
	global_store_dword v[4:5], v7, off offset:2048
.LBB0_1454:
	s_or_b64 exec, exec, s[42:43]
	v_mul_f32_e32 v3, v57, v2
	s_nop 1
	v_mov_b32_dpp v5, v3 quad_perm:[1,0,3,2] row_mask:0xf bank_mask:0xf
	s_waitcnt lgkmcnt(0)
	s_nop 1
	v_mov_b32_dpp v4, v3 quad_perm:[2,3,0,1] row_mask:0xf bank_mask:0xf
	s_waitcnt lgkmcnt(0)
	s_nop 1
	v_mov_b32_dpp v6, v5 quad_perm:[2,3,0,1] row_mask:0xf bank_mask:0xf
	s_and_saveexec_b64 s[42:43], s[6:7]
	s_cbranch_execz .LBB0_1456
	v_mov_b32_e32 v7, v147
	v_cvt_pk_fp8_f32 v7, v3, v5
	s_waitcnt lgkmcnt(0)
	v_cvt_pk_fp8_f32 v7, v4, v6 op_sel:[0,0,1]
	v_add_co_u32_e32 v4, vcc, 0x5000, v66
	s_nop 1
	v_addc_co_u32_e32 v5, vcc, 0, v67, vcc
	global_store_dword v[4:5], v7, off offset:2080
.LBB0_1456:
	s_or_b64 exec, exec, s[42:43]
	v_mul_f32_e32 v3, v25, v2
	s_nop 1
	v_mov_b32_dpp v5, v3 quad_perm:[1,0,3,2] row_mask:0xf bank_mask:0xf
	s_waitcnt lgkmcnt(0)
	s_nop 1
	v_mov_b32_dpp v4, v3 quad_perm:[2,3,0,1] row_mask:0xf bank_mask:0xf
	s_waitcnt lgkmcnt(0)
	s_nop 1
	v_mov_b32_dpp v6, v5 quad_perm:[2,3,0,1] row_mask:0xf bank_mask:0xf
	s_and_saveexec_b64 s[42:43], s[6:7]
	s_cbranch_execz .LBB0_1458
	v_mov_b32_e32 v7, v147
	v_cvt_pk_fp8_f32 v7, v3, v5
	s_waitcnt lgkmcnt(0)
	v_cvt_pk_fp8_f32 v7, v4, v6 op_sel:[0,0,1]
	v_add_co_u32_e32 v4, vcc, 0x5000, v66
	s_nop 1
	v_addc_co_u32_e32 v5, vcc, 0, v67, vcc
	global_store_dword v[4:5], v7, off offset:2112
.LBB0_1458:
	s_or_b64 exec, exec, s[42:43]
	v_mul_f32_e32 v2, v9, v2
	s_waitcnt lgkmcnt(0)
	s_nop 1
	v_mov_b32_dpp v4, v2 quad_perm:[1,0,3,2] row_mask:0xf bank_mask:0xf
	s_nop 1
	v_mov_b32_dpp v3, v2 quad_perm:[2,3,0,1] row_mask:0xf bank_mask:0xf
	s_waitcnt lgkmcnt(0)
	s_nop 1
	v_mov_b32_dpp v5, v4 quad_perm:[2,3,0,1] row_mask:0xf bank_mask:0xf
	s_and_saveexec_b64 s[42:43], s[6:7]
	s_cbranch_execz .LBB0_1460
	v_mov_b32_e32 v6, v147
	v_cvt_pk_fp8_f32 v6, v2, v4
	v_add_co_u32_e32 v2, vcc, 0x5000, v66
	s_waitcnt lgkmcnt(0)
	v_cvt_pk_fp8_f32 v6, v3, v5 op_sel:[0,0,1]
	v_addc_co_u32_e32 v3, vcc, 0, v67, vcc
	global_store_dword v[2:3], v6, off offset:2144
; #define LDS_WAIT() asm volatile("s_waitcnt lgkmcnt(0)" ::: "memory")
; __device__ __forceinline__ unsigned cvt4_fp8(float a, float b, float c, float d) { int w = 0; w = __builtin_amdgcn_cvt_pk_fp8_f32(a, b, w, false); w = __builtin_amdgcn_cvt_pk_fp8_f32(c, d, w, true); return (unsigned)w; }
; template <bool MLA>
; __device__ __forceinline__ void attn_unit(char* lds, int h, int qb, const bf16_t* Qp, int ldq, const bf16_t* Kp, int ldk, const bf16_t* KRp, const bf16_t* Vp, int ldv,
;                                           unsigned char* Op, int ldo, const float* KMp, const float* rel_bias) {
;     ...
;     if (hi == 0) li_l[r32] = l_reg; LDS_WAIT();
;     unsigned char* Ow = Op + (size_t)qlo * ldo;
; #pragma unroll
;     for (int r = 0; r < 16; ++r) { const int orow = CROWC(r) + 4 * hi; const float rl = 16.0f * __builtin_amdgcn_rcpf(li_h[CROWC(r)]);
; #pragma unroll
;         for (int d0 = 0; d0 < 4; ++d0) { const float v = o[d0][r] * rl; const float v1 = __shfl_xor(v, 1), v2 = __shfl_xor(v, 2), v3 = __shfl_xor(v1, 2);
;             if ((r32 & 3) == 0) *(unsigned*)(Ow + (size_t)orow * ldo + d0 * 32 + r32) = cvt4_fp8(v, v1, v2, v3); } }
.LBB0_1460:
	s_or_b64 exec, exec, s[42:43]
	ds_read_b32 v2, v167 offset:64
	s_waitcnt lgkmcnt(0)
	v_rcp_f32_e32 v2, v2
	s_nop 0
	v_mul_f32_e32 v2, 0x41800000, v2
	v_mul_f32_e32 v3, v42, v2
	s_nop 1
	v_mov_b32_dpp v5, v3 quad_perm:[1,0,3,2] row_mask:0xf bank_mask:0xf
	s_nop 1
	v_mov_b32_dpp v4, v3 quad_perm:[2,3,0,1] row_mask:0xf bank_mask:0xf
	s_waitcnt lgkmcnt(0)
	s_nop 1
	v_mov_b32_dpp v6, v5 quad_perm:[2,3,0,1] row_mask:0xf bank_mask:0xf
	s_and_saveexec_b64 s[42:43], s[6:7]
	s_cbranch_execz .LBB0_1462
	v_mov_b32_e32 v7, v147
	v_cvt_pk_fp8_f32 v7, v3, v5
	s_waitcnt lgkmcnt(0)
	v_cvt_pk_fp8_f32 v7, v4, v6 op_sel:[0,0,1]
	v_add_co_u32_e32 v4, vcc, 0x8000, v66
	s_nop 1
	v_addc_co_u32_e32 v5, vcc, 0, v67, vcc
	global_store_dword v[4:5], v7, off
.LBB0_1462:
	s_or_b64 exec, exec, s[42:43]
	v_mul_f32_e32 v3, v58, v2
	s_nop 1
	v_mov_b32_dpp v5, v3 quad_perm:[1,0,3,2] row_mask:0xf bank_mask:0xf
	s_waitcnt lgkmcnt(0)
	s_nop 1
	v_mov_b32_dpp v4, v3 quad_perm:[2,3,0,1] row_mask:0xf bank_mask:0xf
	s_waitcnt lgkmcnt(0)
	s_nop 1
	v_mov_b32_dpp v6, v5 quad_perm:[2,3,0,1] row_mask:0xf bank_mask:0xf
	s_and_saveexec_b64 s[42:43], s[6:7]
	s_cbranch_execz .LBB0_1464
	v_mov_b32_e32 v7, v147
	v_cvt_pk_fp8_f32 v7, v3, v5
	s_waitcnt lgkmcnt(0)
	v_cvt_pk_fp8_f32 v7, v4, v6 op_sel:[0,0,1]
	v_add_co_u32_e32 v4, vcc, 0x8000, v66
	s_nop 1
	v_addc_co_u32_e32 v5, vcc, 0, v67, vcc
	global_store_dword v[4:5], v7, off offset:32
.LBB0_1464:
	s_or_b64 exec, exec, s[42:43]
	v_mul_f32_e32 v3, v26, v2
	s_nop 1
	v_mov_b32_dpp v5, v3 quad_perm:[1,0,3,2] row_mask:0xf bank_mask:0xf
	s_waitcnt lgkmcnt(0)
	s_nop 1
	v_mov_b32_dpp v4, v3 quad_perm:[2,3,0,1] row_mask:0xf bank_mask:0xf
	s_waitcnt lgkmcnt(0)
	s_nop 1
	v_mov_b32_dpp v6, v5 quad_perm:[2,3,0,1] row_mask:0xf bank_mask:0xf
	s_and_saveexec_b64 s[42:43], s[6:7]
	s_cbranch_execz .LBB0_1466
	v_mov_b32_e32 v7, v147
	v_cvt_pk_fp8_f32 v7, v3, v5
	s_waitcnt lgkmcnt(0)
	v_cvt_pk_fp8_f32 v7, v4, v6 op_sel:[0,0,1]
	v_add_co_u32_e32 v4, vcc, 0x8000, v66
	s_nop 1
	v_addc_co_u32_e32 v5, vcc, 0, v67, vcc
	global_store_dword v[4:5], v7, off offset:64
.LBB0_1466:
	s_or_b64 exec, exec, s[42:43]
	v_mul_f32_e32 v2, v10, v2
	s_waitcnt lgkmcnt(0)
	s_nop 1
	v_mov_b32_dpp v4, v2 quad_perm:[1,0,3,2] row_mask:0xf bank_mask:0xf
	s_nop 1
	v_mov_b32_dpp v3, v2 quad_perm:[2,3,0,1] row_mask:0xf bank_mask:0xf
	s_waitcnt lgkmcnt(0)
	s_nop 1
	v_mov_b32_dpp v5, v4 quad_perm:[2,3,0,1] row_mask:0xf bank_mask:0xf
	s_and_saveexec_b64 s[42:43], s[6:7]
	s_cbranch_execz .LBB0_1468
	v_mov_b32_e32 v6, v147
	v_cvt_pk_fp8_f32 v6, v2, v4
	v_add_co_u32_e32 v2, vcc, 0x8000, v66
	s_waitcnt lgkmcnt(0)
	v_cvt_pk_fp8_f32 v6, v3, v5 op_sel:[0,0,1]
	v_addc_co_u32_e32 v3, vcc, 0, v67, vcc
	global_store_dword v[2:3], v6, off offset:96
.LBB0_1468:
	s_or_b64 exec, exec, s[42:43]
	ds_read_b32 v2, v167 offset:68
	s_waitcnt lgkmcnt(0)
	v_rcp_f32_e32 v2, v2
	s_nop 0
	v_mul_f32_e32 v2, 0x41800000, v2
	v_mul_f32_e32 v3, v43, v2
	s_nop 1
	v_mov_b32_dpp v5, v3 quad_perm:[1,0,3,2] row_mask:0xf bank_mask:0xf
	s_nop 1
	v_mov_b32_dpp v4, v3 quad_perm:[2,3,0,1] row_mask:0xf bank_mask:0xf
	s_waitcnt lgkmcnt(0)
	s_nop 1
	v_mov_b32_dpp v6, v5 quad_perm:[2,3,0,1] row_mask:0xf bank_mask:0xf
	s_and_saveexec_b64 s[42:43], s[6:7]
	s_cbranch_execz .LBB0_1470
	v_mov_b32_e32 v7, v147
	v_cvt_pk_fp8_f32 v7, v3, v5
	s_waitcnt lgkmcnt(0)
	v_cvt_pk_fp8_f32 v7, v4, v6 op_sel:[0,0,1]
	v_add_co_u32_e32 v4, vcc, 0x8000, v66
	s_nop 1
	v_addc_co_u32_e32 v5, vcc, 0, v67, vcc
	global_store_dword v[4:5], v7, off offset:2048
.LBB0_1470:
	s_or_b64 exec, exec, s[42:43]
	v_mul_f32_e32 v3, v59, v2
	s_nop 1
	v_mov_b32_dpp v5, v3 quad_perm:[1,0,3,2] row_mask:0xf bank_mask:0xf
	s_waitcnt lgkmcnt(0)
	s_nop 1
	v_mov_b32_dpp v4, v3 quad_perm:[2,3,0,1] row_mask:0xf bank_mask:0xf
	s_waitcnt lgkmcnt(0)
	s_nop 1
	v_mov_b32_dpp v6, v5 quad_perm:[2,3,0,1] row_mask:0xf bank_mask:0xf
	s_and_saveexec_b64 s[42:43], s[6:7]
	s_cbranch_execz .LBB0_1472
	v_mov_b32_e32 v7, v147
	v_cvt_pk_fp8_f32 v7, v3, v5
	s_waitcnt lgkmcnt(0)
	v_cvt_pk_fp8_f32 v7, v4, v6 op_sel:[0,0,1]
	v_add_co_u32_e32 v4, vcc, 0x8000, v66
	s_nop 1
	v_addc_co_u32_e32 v5, vcc, 0, v67, vcc
	global_store_dword v[4:5], v7, off offset:2080
.LBB0_1472:
	s_or_b64 exec, exec, s[42:43]
	v_mul_f32_e32 v3, v27, v2
	s_nop 1
	v_mov_b32_dpp v5, v3 quad_perm:[1,0,3,2] row_mask:0xf bank_mask:0xf
	s_waitcnt lgkmcnt(0)
	s_nop 1
	v_mov_b32_dpp v4, v3 quad_perm:[2,3,0,1] row_mask:0xf bank_mask:0xf
	s_waitcnt lgkmcnt(0)
	s_nop 1
	v_mov_b32_dpp v6, v5 quad_perm:[2,3,0,1] row_mask:0xf bank_mask:0xf
	s_and_saveexec_b64 s[42:43], s[6:7]
	s_cbranch_execz .LBB0_1474
	v_mov_b32_e32 v7, v147
	v_cvt_pk_fp8_f32 v7, v3, v5
	s_waitcnt lgkmcnt(0)
	v_cvt_pk_fp8_f32 v7, v4, v6 op_sel:[0,0,1]
	v_add_co_u32_e32 v4, vcc, 0x8000, v66
	s_nop 1
	v_addc_co_u32_e32 v5, vcc, 0, v67, vcc
	global_store_dword v[4:5], v7, off offset:2112
.LBB0_1474:
	s_or_b64 exec, exec, s[42:43]
	v_mul_f32_e32 v2, v11, v2
	s_waitcnt lgkmcnt(0)
	s_nop 1
	v_mov_b32_dpp v4, v2 quad_perm:[1,0,3,2] row_mask:0xf bank_mask:0xf
	s_nop 1
	v_mov_b32_dpp v3, v2 quad_perm:[2,3,0,1] row_mask:0xf bank_mask:0xf
	s_waitcnt lgkmcnt(0)
	s_nop 1
	v_mov_b32_dpp v5, v4 quad_perm:[2,3,0,1] row_mask:0xf bank_mask:0xf
	s_and_saveexec_b64 s[42:43], s[6:7]
	s_cbranch_execz .LBB0_1476
	v_mov_b32_e32 v6, v147
	v_cvt_pk_fp8_f32 v6, v2, v4
	v_add_co_u32_e32 v2, vcc, 0x8000, v66
	s_waitcnt lgkmcnt(0)
	v_cvt_pk_fp8_f32 v6, v3, v5 op_sel:[0,0,1]
	v_addc_co_u32_e32 v3, vcc, 0, v67, vcc
	global_store_dword v[2:3], v6, off offset:2144
; #define LDS_WAIT() asm volatile("s_waitcnt lgkmcnt(0)" ::: "memory")
; __device__ __forceinline__ unsigned cvt4_fp8(float a, float b, float c, float d) { int w = 0; w = __builtin_amdgcn_cvt_pk_fp8_f32(a, b, w, false); w = __builtin_amdgcn_cvt_pk_fp8_f32(c, d, w, true); return (unsigned)w; }
; template <bool MLA>
; __device__ __forceinline__ void attn_unit(char* lds, int h, int qb, const bf16_t* Qp, int ldq, const bf16_t* Kp, int ldk, const bf16_t* KRp, const bf16_t* Vp, int ldv,
;                                           unsigned char* Op, int ldo, const float* KMp, const float* rel_bias) {
;     ...
;     if (hi == 0) li_l[r32] = l_reg; LDS_WAIT();
;     unsigned char* Ow = Op + (size_t)qlo * ldo;
; #pragma unroll
;     for (int r = 0; r < 16; ++r) { const int orow = CROWC(r) + 4 * hi; const float rl = 16.0f * __builtin_amdgcn_rcpf(li_h[CROWC(r)]);
; #pragma unroll
;         for (int d0 = 0; d0 < 4; ++d0) { const float v = o[d0][r] * rl; const float v1 = __shfl_xor(v, 1), v2 = __shfl_xor(v, 2), v3 = __shfl_xor(v1, 2);
;             if ((r32 & 3) == 0) *(unsigned*)(Ow + (size_t)orow * ldo + d0 * 32 + r32) = cvt4_fp8(v, v1, v2, v3); } }
.LBB0_1476:
	s_or_b64 exec, exec, s[42:43]
	ds_read_b32 v2, v167 offset:72
	s_waitcnt lgkmcnt(0)
	v_rcp_f32_e32 v2, v2
	s_nop 0
	v_mul_f32_e32 v2, 0x41800000, v2
	v_mul_f32_e32 v3, v44, v2
	s_nop 1
	v_mov_b32_dpp v5, v3 quad_perm:[1,0,3,2] row_mask:0xf bank_mask:0xf
	s_nop 1
	v_mov_b32_dpp v4, v3 quad_perm:[2,3,0,1] row_mask:0xf bank_mask:0xf
	s_waitcnt lgkmcnt(0)
	s_nop 1
	v_mov_b32_dpp v6, v5 quad_perm:[2,3,0,1] row_mask:0xf bank_mask:0xf
	s_and_saveexec_b64 s[42:43], s[6:7]
	s_cbranch_execz .LBB0_1478
	v_mov_b32_e32 v7, v147
	v_cvt_pk_fp8_f32 v7, v3, v5
	s_waitcnt lgkmcnt(0)
	v_cvt_pk_fp8_f32 v7, v4, v6 op_sel:[0,0,1]
	v_add_co_u32_e32 v4, vcc, 0x9000, v66
	s_nop 1
	v_addc_co_u32_e32 v5, vcc, 0, v67, vcc
	global_store_dword v[4:5], v7, off
.LBB0_1478:
	s_or_b64 exec, exec, s[42:43]
	v_mul_f32_e32 v3, v60, v2
	s_nop 1
	v_mov_b32_dpp v5, v3 quad_perm:[1,0,3,2] row_mask:0xf bank_mask:0xf
	s_waitcnt lgkmcnt(0)
	s_nop 1
	v_mov_b32_dpp v4, v3 quad_perm:[2,3,0,1] row_mask:0xf bank_mask:0xf
	s_waitcnt lgkmcnt(0)
	s_nop 1
	v_mov_b32_dpp v6, v5 quad_perm:[2,3,0,1] row_mask:0xf bank_mask:0xf
	s_and_saveexec_b64 s[42:43], s[6:7]
	s_cbranch_execz .LBB0_1480
	v_mov_b32_e32 v7, v147
	v_cvt_pk_fp8_f32 v7, v3, v5
	s_waitcnt lgkmcnt(0)
	v_cvt_pk_fp8_f32 v7, v4, v6 op_sel:[0,0,1]
	v_add_co_u32_e32 v4, vcc, 0x9000, v66
	s_nop 1
	v_addc_co_u32_e32 v5, vcc, 0, v67, vcc
	global_store_dword v[4:5], v7, off offset:32
.LBB0_1480:
	s_or_b64 exec, exec, s[42:43]
	v_mul_f32_e32 v3, v28, v2
	s_nop 1
	v_mov_b32_dpp v5, v3 quad_perm:[1,0,3,2] row_mask:0xf bank_mask:0xf
	s_waitcnt lgkmcnt(0)
	s_nop 1
	v_mov_b32_dpp v4, v3 quad_perm:[2,3,0,1] row_mask:0xf bank_mask:0xf
	s_waitcnt lgkmcnt(0)
	s_nop 1
	v_mov_b32_dpp v6, v5 quad_perm:[2,3,0,1] row_mask:0xf bank_mask:0xf
	s_and_saveexec_b64 s[42:43], s[6:7]
	s_cbranch_execz .LBB0_1482
	v_mov_b32_e32 v7, v147
	v_cvt_pk_fp8_f32 v7, v3, v5
	s_waitcnt lgkmcnt(0)
	v_cvt_pk_fp8_f32 v7, v4, v6 op_sel:[0,0,1]
	v_add_co_u32_e32 v4, vcc, 0x9000, v66
	s_nop 1
	v_addc_co_u32_e32 v5, vcc, 0, v67, vcc
	global_store_dword v[4:5], v7, off offset:64
.LBB0_1482:
	s_or_b64 exec, exec, s[42:43]
	v_mul_f32_e32 v2, v12, v2
	s_waitcnt lgkmcnt(0)
	s_nop 1
	v_mov_b32_dpp v4, v2 quad_perm:[1,0,3,2] row_mask:0xf bank_mask:0xf
	s_nop 1
	v_mov_b32_dpp v3, v2 quad_perm:[2,3,0,1] row_mask:0xf bank_mask:0xf
	s_waitcnt lgkmcnt(0)
	s_nop 1
	v_mov_b32_dpp v5, v4 quad_perm:[2,3,0,1] row_mask:0xf bank_mask:0xf
	s_and_saveexec_b64 s[42:43], s[6:7]
	s_cbranch_execz .LBB0_1484
	v_mov_b32_e32 v6, v147
	v_cvt_pk_fp8_f32 v6, v2, v4
	v_add_co_u32_e32 v2, vcc, 0x9000, v66
	s_waitcnt lgkmcnt(0)
	v_cvt_pk_fp8_f32 v6, v3, v5 op_sel:[0,0,1]
	v_addc_co_u32_e32 v3, vcc, 0, v67, vcc
	global_store_dword v[2:3], v6, off offset:96
.LBB0_1484:
	s_or_b64 exec, exec, s[42:43]
	ds_read_b32 v2, v167 offset:76
	s_waitcnt lgkmcnt(0)
	v_rcp_f32_e32 v2, v2
	s_nop 0
	v_mul_f32_e32 v2, 0x41800000, v2
	v_mul_f32_e32 v3, v45, v2
	s_nop 1
	v_mov_b32_dpp v5, v3 quad_perm:[1,0,3,2] row_mask:0xf bank_mask:0xf
	s_nop 1
	v_mov_b32_dpp v4, v3 quad_perm:[2,3,0,1] row_mask:0xf bank_mask:0xf
	s_waitcnt lgkmcnt(0)
	s_nop 1
	v_mov_b32_dpp v6, v5 quad_perm:[2,3,0,1] row_mask:0xf bank_mask:0xf
	s_and_saveexec_b64 s[42:43], s[6:7]
	s_cbranch_execz .LBB0_1486
	v_mov_b32_e32 v7, v147
	v_cvt_pk_fp8_f32 v7, v3, v5
	s_waitcnt lgkmcnt(0)
	v_cvt_pk_fp8_f32 v7, v4, v6 op_sel:[0,0,1]
	v_add_co_u32_e32 v4, vcc, 0x9000, v66
	s_nop 1
	v_addc_co_u32_e32 v5, vcc, 0, v67, vcc
	global_store_dword v[4:5], v7, off offset:2048
.LBB0_1486:
	s_or_b64 exec, exec, s[42:43]
	v_mul_f32_e32 v3, v61, v2
	s_nop 1
	v_mov_b32_dpp v5, v3 quad_perm:[1,0,3,2] row_mask:0xf bank_mask:0xf
	s_waitcnt lgkmcnt(0)
	s_nop 1
	v_mov_b32_dpp v4, v3 quad_perm:[2,3,0,1] row_mask:0xf bank_mask:0xf
	s_waitcnt lgkmcnt(0)
	s_nop 1
	v_mov_b32_dpp v6, v5 quad_perm:[2,3,0,1] row_mask:0xf bank_mask:0xf
	s_and_saveexec_b64 s[42:43], s[6:7]
	s_cbranch_execz .LBB0_1488
	v_mov_b32_e32 v7, v147
	v_cvt_pk_fp8_f32 v7, v3, v5
	s_waitcnt lgkmcnt(0)
	v_cvt_pk_fp8_f32 v7, v4, v6 op_sel:[0,0,1]
	v_add_co_u32_e32 v4, vcc, 0x9000, v66
	s_nop 1
	v_addc_co_u32_e32 v5, vcc, 0, v67, vcc
	global_store_dword v[4:5], v7, off offset:2080
.LBB0_1488:
	s_or_b64 exec, exec, s[42:43]
	v_mul_f32_e32 v3, v29, v2
	s_nop 1
	v_mov_b32_dpp v5, v3 quad_perm:[1,0,3,2] row_mask:0xf bank_mask:0xf
	s_waitcnt lgkmcnt(0)
	s_nop 1
	v_mov_b32_dpp v4, v3 quad_perm:[2,3,0,1] row_mask:0xf bank_mask:0xf
	s_waitcnt lgkmcnt(0)
	s_nop 1
	v_mov_b32_dpp v6, v5 quad_perm:[2,3,0,1] row_mask:0xf bank_mask:0xf
	s_and_saveexec_b64 s[42:43], s[6:7]
	s_cbranch_execz .LBB0_1490
	v_mov_b32_e32 v7, v147
	v_cvt_pk_fp8_f32 v7, v3, v5
	s_waitcnt lgkmcnt(0)
	v_cvt_pk_fp8_f32 v7, v4, v6 op_sel:[0,0,1]
	v_add_co_u32_e32 v4, vcc, 0x9000, v66
	s_nop 1
	v_addc_co_u32_e32 v5, vcc, 0, v67, vcc
	global_store_dword v[4:5], v7, off offset:2112
.LBB0_1490:
	s_or_b64 exec, exec, s[42:43]
	v_mul_f32_e32 v2, v13, v2
	s_waitcnt lgkmcnt(0)
	s_nop 1
	v_mov_b32_dpp v4, v2 quad_perm:[1,0,3,2] row_mask:0xf bank_mask:0xf
	s_nop 1
	v_mov_b32_dpp v3, v2 quad_perm:[2,3,0,1] row_mask:0xf bank_mask:0xf
	s_waitcnt lgkmcnt(0)
	s_nop 1
	v_mov_b32_dpp v5, v4 quad_perm:[2,3,0,1] row_mask:0xf bank_mask:0xf
	s_and_saveexec_b64 s[42:43], s[6:7]
	s_cbranch_execz .LBB0_1492
	v_mov_b32_e32 v6, v147
	v_cvt_pk_fp8_f32 v6, v2, v4
	v_add_co_u32_e32 v2, vcc, 0x9000, v66
	s_waitcnt lgkmcnt(0)
	v_cvt_pk_fp8_f32 v6, v3, v5 op_sel:[0,0,1]
	v_addc_co_u32_e32 v3, vcc, 0, v67, vcc
	global_store_dword v[2:3], v6, off offset:2144
; #define LDS_WAIT() asm volatile("s_waitcnt lgkmcnt(0)" ::: "memory")
; __device__ __forceinline__ unsigned cvt4_fp8(float a, float b, float c, float d) { int w = 0; w = __builtin_amdgcn_cvt_pk_fp8_f32(a, b, w, false); w = __builtin_amdgcn_cvt_pk_fp8_f32(c, d, w, true); return (unsigned)w; }
; template <bool MLA>
; __device__ __forceinline__ void attn_unit(char* lds, int h, int qb, const bf16_t* Qp, int ldq, const bf16_t* Kp, int ldk, const bf16_t* KRp, const bf16_t* Vp, int ldv,
;                                           unsigned char* Op, int ldo, const float* KMp, const float* rel_bias) {
;     ...
;     if (hi == 0) li_l[r32] = l_reg; LDS_WAIT();
;     unsigned char* Ow = Op + (size_t)qlo * ldo;
; #pragma unroll
;     for (int r = 0; r < 16; ++r) { const int orow = CROWC(r) + 4 * hi; const float rl = 16.0f * __builtin_amdgcn_rcpf(li_h[CROWC(r)]);
; #pragma unroll
;         for (int d0 = 0; d0 < 4; ++d0) { const float v = o[d0][r] * rl; const float v1 = __shfl_xor(v, 1), v2 = __shfl_xor(v, 2), v3 = __shfl_xor(v1, 2);
;             if ((r32 & 3) == 0) *(unsigned*)(Ow + (size_t)orow * ldo + d0 * 32 + r32) = cvt4_fp8(v, v1, v2, v3); } }
.LBB0_1492:
	s_or_b64 exec, exec, s[42:43]
	ds_read_b32 v2, v167 offset:96
	s_waitcnt lgkmcnt(0)
	v_rcp_f32_e32 v2, v2
	s_nop 0
	v_mul_f32_e32 v2, 0x41800000, v2
	v_mul_f32_e32 v3, v46, v2
	s_nop 1
	v_mov_b32_dpp v5, v3 quad_perm:[1,0,3,2] row_mask:0xf bank_mask:0xf
	s_nop 1
	v_mov_b32_dpp v4, v3 quad_perm:[2,3,0,1] row_mask:0xf bank_mask:0xf
	s_waitcnt lgkmcnt(0)
	s_nop 1
	v_mov_b32_dpp v6, v5 quad_perm:[2,3,0,1] row_mask:0xf bank_mask:0xf
	s_and_saveexec_b64 s[42:43], s[6:7]
	s_cbranch_execz .LBB0_1494
	v_mov_b32_e32 v7, v147
	v_cvt_pk_fp8_f32 v7, v3, v5
	s_waitcnt lgkmcnt(0)
	v_cvt_pk_fp8_f32 v7, v4, v6 op_sel:[0,0,1]
	v_add_co_u32_e32 v4, vcc, 0xc000, v66
	s_nop 1
	v_addc_co_u32_e32 v5, vcc, 0, v67, vcc
	global_store_dword v[4:5], v7, off
.LBB0_1494:
	s_or_b64 exec, exec, s[42:43]
	v_mul_f32_e32 v3, v62, v2
	s_nop 1
	v_mov_b32_dpp v5, v3 quad_perm:[1,0,3,2] row_mask:0xf bank_mask:0xf
	s_waitcnt lgkmcnt(0)
	s_nop 1
	v_mov_b32_dpp v4, v3 quad_perm:[2,3,0,1] row_mask:0xf bank_mask:0xf
	s_waitcnt lgkmcnt(0)
	s_nop 1
	v_mov_b32_dpp v6, v5 quad_perm:[2,3,0,1] row_mask:0xf bank_mask:0xf
	s_and_saveexec_b64 s[42:43], s[6:7]
	s_cbranch_execz .LBB0_1496
	v_mov_b32_e32 v7, v147
	v_cvt_pk_fp8_f32 v7, v3, v5
	s_waitcnt lgkmcnt(0)
	v_cvt_pk_fp8_f32 v7, v4, v6 op_sel:[0,0,1]
	v_add_co_u32_e32 v4, vcc, 0xc000, v66
	s_nop 1
	v_addc_co_u32_e32 v5, vcc, 0, v67, vcc
	global_store_dword v[4:5], v7, off offset:32
.LBB0_1496:
	s_or_b64 exec, exec, s[42:43]
	v_mul_f32_e32 v3, v30, v2
	s_nop 1
	v_mov_b32_dpp v5, v3 quad_perm:[1,0,3,2] row_mask:0xf bank_mask:0xf
	s_waitcnt lgkmcnt(0)
	s_nop 1
	v_mov_b32_dpp v4, v3 quad_perm:[2,3,0,1] row_mask:0xf bank_mask:0xf
	s_waitcnt lgkmcnt(0)
	s_nop 1
	v_mov_b32_dpp v6, v5 quad_perm:[2,3,0,1] row_mask:0xf bank_mask:0xf
	s_and_saveexec_b64 s[42:43], s[6:7]
	s_cbranch_execz .LBB0_1498
	v_mov_b32_e32 v7, v147
	v_cvt_pk_fp8_f32 v7, v3, v5
	s_waitcnt lgkmcnt(0)
	v_cvt_pk_fp8_f32 v7, v4, v6 op_sel:[0,0,1]
	v_add_co_u32_e32 v4, vcc, 0xc000, v66
	s_nop 1
	v_addc_co_u32_e32 v5, vcc, 0, v67, vcc
	global_store_dword v[4:5], v7, off offset:64
.LBB0_1498:
	s_or_b64 exec, exec, s[42:43]
	v_mul_f32_e32 v2, v14, v2
	s_waitcnt lgkmcnt(0)
	s_nop 1
	v_mov_b32_dpp v4, v2 quad_perm:[1,0,3,2] row_mask:0xf bank_mask:0xf
	s_nop 1
	v_mov_b32_dpp v3, v2 quad_perm:[2,3,0,1] row_mask:0xf bank_mask:0xf
	s_waitcnt lgkmcnt(0)
	s_nop 1
	v_mov_b32_dpp v5, v4 quad_perm:[2,3,0,1] row_mask:0xf bank_mask:0xf
	s_and_saveexec_b64 s[42:43], s[6:7]
	s_cbranch_execz .LBB0_1500
	v_mov_b32_e32 v6, v147
	v_cvt_pk_fp8_f32 v6, v2, v4
	v_add_co_u32_e32 v2, vcc, 0xc000, v66
	s_waitcnt lgkmcnt(0)
	v_cvt_pk_fp8_f32 v6, v3, v5 op_sel:[0,0,1]
	v_addc_co_u32_e32 v3, vcc, 0, v67, vcc
	global_store_dword v[2:3], v6, off offset:96
.LBB0_1500:
	s_or_b64 exec, exec, s[42:43]
	ds_read_b32 v2, v167 offset:100
	s_waitcnt lgkmcnt(0)
	v_rcp_f32_e32 v2, v2
	s_nop 0
	v_mul_f32_e32 v2, 0x41800000, v2
	v_mul_f32_e32 v3, v47, v2
	s_nop 1
	v_mov_b32_dpp v5, v3 quad_perm:[1,0,3,2] row_mask:0xf bank_mask:0xf
	s_nop 1
	v_mov_b32_dpp v4, v3 quad_perm:[2,3,0,1] row_mask:0xf bank_mask:0xf
	s_waitcnt lgkmcnt(0)
	s_nop 1
	v_mov_b32_dpp v6, v5 quad_perm:[2,3,0,1] row_mask:0xf bank_mask:0xf
	s_and_saveexec_b64 s[42:43], s[6:7]
	s_cbranch_execz .LBB0_1502
	v_mov_b32_e32 v7, v147
	v_cvt_pk_fp8_f32 v7, v3, v5
	s_waitcnt lgkmcnt(0)
	v_cvt_pk_fp8_f32 v7, v4, v6 op_sel:[0,0,1]
	v_add_co_u32_e32 v4, vcc, 0xc000, v66
	s_nop 1
	v_addc_co_u32_e32 v5, vcc, 0, v67, vcc
	global_store_dword v[4:5], v7, off offset:2048
.LBB0_1502:
	s_or_b64 exec, exec, s[42:43]
	v_mul_f32_e32 v3, v63, v2
	s_nop 1
	v_mov_b32_dpp v5, v3 quad_perm:[1,0,3,2] row_mask:0xf bank_mask:0xf
	s_waitcnt lgkmcnt(0)
	s_nop 1
	v_mov_b32_dpp v4, v3 quad_perm:[2,3,0,1] row_mask:0xf bank_mask:0xf
	s_waitcnt lgkmcnt(0)
	s_nop 1
	v_mov_b32_dpp v6, v5 quad_perm:[2,3,0,1] row_mask:0xf bank_mask:0xf
	s_and_saveexec_b64 s[42:43], s[6:7]
	s_cbranch_execz .LBB0_1504
	v_mov_b32_e32 v7, v147
	v_cvt_pk_fp8_f32 v7, v3, v5
	s_waitcnt lgkmcnt(0)
	v_cvt_pk_fp8_f32 v7, v4, v6 op_sel:[0,0,1]
	v_add_co_u32_e32 v4, vcc, 0xc000, v66
	s_nop 1
	v_addc_co_u32_e32 v5, vcc, 0, v67, vcc
	global_store_dword v[4:5], v7, off offset:2080
.LBB0_1504:
	s_or_b64 exec, exec, s[42:43]
	v_mul_f32_e32 v3, v31, v2
	s_nop 1
	v_mov_b32_dpp v5, v3 quad_perm:[1,0,3,2] row_mask:0xf bank_mask:0xf
	s_waitcnt lgkmcnt(0)
	s_nop 1
	v_mov_b32_dpp v4, v3 quad_perm:[2,3,0,1] row_mask:0xf bank_mask:0xf
	s_waitcnt lgkmcnt(0)
	s_nop 1
	v_mov_b32_dpp v6, v5 quad_perm:[2,3,0,1] row_mask:0xf bank_mask:0xf
	s_and_saveexec_b64 s[42:43], s[6:7]
	s_cbranch_execz .LBB0_1506
	v_mov_b32_e32 v7, v147
	v_cvt_pk_fp8_f32 v7, v3, v5
	s_waitcnt lgkmcnt(0)
	v_cvt_pk_fp8_f32 v7, v4, v6 op_sel:[0,0,1]
	v_add_co_u32_e32 v4, vcc, 0xc000, v66
	s_nop 1
	v_addc_co_u32_e32 v5, vcc, 0, v67, vcc
	global_store_dword v[4:5], v7, off offset:2112
.LBB0_1506:
	s_or_b64 exec, exec, s[42:43]
	v_mul_f32_e32 v2, v15, v2
	s_waitcnt lgkmcnt(0)
	s_nop 1
	v_mov_b32_dpp v4, v2 quad_perm:[1,0,3,2] row_mask:0xf bank_mask:0xf
	s_nop 1
	v_mov_b32_dpp v3, v2 quad_perm:[2,3,0,1] row_mask:0xf bank_mask:0xf
	s_waitcnt lgkmcnt(0)
	s_nop 1
	v_mov_b32_dpp v5, v4 quad_perm:[2,3,0,1] row_mask:0xf bank_mask:0xf
	s_and_saveexec_b64 s[42:43], s[6:7]
	s_cbranch_execz .LBB0_1508
	v_mov_b32_e32 v6, v147
	v_cvt_pk_fp8_f32 v6, v2, v4
	v_add_co_u32_e32 v2, vcc, 0xc000, v66
	s_waitcnt lgkmcnt(0)
	v_cvt_pk_fp8_f32 v6, v3, v5 op_sel:[0,0,1]
	v_addc_co_u32_e32 v3, vcc, 0, v67, vcc
	global_store_dword v[2:3], v6, off offset:2144
; #define LDS_WAIT() asm volatile("s_waitcnt lgkmcnt(0)" ::: "memory")
; __device__ __forceinline__ unsigned cvt4_fp8(float a, float b, float c, float d) { int w = 0; w = __builtin_amdgcn_cvt_pk_fp8_f32(a, b, w, false); w = __builtin_amdgcn_cvt_pk_fp8_f32(c, d, w, true); return (unsigned)w; }
; template <bool MLA>
; __device__ __forceinline__ void attn_unit(char* lds, int h, int qb, const bf16_t* Qp, int ldq, const bf16_t* Kp, int ldk, const bf16_t* KRp, const bf16_t* Vp, int ldv,
;                                           unsigned char* Op, int ldo, const float* KMp, const float* rel_bias) {
;     ...
;     if (hi == 0) li_l[r32] = l_reg; LDS_WAIT();
;     unsigned char* Ow = Op + (size_t)qlo * ldo;
; #pragma unroll
;     for (int r = 0; r < 16; ++r) { const int orow = CROWC(r) + 4 * hi; const float rl = 16.0f * __builtin_amdgcn_rcpf(li_h[CROWC(r)]);
; #pragma unroll
;         for (int d0 = 0; d0 < 4; ++d0) { const float v = o[d0][r] * rl; const float v1 = __shfl_xor(v, 1), v2 = __shfl_xor(v, 2), v3 = __shfl_xor(v1, 2);
;             if ((r32 & 3) == 0) *(unsigned*)(Ow + (size_t)orow * ldo + d0 * 32 + r32) = cvt4_fp8(v, v1, v2, v3); } }
; __global__ void __launch_bounds__(512, 2) mega_fwd(Args args) {
;     ...
;         for (;;) { if (tid == 0) MISC[12] = atomicAdd(ctl + CW_AQ1, 1u);
;             __syncthreads(); const int it = (int)MISC[12]; __syncthreads();
;             if (it >= 512) break;
;             const int qb = 15 - (it >> 5), bh = it & 31, b = bh >> 3, hh = bh & 7;
;             att::attn_unit<true>((char*)lds_raw, hh, qb, QM + (size_t)b * SEQ * 1536 + hh * 192, 1536, KV + (size_t)b * SEQ * 2048 + hh * 256, 2048, KR + (size_t)b * SEQ * 64,
;                                  KV + (size_t)b * SEQ * 2048 + hh * 256 + 128, 2048, YAB + (size_t)b * SEQ * 2048 + hh * 128, 2048, nullptr, nullptr); }
.LBB0_1508:
	s_or_b64 exec, exec, s[42:43]
	ds_read_b32 v2, v167 offset:104
	s_waitcnt lgkmcnt(0)
	v_rcp_f32_e32 v2, v2
	s_nop 0
	v_mul_f32_e32 v2, 0x41800000, v2
	v_mul_f32_e32 v3, v48, v2
	s_nop 1
	v_mov_b32_dpp v5, v3 quad_perm:[1,0,3,2] row_mask:0xf bank_mask:0xf
	s_nop 1
	v_mov_b32_dpp v4, v3 quad_perm:[2,3,0,1] row_mask:0xf bank_mask:0xf
	s_waitcnt lgkmcnt(0)
	s_nop 1
	v_mov_b32_dpp v6, v5 quad_perm:[2,3,0,1] row_mask:0xf bank_mask:0xf
	s_and_saveexec_b64 s[42:43], s[6:7]
	s_cbranch_execz .LBB0_1510
	v_mov_b32_e32 v7, v147
	v_cvt_pk_fp8_f32 v7, v3, v5
	s_waitcnt lgkmcnt(0)
	v_cvt_pk_fp8_f32 v7, v4, v6 op_sel:[0,0,1]
	v_add_co_u32_e32 v4, vcc, 0xd000, v66
	s_nop 1
	v_addc_co_u32_e32 v5, vcc, 0, v67, vcc
	global_store_dword v[4:5], v7, off
.LBB0_1510:
	s_or_b64 exec, exec, s[42:43]
	v_mul_f32_e32 v3, v64, v2
	s_nop 1
	v_mov_b32_dpp v5, v3 quad_perm:[1,0,3,2] row_mask:0xf bank_mask:0xf
	s_waitcnt lgkmcnt(0)
	s_nop 1
	v_mov_b32_dpp v4, v3 quad_perm:[2,3,0,1] row_mask:0xf bank_mask:0xf
	s_waitcnt lgkmcnt(0)
	s_nop 1
	v_mov_b32_dpp v6, v5 quad_perm:[2,3,0,1] row_mask:0xf bank_mask:0xf
	s_and_saveexec_b64 s[42:43], s[6:7]
	s_cbranch_execz .LBB0_1512
	v_mov_b32_e32 v7, v147
	v_cvt_pk_fp8_f32 v7, v3, v5
	s_waitcnt lgkmcnt(0)
	v_cvt_pk_fp8_f32 v7, v4, v6 op_sel:[0,0,1]
	v_add_co_u32_e32 v4, vcc, 0xd000, v66
	s_nop 1
	v_addc_co_u32_e32 v5, vcc, 0, v67, vcc
	global_store_dword v[4:5], v7, off offset:32
.LBB0_1512:
	s_or_b64 exec, exec, s[42:43]
	v_mul_f32_e32 v3, v32, v2
	s_nop 1
	v_mov_b32_dpp v5, v3 quad_perm:[1,0,3,2] row_mask:0xf bank_mask:0xf
	s_waitcnt lgkmcnt(0)
	s_nop 1
	v_mov_b32_dpp v4, v3 quad_perm:[2,3,0,1] row_mask:0xf bank_mask:0xf
	s_waitcnt lgkmcnt(0)
	s_nop 1
	v_mov_b32_dpp v6, v5 quad_perm:[2,3,0,1] row_mask:0xf bank_mask:0xf
	s_and_saveexec_b64 s[42:43], s[6:7]
	s_cbranch_execz .LBB0_1514
	v_mov_b32_e32 v7, v147
	v_cvt_pk_fp8_f32 v7, v3, v5
	s_waitcnt lgkmcnt(0)
	v_cvt_pk_fp8_f32 v7, v4, v6 op_sel:[0,0,1]
	v_add_co_u32_e32 v4, vcc, 0xd000, v66
	s_nop 1
	v_addc_co_u32_e32 v5, vcc, 0, v67, vcc
	global_store_dword v[4:5], v7, off offset:64
.LBB0_1514:
	s_or_b64 exec, exec, s[42:43]
	v_mul_f32_e32 v2, v16, v2
	s_waitcnt lgkmcnt(0)
	s_nop 1
	v_mov_b32_dpp v4, v2 quad_perm:[1,0,3,2] row_mask:0xf bank_mask:0xf
	s_nop 1
	v_mov_b32_dpp v3, v2 quad_perm:[2,3,0,1] row_mask:0xf bank_mask:0xf
	s_waitcnt lgkmcnt(0)
	s_nop 1
	v_mov_b32_dpp v5, v4 quad_perm:[2,3,0,1] row_mask:0xf bank_mask:0xf
	s_and_saveexec_b64 s[42:43], s[6:7]
	s_cbranch_execz .LBB0_1516
	v_mov_b32_e32 v6, v147
	v_cvt_pk_fp8_f32 v6, v2, v4
	v_add_co_u32_e32 v2, vcc, 0xd000, v66
	s_waitcnt lgkmcnt(0)
	v_cvt_pk_fp8_f32 v6, v3, v5 op_sel:[0,0,1]
	v_addc_co_u32_e32 v3, vcc, 0, v67, vcc
	global_store_dword v[2:3], v6, off offset:96
.LBB0_1516:
	s_or_b64 exec, exec, s[42:43]
	ds_read_b32 v2, v167 offset:108
	s_waitcnt lgkmcnt(0)
	v_rcp_f32_e32 v2, v2
	s_nop 0
	v_mul_f32_e32 v2, 0x41800000, v2
	v_mul_f32_e32 v3, v49, v2
	s_nop 1
	v_mov_b32_dpp v5, v3 quad_perm:[1,0,3,2] row_mask:0xf bank_mask:0xf
	s_nop 1
	v_mov_b32_dpp v4, v3 quad_perm:[2,3,0,1] row_mask:0xf bank_mask:0xf
	s_waitcnt lgkmcnt(0)
	s_nop 1
	v_mov_b32_dpp v6, v5 quad_perm:[2,3,0,1] row_mask:0xf bank_mask:0xf
	s_and_saveexec_b64 s[42:43], s[6:7]
	s_cbranch_execz .LBB0_1518
	v_mov_b32_e32 v7, v147
	v_cvt_pk_fp8_f32 v7, v3, v5
	s_waitcnt lgkmcnt(0)
	v_cvt_pk_fp8_f32 v7, v4, v6 op_sel:[0,0,1]
	v_add_co_u32_e32 v4, vcc, 0xd000, v66
	s_nop 1
	v_addc_co_u32_e32 v5, vcc, 0, v67, vcc
	global_store_dword v[4:5], v7, off offset:2048
.LBB0_1518:
	s_or_b64 exec, exec, s[42:43]
	v_mul_f32_e32 v3, v65, v2
	s_nop 1
	v_mov_b32_dpp v5, v3 quad_perm:[1,0,3,2] row_mask:0xf bank_mask:0xf
	s_waitcnt lgkmcnt(0)
	s_nop 1
	v_mov_b32_dpp v4, v3 quad_perm:[2,3,0,1] row_mask:0xf bank_mask:0xf
	s_waitcnt lgkmcnt(0)
	s_nop 1
	v_mov_b32_dpp v6, v5 quad_perm:[2,3,0,1] row_mask:0xf bank_mask:0xf
	s_and_saveexec_b64 s[42:43], s[6:7]
	s_cbranch_execz .LBB0_1520
	v_mov_b32_e32 v7, v147
	v_cvt_pk_fp8_f32 v7, v3, v5
	s_waitcnt lgkmcnt(0)
	v_cvt_pk_fp8_f32 v7, v4, v6 op_sel:[0,0,1]
	v_add_co_u32_e32 v4, vcc, 0xd000, v66
	s_nop 1
	v_addc_co_u32_e32 v5, vcc, 0, v67, vcc
	global_store_dword v[4:5], v7, off offset:2080
.LBB0_1520:
	s_or_b64 exec, exec, s[42:43]
	v_mul_f32_e32 v3, v33, v2
	s_nop 1
	v_mov_b32_dpp v5, v3 quad_perm:[1,0,3,2] row_mask:0xf bank_mask:0xf
	s_waitcnt lgkmcnt(0)
	s_nop 1
	v_mov_b32_dpp v4, v3 quad_perm:[2,3,0,1] row_mask:0xf bank_mask:0xf
	s_waitcnt lgkmcnt(0)
	s_nop 1
	v_mov_b32_dpp v6, v5 quad_perm:[2,3,0,1] row_mask:0xf bank_mask:0xf
	s_and_saveexec_b64 s[42:43], s[6:7]
	s_cbranch_execz .LBB0_1522
	v_mov_b32_e32 v7, v147
	v_cvt_pk_fp8_f32 v7, v3, v5
	s_waitcnt lgkmcnt(0)
	v_cvt_pk_fp8_f32 v7, v4, v6 op_sel:[0,0,1]
	v_add_co_u32_e32 v4, vcc, 0xd000, v66
	s_nop 1
	v_addc_co_u32_e32 v5, vcc, 0, v67, vcc
	global_store_dword v[4:5], v7, off offset:2112
.LBB0_1522:
	s_or_b64 exec, exec, s[42:43]
	v_mul_f32_e32 v2, v17, v2
	s_waitcnt lgkmcnt(0)
	s_nop 1
	v_mov_b32_dpp v4, v2 quad_perm:[1,0,3,2] row_mask:0xf bank_mask:0xf
	s_nop 1
	v_mov_b32_dpp v3, v2 quad_perm:[2,3,0,1] row_mask:0xf bank_mask:0xf
	s_waitcnt lgkmcnt(0)
	s_nop 1
	v_mov_b32_dpp v5, v4 quad_perm:[2,3,0,1] row_mask:0xf bank_mask:0xf
	s_and_saveexec_b64 s[42:43], s[6:7]
	s_cbranch_execz .LBB0_1375
	v_mov_b32_e32 v6, v147
	v_cvt_pk_fp8_f32 v6, v2, v4
	v_add_co_u32_e32 v2, vcc, 0xd000, v66
	s_waitcnt lgkmcnt(0)
	v_cvt_pk_fp8_f32 v6, v3, v5 op_sel:[0,0,1]
	v_addc_co_u32_e32 v3, vcc, 0, v67, vcc
	global_store_dword v[2:3], v6, off offset:2144
	s_branch .LBB0_1375

; #define LDS_WAIT() asm volatile("s_waitcnt lgkmcnt(0)" ::: "memory")
; __device__ __forceinline__ unsigned cvt4_fp8(float a, float b, float c, float d) { int w = 0; w = __builtin_amdgcn_cvt_pk_fp8_f32(a, b, w, false); w = __builtin_amdgcn_cvt_pk_fp8_f32(c, d, w, true); return (unsigned)w; }
; template <bool MLA>
; __device__ __forceinline__ void attn_unit(char* lds, int h, int qb, const bf16_t* Qp, int ldq, const bf16_t* Kp, int ldk, const bf16_t* KRp, const bf16_t* Vp, int ldv,
;                                           unsigned char* Op, int ldo, const float* KMp, const float* rel_bias) {
;     ...
;     if (hi == 0) li_l[r32] = l_reg; LDS_WAIT();
;     unsigned char* Ow = Op + (size_t)qlo * ldo;
; #pragma unroll
;     for (int r = 0; r < 16; ++r) { const int orow = CROWC(r) + 4 * hi; const float rl = 16.0f * __builtin_amdgcn_rcpf(li_h[CROWC(r)]);
; #pragma unroll
;         for (int d0 = 0; d0 < 4; ++d0) { const float v = o[d0][r] * rl; const float v1 = __shfl_xor(v, 1), v2 = __shfl_xor(v, 2), v3 = __shfl_xor(v1, 2);
;             if ((r32 & 3) == 0) *(unsigned*)(Ow + (size_t)orow * ldo + d0 * 32 + r32) = cvt4_fp8(v, v1, v2, v3); } }
.LBB0_1645:
	s_waitcnt vmcnt(0)
	s_barrier
	s_and_saveexec_b64 s[12:13], s[4:5]
	ds_write_b32 v177, v216
	s_or_b64 exec, exec, s[12:13]
	s_waitcnt lgkmcnt(0)
	ds_read_b32 v2, v173
	v_and_b32_e32 v69, 64, v195
	v_xor_b32_e32 v68, 1, v195
	v_add_u32_e32 v69, 64, v69
	v_cmp_lt_i32_e32 vcc, v68, v69
	s_waitcnt lgkmcnt(0)
	v_rcp_f32_e32 v70, v2
	s_lshl_b32 s12, s64, 11
	v_cndmask_b32_e32 v2, v195, v68, vcc
	v_lshlrev_b32_e32 v2, 2, v2
	v_mul_f32_e32 v72, 0x41800000, v70
	v_mul_f32_e32 v73, v52, v72
	s_nop 1
	v_mov_b32_dpp v74, v73 quad_perm:[1,0,3,2] row_mask:0xf bank_mask:0xf
	s_add_u32 s12, s70, s12
	v_xor_b32_e32 v68, 2, v195
	s_addc_u32 s13, s71, 0
	v_cmp_lt_i32_e32 vcc, v68, v69
	s_add_u32 s3, s12, s3
	s_addc_u32 s22, s13, 0
	v_cndmask_b32_e32 v52, v195, v68, vcc
	s_lshl_b64 s[12:13], s[42:43], 11
	v_lshlrev_b32_e32 v52, 2, v52
	s_add_u32 s12, s3, s12
	s_nop 1
	v_mov_b32_dpp v75, v73 quad_perm:[2,3,0,1] row_mask:0xf bank_mask:0xf
	s_waitcnt lgkmcnt(0)
	s_nop 1
	v_mov_b32_dpp v76, v74 quad_perm:[2,3,0,1] row_mask:0xf bank_mask:0xf
	s_addc_u32 s13, s22, s13
	v_lshl_add_u64 v[68:69], s[12:13], 0, v[168:169]
	v_lshl_add_u64 v[70:71], v[68:69], 0, v[170:171]
	v_lshl_add_u64 v[68:69], v[70:71], 0, s[50:51]
	s_and_saveexec_b64 s[12:13], s[6:7]
	s_cbranch_execz .LBB0_1649
	v_mov_b32_e32 v77, v3
	v_cvt_pk_fp8_f32 v77, v73, v74
	s_waitcnt lgkmcnt(0)
	v_cvt_pk_fp8_f32 v77, v75, v76 op_sel:[0,0,1]
	global_store_dword v[68:69], v77, off
.LBB0_1649:
	s_or_b64 exec, exec, s[12:13]
	v_mul_f32_e32 v36, v36, v72
	s_nop 1
	v_mov_b32_dpp v74, v36 quad_perm:[1,0,3,2] row_mask:0xf bank_mask:0xf
	s_nop 1
	v_mov_b32_dpp v73, v36 quad_perm:[2,3,0,1] row_mask:0xf bank_mask:0xf
	s_waitcnt lgkmcnt(0)
	s_nop 1
	v_mov_b32_dpp v75, v74 quad_perm:[2,3,0,1] row_mask:0xf bank_mask:0xf
	s_and_saveexec_b64 s[12:13], s[6:7]
	s_cbranch_execz .LBB0_1651
	v_mov_b32_e32 v76, v3
	v_cvt_pk_fp8_f32 v76, v36, v74
	s_waitcnt lgkmcnt(0)
	v_cvt_pk_fp8_f32 v76, v73, v75 op_sel:[0,0,1]
	global_store_dword v[70:71], v76, off offset:1056
.LBB0_1651:
	s_or_b64 exec, exec, s[12:13]
	v_mul_f32_e32 v20, v20, v72
	s_waitcnt lgkmcnt(0)
	s_nop 1
	v_mov_b32_dpp v73, v20 quad_perm:[1,0,3,2] row_mask:0xf bank_mask:0xf
	s_nop 1
	v_mov_b32_dpp v36, v20 quad_perm:[2,3,0,1] row_mask:0xf bank_mask:0xf
	s_waitcnt lgkmcnt(0)
	s_nop 1
	v_mov_b32_dpp v74, v73 quad_perm:[2,3,0,1] row_mask:0xf bank_mask:0xf
	s_and_saveexec_b64 s[12:13], s[6:7]
	s_cbranch_execz .LBB0_1653
	v_mov_b32_e32 v75, v3
	v_cvt_pk_fp8_f32 v75, v20, v73
	s_waitcnt lgkmcnt(0)
	v_cvt_pk_fp8_f32 v75, v36, v74 op_sel:[0,0,1]
	global_store_dword v[70:71], v75, off offset:1088
.LBB0_1653:
	s_or_b64 exec, exec, s[12:13]
	v_mul_f32_e32 v4, v4, v72
	s_waitcnt lgkmcnt(0)
	s_nop 1
	v_mov_b32_dpp v36, v4 quad_perm:[1,0,3,2] row_mask:0xf bank_mask:0xf
	s_nop 1
	v_mov_b32_dpp v20, v4 quad_perm:[2,3,0,1] row_mask:0xf bank_mask:0xf
	s_waitcnt lgkmcnt(0)
	s_nop 1
	v_mov_b32_dpp v72, v36 quad_perm:[2,3,0,1] row_mask:0xf bank_mask:0xf
	s_and_saveexec_b64 s[12:13], s[6:7]
	s_cbranch_execz .LBB0_1655
	v_mov_b32_e32 v73, v3
	v_cvt_pk_fp8_f32 v73, v4, v36
	s_waitcnt lgkmcnt(0)
	v_cvt_pk_fp8_f32 v73, v20, v72 op_sel:[0,0,1]
	global_store_dword v[70:71], v73, off offset:1120
.LBB0_1655:
	s_or_b64 exec, exec, s[12:13]
	ds_read_b32 v4, v173 offset:4
	s_waitcnt lgkmcnt(0)
	v_rcp_f32_e32 v4, v4
	s_nop 0
	v_mul_f32_e32 v4, 0x41800000, v4
	v_mul_f32_e32 v20, v53, v4
	s_nop 1
	v_mov_b32_dpp v53, v20 quad_perm:[1,0,3,2] row_mask:0xf bank_mask:0xf
	s_nop 1
	v_mov_b32_dpp v36, v20 quad_perm:[2,3,0,1] row_mask:0xf bank_mask:0xf
	s_waitcnt lgkmcnt(0)
	s_nop 1
	v_mov_b32_dpp v72, v53 quad_perm:[2,3,0,1] row_mask:0xf bank_mask:0xf
	s_and_saveexec_b64 s[12:13], s[6:7]
	s_cbranch_execz .LBB0_1657
	v_mov_b32_e32 v73, v3
	v_cvt_pk_fp8_f32 v73, v20, v53
	s_waitcnt lgkmcnt(0)
	v_cvt_pk_fp8_f32 v73, v36, v72 op_sel:[0,0,1]
	global_store_dword v[70:71], v73, off offset:3072
.LBB0_1657:
	s_or_b64 exec, exec, s[12:13]
	v_mul_f32_e32 v20, v37, v4
	s_nop 1
	v_mov_b32_dpp v37, v20 quad_perm:[1,0,3,2] row_mask:0xf bank_mask:0xf
	s_waitcnt lgkmcnt(0)
	s_nop 1
	v_mov_b32_dpp v36, v20 quad_perm:[2,3,0,1] row_mask:0xf bank_mask:0xf
	s_waitcnt lgkmcnt(0)
	s_nop 1
	v_mov_b32_dpp v53, v37 quad_perm:[2,3,0,1] row_mask:0xf bank_mask:0xf
	s_and_saveexec_b64 s[12:13], s[6:7]
	s_cbranch_execz .LBB0_1659
	v_mov_b32_e32 v72, v3
	v_cvt_pk_fp8_f32 v72, v20, v37
	s_waitcnt lgkmcnt(0)
	v_cvt_pk_fp8_f32 v72, v36, v53 op_sel:[0,0,1]
	global_store_dword v[70:71], v72, off offset:3104
.LBB0_1659:
	s_or_b64 exec, exec, s[12:13]
	v_mul_f32_e32 v20, v21, v4
	s_waitcnt lgkmcnt(0)
	s_nop 1
	v_mov_b32_dpp v36, v20 quad_perm:[1,0,3,2] row_mask:0xf bank_mask:0xf
	s_nop 1
	v_mov_b32_dpp v21, v20 quad_perm:[2,3,0,1] row_mask:0xf bank_mask:0xf
	s_waitcnt lgkmcnt(0)
	s_nop 1
	v_mov_b32_dpp v37, v36 quad_perm:[2,3,0,1] row_mask:0xf bank_mask:0xf
	s_and_saveexec_b64 s[12:13], s[6:7]
	s_cbranch_execz .LBB0_1661
	v_mov_b32_e32 v53, v3
	v_cvt_pk_fp8_f32 v53, v20, v36
	s_waitcnt lgkmcnt(0)
	v_cvt_pk_fp8_f32 v53, v21, v37 op_sel:[0,0,1]
	global_store_dword v[70:71], v53, off offset:3136
.LBB0_1661:
	s_or_b64 exec, exec, s[12:13]
	v_mul_f32_e32 v4, v5, v4
	s_nop 1
	v_mov_b32_dpp v20, v4 quad_perm:[1,0,3,2] row_mask:0xf bank_mask:0xf
	s_nop 1
	v_mov_b32_dpp v5, v4 quad_perm:[2,3,0,1] row_mask:0xf bank_mask:0xf
	s_waitcnt lgkmcnt(0)
	s_nop 1
	v_mov_b32_dpp v21, v20 quad_perm:[2,3,0,1] row_mask:0xf bank_mask:0xf
	s_and_saveexec_b64 s[12:13], s[6:7]
	s_cbranch_execz .LBB0_1663
	v_mov_b32_e32 v36, v3
	v_cvt_pk_fp8_f32 v36, v4, v20
	s_waitcnt lgkmcnt(0)
	v_cvt_pk_fp8_f32 v36, v5, v21 op_sel:[0,0,1]
	global_store_dword v[70:71], v36, off offset:3168
; __device__ __forceinline__ unsigned cvt4_fp8(float a, float b, float c, float d) { int w = 0; w = __builtin_amdgcn_cvt_pk_fp8_f32(a, b, w, false); w = __builtin_amdgcn_cvt_pk_fp8_f32(c, d, w, true); return (unsigned)w; }
; template <bool MLA>
; __device__ __forceinline__ void attn_unit(char* lds, int h, int qb, const bf16_t* Qp, int ldq, const bf16_t* Kp, int ldk, const bf16_t* KRp, const bf16_t* Vp, int ldv,
;                                           unsigned char* Op, int ldo, const float* KMp, const float* rel_bias) {
;     ...
;     for (int r = 0; r < 16; ++r) { const int orow = CROWC(r) + 4 * hi; const float rl = 16.0f * __builtin_amdgcn_rcpf(li_h[CROWC(r)]);
; #pragma unroll
;         for (int d0 = 0; d0 < 4; ++d0) { const float v = o[d0][r] * rl; const float v1 = __shfl_xor(v, 1), v2 = __shfl_xor(v, 2), v3 = __shfl_xor(v1, 2);
;             if ((r32 & 3) == 0) *(unsigned*)(Ow + (size_t)orow * ldo + d0 * 32 + r32) = cvt4_fp8(v, v1, v2, v3); } }
.LBB0_1663:
	s_or_b64 exec, exec, s[12:13]
	ds_read_b32 v4, v173 offset:8
	s_waitcnt lgkmcnt(0)
	v_rcp_f32_e32 v4, v4
	s_nop 0
	v_mul_f32_e32 v4, 0x41800000, v4
	v_mul_f32_e32 v5, v54, v4
	s_nop 1
	v_mov_b32_dpp v21, v5 quad_perm:[1,0,3,2] row_mask:0xf bank_mask:0xf
	s_nop 1
	v_mov_b32_dpp v20, v5 quad_perm:[2,3,0,1] row_mask:0xf bank_mask:0xf
	s_waitcnt lgkmcnt(0)
	s_nop 1
	v_mov_b32_dpp v36, v21 quad_perm:[2,3,0,1] row_mask:0xf bank_mask:0xf
	s_and_saveexec_b64 s[12:13], s[6:7]
	s_cbranch_execz .LBB0_1665
	v_mov_b32_e32 v37, v3
	v_cvt_pk_fp8_f32 v37, v5, v21
	s_waitcnt lgkmcnt(0)
	v_cvt_pk_fp8_f32 v37, v20, v36 op_sel:[0,0,1]
	v_add_co_u32_e32 v20, vcc, 0x1000, v68
	s_nop 1
	v_addc_co_u32_e32 v21, vcc, 0, v69, vcc
	global_store_dword v[20:21], v37, off
.LBB0_1665:
	s_or_b64 exec, exec, s[12:13]
	v_mul_f32_e32 v5, v38, v4
	s_nop 1
	v_mov_b32_dpp v21, v5 quad_perm:[1,0,3,2] row_mask:0xf bank_mask:0xf
	s_waitcnt lgkmcnt(0)
	s_nop 1
	v_mov_b32_dpp v20, v5 quad_perm:[2,3,0,1] row_mask:0xf bank_mask:0xf
	s_waitcnt lgkmcnt(0)
	s_nop 1
	v_mov_b32_dpp v36, v21 quad_perm:[2,3,0,1] row_mask:0xf bank_mask:0xf
	s_and_saveexec_b64 s[12:13], s[6:7]
	s_cbranch_execz .LBB0_1667
	v_mov_b32_e32 v37, v3
	v_cvt_pk_fp8_f32 v37, v5, v21
	s_waitcnt lgkmcnt(0)
	v_cvt_pk_fp8_f32 v37, v20, v36 op_sel:[0,0,1]
	v_add_co_u32_e32 v20, vcc, 0x1000, v68
	s_nop 1
	v_addc_co_u32_e32 v21, vcc, 0, v69, vcc
	global_store_dword v[20:21], v37, off offset:32
.LBB0_1667:
	s_or_b64 exec, exec, s[12:13]
	v_mul_f32_e32 v5, v22, v4
	s_nop 1
	v_mov_b32_dpp v21, v5 quad_perm:[1,0,3,2] row_mask:0xf bank_mask:0xf
	s_waitcnt lgkmcnt(0)
	s_nop 1
	v_mov_b32_dpp v20, v5 quad_perm:[2,3,0,1] row_mask:0xf bank_mask:0xf
	s_waitcnt lgkmcnt(0)
	s_nop 1
	v_mov_b32_dpp v22, v21 quad_perm:[2,3,0,1] row_mask:0xf bank_mask:0xf
	s_and_saveexec_b64 s[12:13], s[6:7]
	s_cbranch_execz .LBB0_1669
	v_mov_b32_e32 v36, v3
	v_cvt_pk_fp8_f32 v36, v5, v21
	s_waitcnt lgkmcnt(0)
	v_cvt_pk_fp8_f32 v36, v20, v22 op_sel:[0,0,1]
	v_add_co_u32_e32 v20, vcc, 0x1000, v68
	s_nop 1
	v_addc_co_u32_e32 v21, vcc, 0, v69, vcc
	global_store_dword v[20:21], v36, off offset:64
.LBB0_1669:
	s_or_b64 exec, exec, s[12:13]
	v_mul_f32_e32 v4, v6, v4
	s_nop 1
	v_mov_b32_dpp v6, v4 quad_perm:[1,0,3,2] row_mask:0xf bank_mask:0xf
	s_nop 1
	v_mov_b32_dpp v5, v4 quad_perm:[2,3,0,1] row_mask:0xf bank_mask:0xf
	s_waitcnt lgkmcnt(0)
	s_nop 1
	v_mov_b32_dpp v20, v6 quad_perm:[2,3,0,1] row_mask:0xf bank_mask:0xf
	s_and_saveexec_b64 s[12:13], s[6:7]
	s_cbranch_execz .LBB0_1671
	v_mov_b32_e32 v21, v3
	v_cvt_pk_fp8_f32 v21, v4, v6
	v_add_co_u32_e32 v4, vcc, 0x1000, v68
	s_waitcnt lgkmcnt(0)
	v_cvt_pk_fp8_f32 v21, v5, v20 op_sel:[0,0,1]
	v_addc_co_u32_e32 v5, vcc, 0, v69, vcc
	global_store_dword v[4:5], v21, off offset:96
.LBB0_1671:
	s_or_b64 exec, exec, s[12:13]
	ds_read_b32 v4, v173 offset:12
	s_waitcnt lgkmcnt(0)
	v_rcp_f32_e32 v4, v4
	s_nop 0
	v_mul_f32_e32 v4, 0x41800000, v4
	v_mul_f32_e32 v5, v55, v4
	s_nop 1
	v_mov_b32_dpp v20, v5 quad_perm:[1,0,3,2] row_mask:0xf bank_mask:0xf
	s_nop 1
	v_mov_b32_dpp v6, v5 quad_perm:[2,3,0,1] row_mask:0xf bank_mask:0xf
	s_waitcnt lgkmcnt(0)
	s_nop 1
	v_mov_b32_dpp v21, v20 quad_perm:[2,3,0,1] row_mask:0xf bank_mask:0xf
	s_and_saveexec_b64 s[12:13], s[6:7]
	s_cbranch_execz .LBB0_1673
	v_mov_b32_e32 v22, v3
	v_cvt_pk_fp8_f32 v22, v5, v20
	v_add_co_u32_e32 v20, vcc, 0x1000, v68
	s_waitcnt lgkmcnt(0)
	v_cvt_pk_fp8_f32 v22, v6, v21 op_sel:[0,0,1]
	v_addc_co_u32_e32 v21, vcc, 0, v69, vcc
	global_store_dword v[20:21], v22, off offset:2048
.LBB0_1673:
	s_or_b64 exec, exec, s[12:13]
	v_mul_f32_e32 v5, v39, v4
	s_nop 1
	v_mov_b32_dpp v20, v5 quad_perm:[1,0,3,2] row_mask:0xf bank_mask:0xf
	s_waitcnt lgkmcnt(0)
	s_nop 1
	v_mov_b32_dpp v6, v5 quad_perm:[2,3,0,1] row_mask:0xf bank_mask:0xf
	s_waitcnt lgkmcnt(0)
	s_nop 1
	v_mov_b32_dpp v21, v20 quad_perm:[2,3,0,1] row_mask:0xf bank_mask:0xf
	s_and_saveexec_b64 s[12:13], s[6:7]
	s_cbranch_execz .LBB0_1675
	v_mov_b32_e32 v22, v3
	v_cvt_pk_fp8_f32 v22, v5, v20
	v_add_co_u32_e32 v20, vcc, 0x1000, v68
	s_waitcnt lgkmcnt(0)
	v_cvt_pk_fp8_f32 v22, v6, v21 op_sel:[0,0,1]
	v_addc_co_u32_e32 v21, vcc, 0, v69, vcc
	global_store_dword v[20:21], v22, off offset:2080
.LBB0_1675:
	s_or_b64 exec, exec, s[12:13]
	v_mul_f32_e32 v5, v23, v4
	s_nop 1
	v_mov_b32_dpp v20, v5 quad_perm:[1,0,3,2] row_mask:0xf bank_mask:0xf
	s_waitcnt lgkmcnt(0)
	s_nop 1
	v_mov_b32_dpp v6, v5 quad_perm:[2,3,0,1] row_mask:0xf bank_mask:0xf
	s_waitcnt lgkmcnt(0)
	s_nop 1
	v_mov_b32_dpp v21, v20 quad_perm:[2,3,0,1] row_mask:0xf bank_mask:0xf
	s_and_saveexec_b64 s[12:13], s[6:7]
	s_cbranch_execz .LBB0_1677
	v_mov_b32_e32 v22, v3
	v_cvt_pk_fp8_f32 v22, v5, v20
	v_add_co_u32_e32 v20, vcc, 0x1000, v68
	s_waitcnt lgkmcnt(0)
	v_cvt_pk_fp8_f32 v22, v6, v21 op_sel:[0,0,1]
	v_addc_co_u32_e32 v21, vcc, 0, v69, vcc
	global_store_dword v[20:21], v22, off offset:2112
.LBB0_1677:
	s_or_b64 exec, exec, s[12:13]
	v_mul_f32_e32 v4, v7, v4
	s_waitcnt lgkmcnt(0)
	s_nop 1
	v_mov_b32_dpp v6, v4 quad_perm:[1,0,3,2] row_mask:0xf bank_mask:0xf
	s_nop 1
	v_mov_b32_dpp v5, v4 quad_perm:[2,3,0,1] row_mask:0xf bank_mask:0xf
	s_waitcnt lgkmcnt(0)
	s_nop 1
	v_mov_b32_dpp v7, v6 quad_perm:[2,3,0,1] row_mask:0xf bank_mask:0xf
	s_and_saveexec_b64 s[12:13], s[6:7]
	s_cbranch_execz .LBB0_1679
	v_mov_b32_e32 v20, v3
	v_cvt_pk_fp8_f32 v20, v4, v6
	v_add_co_u32_e32 v4, vcc, 0x1000, v68
	s_waitcnt lgkmcnt(0)
	v_cvt_pk_fp8_f32 v20, v5, v7 op_sel:[0,0,1]
	v_addc_co_u32_e32 v5, vcc, 0, v69, vcc
	global_store_dword v[4:5], v20, off offset:2144
; __device__ __forceinline__ unsigned cvt4_fp8(float a, float b, float c, float d) { int w = 0; w = __builtin_amdgcn_cvt_pk_fp8_f32(a, b, w, false); w = __builtin_amdgcn_cvt_pk_fp8_f32(c, d, w, true); return (unsigned)w; }
; template <bool MLA>
; __device__ __forceinline__ void attn_unit(char* lds, int h, int qb, const bf16_t* Qp, int ldq, const bf16_t* Kp, int ldk, const bf16_t* KRp, const bf16_t* Vp, int ldv,
;                                           unsigned char* Op, int ldo, const float* KMp, const float* rel_bias) {
;     ...
;     for (int r = 0; r < 16; ++r) { const int orow = CROWC(r) + 4 * hi; const float rl = 16.0f * __builtin_amdgcn_rcpf(li_h[CROWC(r)]);
; #pragma unroll
;         for (int d0 = 0; d0 < 4; ++d0) { const float v = o[d0][r] * rl; const float v1 = __shfl_xor(v, 1), v2 = __shfl_xor(v, 2), v3 = __shfl_xor(v1, 2);
;             if ((r32 & 3) == 0) *(unsigned*)(Ow + (size_t)orow * ldo + d0 * 32 + r32) = cvt4_fp8(v, v1, v2, v3); } }
.LBB0_1679:
	s_or_b64 exec, exec, s[12:13]
	ds_read_b32 v4, v173 offset:32
	s_waitcnt lgkmcnt(0)
	v_rcp_f32_e32 v4, v4
	s_nop 0
	v_mul_f32_e32 v4, 0x41800000, v4
	v_mul_f32_e32 v5, v56, v4
	s_nop 1
	v_mov_b32_dpp v7, v5 quad_perm:[1,0,3,2] row_mask:0xf bank_mask:0xf
	s_nop 1
	v_mov_b32_dpp v6, v5 quad_perm:[2,3,0,1] row_mask:0xf bank_mask:0xf
	s_waitcnt lgkmcnt(0)
	s_nop 1
	v_mov_b32_dpp v20, v7 quad_perm:[2,3,0,1] row_mask:0xf bank_mask:0xf
	s_and_saveexec_b64 s[12:13], s[6:7]
	s_cbranch_execz .LBB0_1681
	v_mov_b32_e32 v21, v3
	v_cvt_pk_fp8_f32 v21, v5, v7
	s_waitcnt lgkmcnt(0)
	v_cvt_pk_fp8_f32 v21, v6, v20 op_sel:[0,0,1]
	v_add_co_u32_e32 v6, vcc, 0x4000, v68
	s_nop 1
	v_addc_co_u32_e32 v7, vcc, 0, v69, vcc
	global_store_dword v[6:7], v21, off
.LBB0_1681:
	s_or_b64 exec, exec, s[12:13]
	v_mul_f32_e32 v5, v40, v4
	s_nop 1
	v_mov_b32_dpp v7, v5 quad_perm:[1,0,3,2] row_mask:0xf bank_mask:0xf
	s_waitcnt lgkmcnt(0)
	s_nop 1
	v_mov_b32_dpp v6, v5 quad_perm:[2,3,0,1] row_mask:0xf bank_mask:0xf
	s_waitcnt lgkmcnt(0)
	s_nop 1
	v_mov_b32_dpp v20, v7 quad_perm:[2,3,0,1] row_mask:0xf bank_mask:0xf
	s_and_saveexec_b64 s[12:13], s[6:7]
	s_cbranch_execz .LBB0_1683
	v_mov_b32_e32 v21, v3
	v_cvt_pk_fp8_f32 v21, v5, v7
	s_waitcnt lgkmcnt(0)
	v_cvt_pk_fp8_f32 v21, v6, v20 op_sel:[0,0,1]
	v_add_co_u32_e32 v6, vcc, 0x4000, v68
	s_nop 1
	v_addc_co_u32_e32 v7, vcc, 0, v69, vcc
	global_store_dword v[6:7], v21, off offset:32
.LBB0_1683:
	s_or_b64 exec, exec, s[12:13]
	v_mul_f32_e32 v5, v24, v4
	s_nop 1
	v_mov_b32_dpp v7, v5 quad_perm:[1,0,3,2] row_mask:0xf bank_mask:0xf
	s_waitcnt lgkmcnt(0)
	s_nop 1
	v_mov_b32_dpp v6, v5 quad_perm:[2,3,0,1] row_mask:0xf bank_mask:0xf
	s_waitcnt lgkmcnt(0)
	s_nop 1
	v_mov_b32_dpp v20, v7 quad_perm:[2,3,0,1] row_mask:0xf bank_mask:0xf
	s_and_saveexec_b64 s[12:13], s[6:7]
	s_cbranch_execz .LBB0_1685
	v_mov_b32_e32 v21, v3
	v_cvt_pk_fp8_f32 v21, v5, v7
	s_waitcnt lgkmcnt(0)
	v_cvt_pk_fp8_f32 v21, v6, v20 op_sel:[0,0,1]
	v_add_co_u32_e32 v6, vcc, 0x4000, v68
	s_nop 1
	v_addc_co_u32_e32 v7, vcc, 0, v69, vcc
	global_store_dword v[6:7], v21, off offset:64
.LBB0_1685:
	s_or_b64 exec, exec, s[12:13]
	v_mul_f32_e32 v4, v8, v4
	s_waitcnt lgkmcnt(0)
	s_nop 1
	v_mov_b32_dpp v6, v4 quad_perm:[1,0,3,2] row_mask:0xf bank_mask:0xf
	s_nop 1
	v_mov_b32_dpp v5, v4 quad_perm:[2,3,0,1] row_mask:0xf bank_mask:0xf
	s_waitcnt lgkmcnt(0)
	s_nop 1
	v_mov_b32_dpp v7, v6 quad_perm:[2,3,0,1] row_mask:0xf bank_mask:0xf
	s_and_saveexec_b64 s[12:13], s[6:7]
	s_cbranch_execz .LBB0_1687
	v_mov_b32_e32 v8, v3
	v_cvt_pk_fp8_f32 v8, v4, v6
	v_add_co_u32_e32 v4, vcc, 0x4000, v68
	s_waitcnt lgkmcnt(0)
	v_cvt_pk_fp8_f32 v8, v5, v7 op_sel:[0,0,1]
	v_addc_co_u32_e32 v5, vcc, 0, v69, vcc
	global_store_dword v[4:5], v8, off offset:96
.LBB0_1687:
	s_or_b64 exec, exec, s[12:13]
	ds_read_b32 v4, v173 offset:36
	s_waitcnt lgkmcnt(0)
	v_rcp_f32_e32 v4, v4
	s_nop 0
	v_mul_f32_e32 v4, 0x41800000, v4
	v_mul_f32_e32 v5, v57, v4
	s_nop 1
	v_mov_b32_dpp v7, v5 quad_perm:[1,0,3,2] row_mask:0xf bank_mask:0xf
	s_nop 1
	v_mov_b32_dpp v6, v5 quad_perm:[2,3,0,1] row_mask:0xf bank_mask:0xf
	s_waitcnt lgkmcnt(0)
	s_nop 1
	v_mov_b32_dpp v8, v7 quad_perm:[2,3,0,1] row_mask:0xf bank_mask:0xf
	s_and_saveexec_b64 s[12:13], s[6:7]
	s_cbranch_execz .LBB0_1689
	v_mov_b32_e32 v20, v3
	v_cvt_pk_fp8_f32 v20, v5, v7
	s_waitcnt lgkmcnt(0)
	v_cvt_pk_fp8_f32 v20, v6, v8 op_sel:[0,0,1]
	v_add_co_u32_e32 v6, vcc, 0x4000, v68
	s_nop 1
	v_addc_co_u32_e32 v7, vcc, 0, v69, vcc
	global_store_dword v[6:7], v20, off offset:2048
.LBB0_1689:
	s_or_b64 exec, exec, s[12:13]
	v_mul_f32_e32 v5, v41, v4
	s_nop 1
	v_mov_b32_dpp v7, v5 quad_perm:[1,0,3,2] row_mask:0xf bank_mask:0xf
	s_waitcnt lgkmcnt(0)
	s_nop 1
	v_mov_b32_dpp v6, v5 quad_perm:[2,3,0,1] row_mask:0xf bank_mask:0xf
	s_waitcnt lgkmcnt(0)
	s_nop 1
	v_mov_b32_dpp v8, v7 quad_perm:[2,3,0,1] row_mask:0xf bank_mask:0xf
	s_and_saveexec_b64 s[12:13], s[6:7]
	s_cbranch_execz .LBB0_1691
	v_mov_b32_e32 v20, v3
	v_cvt_pk_fp8_f32 v20, v5, v7
	s_waitcnt lgkmcnt(0)
	v_cvt_pk_fp8_f32 v20, v6, v8 op_sel:[0,0,1]
	v_add_co_u32_e32 v6, vcc, 0x4000, v68
	s_nop 1
	v_addc_co_u32_e32 v7, vcc, 0, v69, vcc
	global_store_dword v[6:7], v20, off offset:2080
.LBB0_1691:
	s_or_b64 exec, exec, s[12:13]
	v_mul_f32_e32 v5, v25, v4
	s_nop 1
	v_mov_b32_dpp v7, v5 quad_perm:[1,0,3,2] row_mask:0xf bank_mask:0xf
	s_waitcnt lgkmcnt(0)
	s_nop 1
	v_mov_b32_dpp v6, v5 quad_perm:[2,3,0,1] row_mask:0xf bank_mask:0xf
	s_waitcnt lgkmcnt(0)
	s_nop 1
	v_mov_b32_dpp v8, v7 quad_perm:[2,3,0,1] row_mask:0xf bank_mask:0xf
	s_and_saveexec_b64 s[12:13], s[6:7]
	s_cbranch_execz .LBB0_1693
	v_mov_b32_e32 v20, v3
	v_cvt_pk_fp8_f32 v20, v5, v7
	s_waitcnt lgkmcnt(0)
	v_cvt_pk_fp8_f32 v20, v6, v8 op_sel:[0,0,1]
	v_add_co_u32_e32 v6, vcc, 0x4000, v68
	s_nop 1
	v_addc_co_u32_e32 v7, vcc, 0, v69, vcc
	global_store_dword v[6:7], v20, off offset:2112
.LBB0_1693:
	s_or_b64 exec, exec, s[12:13]
	v_mul_f32_e32 v4, v9, v4
	s_waitcnt lgkmcnt(0)
	s_nop 1
	v_mov_b32_dpp v6, v4 quad_perm:[1,0,3,2] row_mask:0xf bank_mask:0xf
	s_nop 1
	v_mov_b32_dpp v5, v4 quad_perm:[2,3,0,1] row_mask:0xf bank_mask:0xf
	s_waitcnt lgkmcnt(0)
	s_nop 1
	v_mov_b32_dpp v7, v6 quad_perm:[2,3,0,1] row_mask:0xf bank_mask:0xf
	s_and_saveexec_b64 s[12:13], s[6:7]
	s_cbranch_execz .LBB0_1695
	v_mov_b32_e32 v8, v3
	v_cvt_pk_fp8_f32 v8, v4, v6
	v_add_co_u32_e32 v4, vcc, 0x4000, v68
	s_waitcnt lgkmcnt(0)
	v_cvt_pk_fp8_f32 v8, v5, v7 op_sel:[0,0,1]
	v_addc_co_u32_e32 v5, vcc, 0, v69, vcc
	global_store_dword v[4:5], v8, off offset:2144
; __device__ __forceinline__ unsigned cvt4_fp8(float a, float b, float c, float d) { int w = 0; w = __builtin_amdgcn_cvt_pk_fp8_f32(a, b, w, false); w = __builtin_amdgcn_cvt_pk_fp8_f32(c, d, w, true); return (unsigned)w; }
; template <bool MLA>
; __device__ __forceinline__ void attn_unit(char* lds, int h, int qb, const bf16_t* Qp, int ldq, const bf16_t* Kp, int ldk, const bf16_t* KRp, const bf16_t* Vp, int ldv,
;                                           unsigned char* Op, int ldo, const float* KMp, const float* rel_bias) {
;     ...
;     for (int r = 0; r < 16; ++r) { const int orow = CROWC(r) + 4 * hi; const float rl = 16.0f * __builtin_amdgcn_rcpf(li_h[CROWC(r)]);
; #pragma unroll
;         for (int d0 = 0; d0 < 4; ++d0) { const float v = o[d0][r] * rl; const float v1 = __shfl_xor(v, 1), v2 = __shfl_xor(v, 2), v3 = __shfl_xor(v1, 2);
;             if ((r32 & 3) == 0) *(unsigned*)(Ow + (size_t)orow * ldo + d0 * 32 + r32) = cvt4_fp8(v, v1, v2, v3); } }
.LBB0_1695:
	s_or_b64 exec, exec, s[12:13]
	ds_read_b32 v4, v173 offset:40
	s_waitcnt lgkmcnt(0)
	v_rcp_f32_e32 v4, v4
	s_nop 0
	v_mul_f32_e32 v4, 0x41800000, v4
	v_mul_f32_e32 v5, v58, v4
	s_nop 1
	v_mov_b32_dpp v7, v5 quad_perm:[1,0,3,2] row_mask:0xf bank_mask:0xf
	s_nop 1
	v_mov_b32_dpp v6, v5 quad_perm:[2,3,0,1] row_mask:0xf bank_mask:0xf
	s_waitcnt lgkmcnt(0)
	s_nop 1
	v_mov_b32_dpp v8, v7 quad_perm:[2,3,0,1] row_mask:0xf bank_mask:0xf
	s_and_saveexec_b64 s[12:13], s[6:7]
	s_cbranch_execz .LBB0_1697
	v_mov_b32_e32 v9, v3
	v_cvt_pk_fp8_f32 v9, v5, v7
	s_waitcnt lgkmcnt(0)
	v_cvt_pk_fp8_f32 v9, v6, v8 op_sel:[0,0,1]
	v_add_co_u32_e32 v6, vcc, 0x5000, v68
	s_nop 1
	v_addc_co_u32_e32 v7, vcc, 0, v69, vcc
	global_store_dword v[6:7], v9, off
.LBB0_1697:
	s_or_b64 exec, exec, s[12:13]
	v_mul_f32_e32 v5, v42, v4
	s_nop 1
	v_mov_b32_dpp v7, v5 quad_perm:[1,0,3,2] row_mask:0xf bank_mask:0xf
	s_waitcnt lgkmcnt(0)
	s_nop 1
	v_mov_b32_dpp v6, v5 quad_perm:[2,3,0,1] row_mask:0xf bank_mask:0xf
	s_waitcnt lgkmcnt(0)
	s_nop 1
	v_mov_b32_dpp v8, v7 quad_perm:[2,3,0,1] row_mask:0xf bank_mask:0xf
	s_and_saveexec_b64 s[12:13], s[6:7]
	s_cbranch_execz .LBB0_1699
	v_mov_b32_e32 v9, v3
	v_cvt_pk_fp8_f32 v9, v5, v7
	s_waitcnt lgkmcnt(0)
	v_cvt_pk_fp8_f32 v9, v6, v8 op_sel:[0,0,1]
	v_add_co_u32_e32 v6, vcc, 0x5000, v68
	s_nop 1
	v_addc_co_u32_e32 v7, vcc, 0, v69, vcc
	global_store_dword v[6:7], v9, off offset:32
.LBB0_1699:
	s_or_b64 exec, exec, s[12:13]
	v_mul_f32_e32 v5, v26, v4
	s_nop 1
	v_mov_b32_dpp v7, v5 quad_perm:[1,0,3,2] row_mask:0xf bank_mask:0xf
	s_waitcnt lgkmcnt(0)
	s_nop 1
	v_mov_b32_dpp v6, v5 quad_perm:[2,3,0,1] row_mask:0xf bank_mask:0xf
	s_waitcnt lgkmcnt(0)
	s_nop 1
	v_mov_b32_dpp v8, v7 quad_perm:[2,3,0,1] row_mask:0xf bank_mask:0xf
	s_and_saveexec_b64 s[12:13], s[6:7]
	s_cbranch_execz .LBB0_1701
	v_mov_b32_e32 v9, v3
	v_cvt_pk_fp8_f32 v9, v5, v7
	s_waitcnt lgkmcnt(0)
	v_cvt_pk_fp8_f32 v9, v6, v8 op_sel:[0,0,1]
	v_add_co_u32_e32 v6, vcc, 0x5000, v68
	s_nop 1
	v_addc_co_u32_e32 v7, vcc, 0, v69, vcc
	global_store_dword v[6:7], v9, off offset:64
.LBB0_1701:
	s_or_b64 exec, exec, s[12:13]
	v_mul_f32_e32 v4, v10, v4
	s_waitcnt lgkmcnt(0)
	s_nop 1
	v_mov_b32_dpp v6, v4 quad_perm:[1,0,3,2] row_mask:0xf bank_mask:0xf
	s_nop 1
	v_mov_b32_dpp v5, v4 quad_perm:[2,3,0,1] row_mask:0xf bank_mask:0xf
	s_waitcnt lgkmcnt(0)
	s_nop 1
	v_mov_b32_dpp v7, v6 quad_perm:[2,3,0,1] row_mask:0xf bank_mask:0xf
	s_and_saveexec_b64 s[12:13], s[6:7]
	s_cbranch_execz .LBB0_1703
	v_mov_b32_e32 v8, v3
	v_cvt_pk_fp8_f32 v8, v4, v6
	v_add_co_u32_e32 v4, vcc, 0x5000, v68
	s_waitcnt lgkmcnt(0)
	v_cvt_pk_fp8_f32 v8, v5, v7 op_sel:[0,0,1]
	v_addc_co_u32_e32 v5, vcc, 0, v69, vcc
	global_store_dword v[4:5], v8, off offset:96
.LBB0_1703:
	s_or_b64 exec, exec, s[12:13]
	ds_read_b32 v4, v173 offset:44
	s_waitcnt lgkmcnt(0)
	v_rcp_f32_e32 v4, v4
	s_nop 0
	v_mul_f32_e32 v4, 0x41800000, v4
	v_mul_f32_e32 v5, v59, v4
	s_nop 1
	v_mov_b32_dpp v7, v5 quad_perm:[1,0,3,2] row_mask:0xf bank_mask:0xf
	s_nop 1
	v_mov_b32_dpp v6, v5 quad_perm:[2,3,0,1] row_mask:0xf bank_mask:0xf
	s_waitcnt lgkmcnt(0)
	s_nop 1
	v_mov_b32_dpp v8, v7 quad_perm:[2,3,0,1] row_mask:0xf bank_mask:0xf
	s_and_saveexec_b64 s[12:13], s[6:7]
	s_cbranch_execz .LBB0_1705
	v_mov_b32_e32 v9, v3
	v_cvt_pk_fp8_f32 v9, v5, v7
	s_waitcnt lgkmcnt(0)
	v_cvt_pk_fp8_f32 v9, v6, v8 op_sel:[0,0,1]
	v_add_co_u32_e32 v6, vcc, 0x5000, v68
	s_nop 1
	v_addc_co_u32_e32 v7, vcc, 0, v69, vcc
	global_store_dword v[6:7], v9, off offset:2048
.LBB0_1705:
	s_or_b64 exec, exec, s[12:13]
	v_mul_f32_e32 v5, v43, v4
	s_nop 1
	v_mov_b32_dpp v7, v5 quad_perm:[1,0,3,2] row_mask:0xf bank_mask:0xf
	s_waitcnt lgkmcnt(0)
	s_nop 1
	v_mov_b32_dpp v6, v5 quad_perm:[2,3,0,1] row_mask:0xf bank_mask:0xf
	s_waitcnt lgkmcnt(0)
	s_nop 1
	v_mov_b32_dpp v8, v7 quad_perm:[2,3,0,1] row_mask:0xf bank_mask:0xf
	s_and_saveexec_b64 s[12:13], s[6:7]
	s_cbranch_execz .LBB0_1707
	v_mov_b32_e32 v9, v3
	v_cvt_pk_fp8_f32 v9, v5, v7
	s_waitcnt lgkmcnt(0)
	v_cvt_pk_fp8_f32 v9, v6, v8 op_sel:[0,0,1]
	v_add_co_u32_e32 v6, vcc, 0x5000, v68
	s_nop 1
	v_addc_co_u32_e32 v7, vcc, 0, v69, vcc
	global_store_dword v[6:7], v9, off offset:2080
.LBB0_1707:
	s_or_b64 exec, exec, s[12:13]
	v_mul_f32_e32 v5, v27, v4
	s_nop 1
	v_mov_b32_dpp v7, v5 quad_perm:[1,0,3,2] row_mask:0xf bank_mask:0xf
	s_waitcnt lgkmcnt(0)
	s_nop 1
	v_mov_b32_dpp v6, v5 quad_perm:[2,3,0,1] row_mask:0xf bank_mask:0xf
	s_waitcnt lgkmcnt(0)
	s_nop 1
	v_mov_b32_dpp v8, v7 quad_perm:[2,3,0,1] row_mask:0xf bank_mask:0xf
	s_and_saveexec_b64 s[12:13], s[6:7]
	s_cbranch_execz .LBB0_1709
	v_mov_b32_e32 v9, v3
	v_cvt_pk_fp8_f32 v9, v5, v7
	s_waitcnt lgkmcnt(0)
	v_cvt_pk_fp8_f32 v9, v6, v8 op_sel:[0,0,1]
	v_add_co_u32_e32 v6, vcc, 0x5000, v68
	s_nop 1
	v_addc_co_u32_e32 v7, vcc, 0, v69, vcc
	global_store_dword v[6:7], v9, off offset:2112
.LBB0_1709:
	s_or_b64 exec, exec, s[12:13]
	v_mul_f32_e32 v4, v11, v4
	s_waitcnt lgkmcnt(0)
	s_nop 1
	v_mov_b32_dpp v6, v4 quad_perm:[1,0,3,2] row_mask:0xf bank_mask:0xf
	s_nop 1
	v_mov_b32_dpp v5, v4 quad_perm:[2,3,0,1] row_mask:0xf bank_mask:0xf
	s_waitcnt lgkmcnt(0)
	s_nop 1
	v_mov_b32_dpp v7, v6 quad_perm:[2,3,0,1] row_mask:0xf bank_mask:0xf
	s_and_saveexec_b64 s[12:13], s[6:7]
	s_cbranch_execz .LBB0_1711
	v_mov_b32_e32 v8, v3
	v_cvt_pk_fp8_f32 v8, v4, v6
	v_add_co_u32_e32 v4, vcc, 0x5000, v68
	s_waitcnt lgkmcnt(0)
	v_cvt_pk_fp8_f32 v8, v5, v7 op_sel:[0,0,1]
	v_addc_co_u32_e32 v5, vcc, 0, v69, vcc
	global_store_dword v[4:5], v8, off offset:2144
; __device__ __forceinline__ unsigned cvt4_fp8(float a, float b, float c, float d) { int w = 0; w = __builtin_amdgcn_cvt_pk_fp8_f32(a, b, w, false); w = __builtin_amdgcn_cvt_pk_fp8_f32(c, d, w, true); return (unsigned)w; }
; template <bool MLA>
; __device__ __forceinline__ void attn_unit(char* lds, int h, int qb, const bf16_t* Qp, int ldq, const bf16_t* Kp, int ldk, const bf16_t* KRp, const bf16_t* Vp, int ldv,
;                                           unsigned char* Op, int ldo, const float* KMp, const float* rel_bias) {
;     ...
;     for (int r = 0; r < 16; ++r) { const int orow = CROWC(r) + 4 * hi; const float rl = 16.0f * __builtin_amdgcn_rcpf(li_h[CROWC(r)]);
; #pragma unroll
;         for (int d0 = 0; d0 < 4; ++d0) { const float v = o[d0][r] * rl; const float v1 = __shfl_xor(v, 1), v2 = __shfl_xor(v, 2), v3 = __shfl_xor(v1, 2);
;             if ((r32 & 3) == 0) *(unsigned*)(Ow + (size_t)orow * ldo + d0 * 32 + r32) = cvt4_fp8(v, v1, v2, v3); } }
.LBB0_1711:
	s_or_b64 exec, exec, s[12:13]
	ds_read_b32 v4, v173 offset:64
	s_waitcnt lgkmcnt(0)
	v_rcp_f32_e32 v4, v4
	s_nop 0
	v_mul_f32_e32 v4, 0x41800000, v4
	v_mul_f32_e32 v5, v60, v4
	s_nop 1
	v_mov_b32_dpp v7, v5 quad_perm:[1,0,3,2] row_mask:0xf bank_mask:0xf
	s_nop 1
	v_mov_b32_dpp v6, v5 quad_perm:[2,3,0,1] row_mask:0xf bank_mask:0xf
	s_waitcnt lgkmcnt(0)
	s_nop 1
	v_mov_b32_dpp v8, v7 quad_perm:[2,3,0,1] row_mask:0xf bank_mask:0xf
	s_and_saveexec_b64 s[12:13], s[6:7]
	s_cbranch_execz .LBB0_1713
	v_mov_b32_e32 v9, v3
	v_cvt_pk_fp8_f32 v9, v5, v7
	s_waitcnt lgkmcnt(0)
	v_cvt_pk_fp8_f32 v9, v6, v8 op_sel:[0,0,1]
	v_add_co_u32_e32 v6, vcc, 0x8000, v68
	s_nop 1
	v_addc_co_u32_e32 v7, vcc, 0, v69, vcc
	global_store_dword v[6:7], v9, off
.LBB0_1713:
	s_or_b64 exec, exec, s[12:13]
	v_mul_f32_e32 v5, v44, v4
	s_nop 1
	v_mov_b32_dpp v7, v5 quad_perm:[1,0,3,2] row_mask:0xf bank_mask:0xf
	s_waitcnt lgkmcnt(0)
	s_nop 1
	v_mov_b32_dpp v6, v5 quad_perm:[2,3,0,1] row_mask:0xf bank_mask:0xf
	s_waitcnt lgkmcnt(0)
	s_nop 1
	v_mov_b32_dpp v8, v7 quad_perm:[2,3,0,1] row_mask:0xf bank_mask:0xf
	s_and_saveexec_b64 s[12:13], s[6:7]
	s_cbranch_execz .LBB0_1715
	v_mov_b32_e32 v9, v3
	v_cvt_pk_fp8_f32 v9, v5, v7
	s_waitcnt lgkmcnt(0)
	v_cvt_pk_fp8_f32 v9, v6, v8 op_sel:[0,0,1]
	v_add_co_u32_e32 v6, vcc, 0x8000, v68
	s_nop 1
	v_addc_co_u32_e32 v7, vcc, 0, v69, vcc
	global_store_dword v[6:7], v9, off offset:32
.LBB0_1715:
	s_or_b64 exec, exec, s[12:13]
	v_mul_f32_e32 v5, v28, v4
	s_nop 1
	v_mov_b32_dpp v7, v5 quad_perm:[1,0,3,2] row_mask:0xf bank_mask:0xf
	s_waitcnt lgkmcnt(0)
	s_nop 1
	v_mov_b32_dpp v6, v5 quad_perm:[2,3,0,1] row_mask:0xf bank_mask:0xf
	s_waitcnt lgkmcnt(0)
	s_nop 1
	v_mov_b32_dpp v8, v7 quad_perm:[2,3,0,1] row_mask:0xf bank_mask:0xf
	s_and_saveexec_b64 s[12:13], s[6:7]
	s_cbranch_execz .LBB0_1717
	v_mov_b32_e32 v9, v3
	v_cvt_pk_fp8_f32 v9, v5, v7
	s_waitcnt lgkmcnt(0)
	v_cvt_pk_fp8_f32 v9, v6, v8 op_sel:[0,0,1]
	v_add_co_u32_e32 v6, vcc, 0x8000, v68
	s_nop 1
	v_addc_co_u32_e32 v7, vcc, 0, v69, vcc
	global_store_dword v[6:7], v9, off offset:64
.LBB0_1717:
	s_or_b64 exec, exec, s[12:13]
	v_mul_f32_e32 v4, v12, v4
	s_waitcnt lgkmcnt(0)
	s_nop 1
	v_mov_b32_dpp v6, v4 quad_perm:[1,0,3,2] row_mask:0xf bank_mask:0xf
	s_nop 1
	v_mov_b32_dpp v5, v4 quad_perm:[2,3,0,1] row_mask:0xf bank_mask:0xf
	s_waitcnt lgkmcnt(0)
	s_nop 1
	v_mov_b32_dpp v7, v6 quad_perm:[2,3,0,1] row_mask:0xf bank_mask:0xf
	s_and_saveexec_b64 s[12:13], s[6:7]
	s_cbranch_execz .LBB0_1719
	v_mov_b32_e32 v8, v3
	v_cvt_pk_fp8_f32 v8, v4, v6
	v_add_co_u32_e32 v4, vcc, 0x8000, v68
	s_waitcnt lgkmcnt(0)
	v_cvt_pk_fp8_f32 v8, v5, v7 op_sel:[0,0,1]
	v_addc_co_u32_e32 v5, vcc, 0, v69, vcc
	global_store_dword v[4:5], v8, off offset:96
.LBB0_1719:
	s_or_b64 exec, exec, s[12:13]
	ds_read_b32 v4, v173 offset:68
	s_waitcnt lgkmcnt(0)
	v_rcp_f32_e32 v4, v4
	s_nop 0
	v_mul_f32_e32 v4, 0x41800000, v4
	v_mul_f32_e32 v5, v61, v4
	s_nop 1
	v_mov_b32_dpp v7, v5 quad_perm:[1,0,3,2] row_mask:0xf bank_mask:0xf
	s_nop 1
	v_mov_b32_dpp v6, v5 quad_perm:[2,3,0,1] row_mask:0xf bank_mask:0xf
	s_waitcnt lgkmcnt(0)
	s_nop 1
	v_mov_b32_dpp v8, v7 quad_perm:[2,3,0,1] row_mask:0xf bank_mask:0xf
	s_and_saveexec_b64 s[12:13], s[6:7]
	s_cbranch_execz .LBB0_1721
	v_mov_b32_e32 v9, v3
	v_cvt_pk_fp8_f32 v9, v5, v7
	s_waitcnt lgkmcnt(0)
	v_cvt_pk_fp8_f32 v9, v6, v8 op_sel:[0,0,1]
	v_add_co_u32_e32 v6, vcc, 0x8000, v68
	s_nop 1
	v_addc_co_u32_e32 v7, vcc, 0, v69, vcc
	global_store_dword v[6:7], v9, off offset:2048
.LBB0_1721:
	s_or_b64 exec, exec, s[12:13]
	v_mul_f32_e32 v5, v45, v4
	s_nop 1
	v_mov_b32_dpp v7, v5 quad_perm:[1,0,3,2] row_mask:0xf bank_mask:0xf
	s_waitcnt lgkmcnt(0)
	s_nop 1
	v_mov_b32_dpp v6, v5 quad_perm:[2,3,0,1] row_mask:0xf bank_mask:0xf
	s_waitcnt lgkmcnt(0)
	s_nop 1
	v_mov_b32_dpp v8, v7 quad_perm:[2,3,0,1] row_mask:0xf bank_mask:0xf
	s_and_saveexec_b64 s[12:13], s[6:7]
	s_cbranch_execz .LBB0_1723
	v_mov_b32_e32 v9, v3
	v_cvt_pk_fp8_f32 v9, v5, v7
	s_waitcnt lgkmcnt(0)
	v_cvt_pk_fp8_f32 v9, v6, v8 op_sel:[0,0,1]
	v_add_co_u32_e32 v6, vcc, 0x8000, v68
	s_nop 1
	v_addc_co_u32_e32 v7, vcc, 0, v69, vcc
	global_store_dword v[6:7], v9, off offset:2080
.LBB0_1723:
	s_or_b64 exec, exec, s[12:13]
	v_mul_f32_e32 v5, v29, v4
	s_nop 1
	v_mov_b32_dpp v7, v5 quad_perm:[1,0,3,2] row_mask:0xf bank_mask:0xf
	s_waitcnt lgkmcnt(0)
	s_nop 1
	v_mov_b32_dpp v6, v5 quad_perm:[2,3,0,1] row_mask:0xf bank_mask:0xf
	s_waitcnt lgkmcnt(0)
	s_nop 1
	v_mov_b32_dpp v8, v7 quad_perm:[2,3,0,1] row_mask:0xf bank_mask:0xf
	s_and_saveexec_b64 s[12:13], s[6:7]
	s_cbranch_execz .LBB0_1725
	v_mov_b32_e32 v9, v3
	v_cvt_pk_fp8_f32 v9, v5, v7
	s_waitcnt lgkmcnt(0)
	v_cvt_pk_fp8_f32 v9, v6, v8 op_sel:[0,0,1]
	v_add_co_u32_e32 v6, vcc, 0x8000, v68
	s_nop 1
	v_addc_co_u32_e32 v7, vcc, 0, v69, vcc
	global_store_dword v[6:7], v9, off offset:2112
.LBB0_1725:
	s_or_b64 exec, exec, s[12:13]
	v_mul_f32_e32 v4, v13, v4
	s_waitcnt lgkmcnt(0)
	s_nop 1
	v_mov_b32_dpp v6, v4 quad_perm:[1,0,3,2] row_mask:0xf bank_mask:0xf
	s_nop 1
	v_mov_b32_dpp v5, v4 quad_perm:[2,3,0,1] row_mask:0xf bank_mask:0xf
	s_waitcnt lgkmcnt(0)
	s_nop 1
	v_mov_b32_dpp v7, v6 quad_perm:[2,3,0,1] row_mask:0xf bank_mask:0xf
	s_and_saveexec_b64 s[12:13], s[6:7]
	s_cbranch_execz .LBB0_1727
	v_mov_b32_e32 v8, v3
	v_cvt_pk_fp8_f32 v8, v4, v6
	v_add_co_u32_e32 v4, vcc, 0x8000, v68
	s_waitcnt lgkmcnt(0)
	v_cvt_pk_fp8_f32 v8, v5, v7 op_sel:[0,0,1]
	v_addc_co_u32_e32 v5, vcc, 0, v69, vcc
	global_store_dword v[4:5], v8, off offset:2144
; __device__ __forceinline__ unsigned cvt4_fp8(float a, float b, float c, float d) { int w = 0; w = __builtin_amdgcn_cvt_pk_fp8_f32(a, b, w, false); w = __builtin_amdgcn_cvt_pk_fp8_f32(c, d, w, true); return (unsigned)w; }
; template <bool MLA>
; __device__ __forceinline__ void attn_unit(char* lds, int h, int qb, const bf16_t* Qp, int ldq, const bf16_t* Kp, int ldk, const bf16_t* KRp, const bf16_t* Vp, int ldv,
;                                           unsigned char* Op, int ldo, const float* KMp, const float* rel_bias) {
;     ...
;     for (int r = 0; r < 16; ++r) { const int orow = CROWC(r) + 4 * hi; const float rl = 16.0f * __builtin_amdgcn_rcpf(li_h[CROWC(r)]);
; #pragma unroll
;         for (int d0 = 0; d0 < 4; ++d0) { const float v = o[d0][r] * rl; const float v1 = __shfl_xor(v, 1), v2 = __shfl_xor(v, 2), v3 = __shfl_xor(v1, 2);
;             if ((r32 & 3) == 0) *(unsigned*)(Ow + (size_t)orow * ldo + d0 * 32 + r32) = cvt4_fp8(v, v1, v2, v3); } }
.LBB0_1727:
	s_or_b64 exec, exec, s[12:13]
	ds_read_b32 v4, v173 offset:72
	s_waitcnt lgkmcnt(0)
	v_rcp_f32_e32 v4, v4
	s_nop 0
	v_mul_f32_e32 v4, 0x41800000, v4
	v_mul_f32_e32 v5, v62, v4
	s_nop 1
	v_mov_b32_dpp v7, v5 quad_perm:[1,0,3,2] row_mask:0xf bank_mask:0xf
	s_nop 1
	v_mov_b32_dpp v6, v5 quad_perm:[2,3,0,1] row_mask:0xf bank_mask:0xf
	s_waitcnt lgkmcnt(0)
	s_nop 1
	v_mov_b32_dpp v8, v7 quad_perm:[2,3,0,1] row_mask:0xf bank_mask:0xf
	s_and_saveexec_b64 s[12:13], s[6:7]
	s_cbranch_execz .LBB0_1729
	v_mov_b32_e32 v9, v3
	v_cvt_pk_fp8_f32 v9, v5, v7
	s_waitcnt lgkmcnt(0)
	v_cvt_pk_fp8_f32 v9, v6, v8 op_sel:[0,0,1]
	v_add_co_u32_e32 v6, vcc, 0x9000, v68
	s_nop 1
	v_addc_co_u32_e32 v7, vcc, 0, v69, vcc
	global_store_dword v[6:7], v9, off
.LBB0_1729:
	s_or_b64 exec, exec, s[12:13]
	v_mul_f32_e32 v5, v46, v4
	s_nop 1
	v_mov_b32_dpp v7, v5 quad_perm:[1,0,3,2] row_mask:0xf bank_mask:0xf
	s_waitcnt lgkmcnt(0)
	s_nop 1
	v_mov_b32_dpp v6, v5 quad_perm:[2,3,0,1] row_mask:0xf bank_mask:0xf
	s_waitcnt lgkmcnt(0)
	s_nop 1
	v_mov_b32_dpp v8, v7 quad_perm:[2,3,0,1] row_mask:0xf bank_mask:0xf
	s_and_saveexec_b64 s[12:13], s[6:7]
	s_cbranch_execz .LBB0_1731
	v_mov_b32_e32 v9, v3
	v_cvt_pk_fp8_f32 v9, v5, v7
	s_waitcnt lgkmcnt(0)
	v_cvt_pk_fp8_f32 v9, v6, v8 op_sel:[0,0,1]
	v_add_co_u32_e32 v6, vcc, 0x9000, v68
	s_nop 1
	v_addc_co_u32_e32 v7, vcc, 0, v69, vcc
	global_store_dword v[6:7], v9, off offset:32
.LBB0_1731:
	s_or_b64 exec, exec, s[12:13]
	v_mul_f32_e32 v5, v30, v4
	s_nop 1
	v_mov_b32_dpp v7, v5 quad_perm:[1,0,3,2] row_mask:0xf bank_mask:0xf
	s_waitcnt lgkmcnt(0)
	s_nop 1
	v_mov_b32_dpp v6, v5 quad_perm:[2,3,0,1] row_mask:0xf bank_mask:0xf
	s_waitcnt lgkmcnt(0)
	s_nop 1
	v_mov_b32_dpp v8, v7 quad_perm:[2,3,0,1] row_mask:0xf bank_mask:0xf
	s_and_saveexec_b64 s[12:13], s[6:7]
	s_cbranch_execz .LBB0_1733
	v_mov_b32_e32 v9, v3
	v_cvt_pk_fp8_f32 v9, v5, v7
	s_waitcnt lgkmcnt(0)
	v_cvt_pk_fp8_f32 v9, v6, v8 op_sel:[0,0,1]
	v_add_co_u32_e32 v6, vcc, 0x9000, v68
	s_nop 1
	v_addc_co_u32_e32 v7, vcc, 0, v69, vcc
	global_store_dword v[6:7], v9, off offset:64
.LBB0_1733:
	s_or_b64 exec, exec, s[12:13]
	v_mul_f32_e32 v4, v14, v4
	s_waitcnt lgkmcnt(0)
	s_nop 1
	v_mov_b32_dpp v6, v4 quad_perm:[1,0,3,2] row_mask:0xf bank_mask:0xf
	s_nop 1
	v_mov_b32_dpp v5, v4 quad_perm:[2,3,0,1] row_mask:0xf bank_mask:0xf
	s_waitcnt lgkmcnt(0)
	s_nop 1
	v_mov_b32_dpp v7, v6 quad_perm:[2,3,0,1] row_mask:0xf bank_mask:0xf
	s_and_saveexec_b64 s[12:13], s[6:7]
	s_cbranch_execz .LBB0_1735
	v_mov_b32_e32 v8, v3
	v_cvt_pk_fp8_f32 v8, v4, v6
	v_add_co_u32_e32 v4, vcc, 0x9000, v68
	s_waitcnt lgkmcnt(0)
	v_cvt_pk_fp8_f32 v8, v5, v7 op_sel:[0,0,1]
	v_addc_co_u32_e32 v5, vcc, 0, v69, vcc
	global_store_dword v[4:5], v8, off offset:96
.LBB0_1735:
	s_or_b64 exec, exec, s[12:13]
	ds_read_b32 v4, v173 offset:76
	s_waitcnt lgkmcnt(0)
	v_rcp_f32_e32 v4, v4
	s_nop 0
	v_mul_f32_e32 v4, 0x41800000, v4
	v_mul_f32_e32 v5, v63, v4
	s_nop 1
	v_mov_b32_dpp v7, v5 quad_perm:[1,0,3,2] row_mask:0xf bank_mask:0xf
	s_nop 1
	v_mov_b32_dpp v6, v5 quad_perm:[2,3,0,1] row_mask:0xf bank_mask:0xf
	s_waitcnt lgkmcnt(0)
	s_nop 1
	v_mov_b32_dpp v8, v7 quad_perm:[2,3,0,1] row_mask:0xf bank_mask:0xf
	s_and_saveexec_b64 s[12:13], s[6:7]
	s_cbranch_execz .LBB0_1737
	v_mov_b32_e32 v9, v3
	v_cvt_pk_fp8_f32 v9, v5, v7
	s_waitcnt lgkmcnt(0)
	v_cvt_pk_fp8_f32 v9, v6, v8 op_sel:[0,0,1]
	v_add_co_u32_e32 v6, vcc, 0x9000, v68
	s_nop 1
	v_addc_co_u32_e32 v7, vcc, 0, v69, vcc
	global_store_dword v[6:7], v9, off offset:2048
.LBB0_1737:
	s_or_b64 exec, exec, s[12:13]
	v_mul_f32_e32 v5, v47, v4
	s_nop 1
	v_mov_b32_dpp v7, v5 quad_perm:[1,0,3,2] row_mask:0xf bank_mask:0xf
	s_waitcnt lgkmcnt(0)
	s_nop 1
	v_mov_b32_dpp v6, v5 quad_perm:[2,3,0,1] row_mask:0xf bank_mask:0xf
	s_waitcnt lgkmcnt(0)
	s_nop 1
	v_mov_b32_dpp v8, v7 quad_perm:[2,3,0,1] row_mask:0xf bank_mask:0xf
	s_and_saveexec_b64 s[12:13], s[6:7]
	s_cbranch_execz .LBB0_1739
	v_mov_b32_e32 v9, v3
	v_cvt_pk_fp8_f32 v9, v5, v7
	s_waitcnt lgkmcnt(0)
	v_cvt_pk_fp8_f32 v9, v6, v8 op_sel:[0,0,1]
	v_add_co_u32_e32 v6, vcc, 0x9000, v68
	s_nop 1
	v_addc_co_u32_e32 v7, vcc, 0, v69, vcc
	global_store_dword v[6:7], v9, off offset:2080
.LBB0_1739:
	s_or_b64 exec, exec, s[12:13]
	v_mul_f32_e32 v5, v31, v4
	s_nop 1
	v_mov_b32_dpp v7, v5 quad_perm:[1,0,3,2] row_mask:0xf bank_mask:0xf
	s_waitcnt lgkmcnt(0)
	s_nop 1
	v_mov_b32_dpp v6, v5 quad_perm:[2,3,0,1] row_mask:0xf bank_mask:0xf
	s_waitcnt lgkmcnt(0)
	s_nop 1
	v_mov_b32_dpp v8, v7 quad_perm:[2,3,0,1] row_mask:0xf bank_mask:0xf
	s_and_saveexec_b64 s[12:13], s[6:7]
	s_cbranch_execz .LBB0_1741
	v_mov_b32_e32 v9, v3
	v_cvt_pk_fp8_f32 v9, v5, v7
	s_waitcnt lgkmcnt(0)
	v_cvt_pk_fp8_f32 v9, v6, v8 op_sel:[0,0,1]
	v_add_co_u32_e32 v6, vcc, 0x9000, v68
	s_nop 1
	v_addc_co_u32_e32 v7, vcc, 0, v69, vcc
	global_store_dword v[6:7], v9, off offset:2112
.LBB0_1741:
	s_or_b64 exec, exec, s[12:13]
	v_mul_f32_e32 v4, v15, v4
	s_waitcnt lgkmcnt(0)
	s_nop 1
	v_mov_b32_dpp v6, v4 quad_perm:[1,0,3,2] row_mask:0xf bank_mask:0xf
	s_nop 1
	v_mov_b32_dpp v5, v4 quad_perm:[2,3,0,1] row_mask:0xf bank_mask:0xf
	s_waitcnt lgkmcnt(0)
	s_nop 1
	v_mov_b32_dpp v7, v6 quad_perm:[2,3,0,1] row_mask:0xf bank_mask:0xf
	s_and_saveexec_b64 s[12:13], s[6:7]
	s_cbranch_execz .LBB0_1743
	v_mov_b32_e32 v8, v3
	v_cvt_pk_fp8_f32 v8, v4, v6
	v_add_co_u32_e32 v4, vcc, 0x9000, v68
	s_waitcnt lgkmcnt(0)
	v_cvt_pk_fp8_f32 v8, v5, v7 op_sel:[0,0,1]
	v_addc_co_u32_e32 v5, vcc, 0, v69, vcc
	global_store_dword v[4:5], v8, off offset:2144
; __device__ __forceinline__ unsigned cvt4_fp8(float a, float b, float c, float d) { int w = 0; w = __builtin_amdgcn_cvt_pk_fp8_f32(a, b, w, false); w = __builtin_amdgcn_cvt_pk_fp8_f32(c, d, w, true); return (unsigned)w; }
; template <bool MLA>
; __device__ __forceinline__ void attn_unit(char* lds, int h, int qb, const bf16_t* Qp, int ldq, const bf16_t* Kp, int ldk, const bf16_t* KRp, const bf16_t* Vp, int ldv,
;                                           unsigned char* Op, int ldo, const float* KMp, const float* rel_bias) {
;     ...
;     for (int r = 0; r < 16; ++r) { const int orow = CROWC(r) + 4 * hi; const float rl = 16.0f * __builtin_amdgcn_rcpf(li_h[CROWC(r)]);
; #pragma unroll
;         for (int d0 = 0; d0 < 4; ++d0) { const float v = o[d0][r] * rl; const float v1 = __shfl_xor(v, 1), v2 = __shfl_xor(v, 2), v3 = __shfl_xor(v1, 2);
;             if ((r32 & 3) == 0) *(unsigned*)(Ow + (size_t)orow * ldo + d0 * 32 + r32) = cvt4_fp8(v, v1, v2, v3); } }
.LBB0_1743:
	s_or_b64 exec, exec, s[12:13]
	ds_read_b32 v4, v173 offset:96
	s_waitcnt lgkmcnt(0)
	v_rcp_f32_e32 v4, v4
	s_nop 0
	v_mul_f32_e32 v4, 0x41800000, v4
	v_mul_f32_e32 v5, v64, v4
	s_nop 1
	v_mov_b32_dpp v7, v5 quad_perm:[1,0,3,2] row_mask:0xf bank_mask:0xf
	s_nop 1
	v_mov_b32_dpp v6, v5 quad_perm:[2,3,0,1] row_mask:0xf bank_mask:0xf
	s_waitcnt lgkmcnt(0)
	s_nop 1
	v_mov_b32_dpp v8, v7 quad_perm:[2,3,0,1] row_mask:0xf bank_mask:0xf
	s_and_saveexec_b64 s[12:13], s[6:7]
	s_cbranch_execz .LBB0_1745
	v_mov_b32_e32 v9, v3
	v_cvt_pk_fp8_f32 v9, v5, v7
	s_waitcnt lgkmcnt(0)
	v_cvt_pk_fp8_f32 v9, v6, v8 op_sel:[0,0,1]
	v_add_co_u32_e32 v6, vcc, 0xc000, v68
	s_nop 1
	v_addc_co_u32_e32 v7, vcc, 0, v69, vcc
	global_store_dword v[6:7], v9, off
.LBB0_1745:
	s_or_b64 exec, exec, s[12:13]
	v_mul_f32_e32 v5, v48, v4
	s_nop 1
	v_mov_b32_dpp v7, v5 quad_perm:[1,0,3,2] row_mask:0xf bank_mask:0xf
	s_waitcnt lgkmcnt(0)
	s_nop 1
	v_mov_b32_dpp v6, v5 quad_perm:[2,3,0,1] row_mask:0xf bank_mask:0xf
	s_waitcnt lgkmcnt(0)
	s_nop 1
	v_mov_b32_dpp v8, v7 quad_perm:[2,3,0,1] row_mask:0xf bank_mask:0xf
	s_and_saveexec_b64 s[12:13], s[6:7]
	s_cbranch_execz .LBB0_1747
	v_mov_b32_e32 v9, v3
	v_cvt_pk_fp8_f32 v9, v5, v7
	s_waitcnt lgkmcnt(0)
	v_cvt_pk_fp8_f32 v9, v6, v8 op_sel:[0,0,1]
	v_add_co_u32_e32 v6, vcc, 0xc000, v68
	s_nop 1
	v_addc_co_u32_e32 v7, vcc, 0, v69, vcc
	global_store_dword v[6:7], v9, off offset:32
.LBB0_1747:
	s_or_b64 exec, exec, s[12:13]
	v_mul_f32_e32 v5, v32, v4
	s_nop 1
	v_mov_b32_dpp v7, v5 quad_perm:[1,0,3,2] row_mask:0xf bank_mask:0xf
	s_waitcnt lgkmcnt(0)
	s_nop 1
	v_mov_b32_dpp v6, v5 quad_perm:[2,3,0,1] row_mask:0xf bank_mask:0xf
	s_waitcnt lgkmcnt(0)
	s_nop 1
	v_mov_b32_dpp v8, v7 quad_perm:[2,3,0,1] row_mask:0xf bank_mask:0xf
	s_and_saveexec_b64 s[12:13], s[6:7]
	s_cbranch_execz .LBB0_1749
	v_mov_b32_e32 v9, v3
	v_cvt_pk_fp8_f32 v9, v5, v7
	s_waitcnt lgkmcnt(0)
	v_cvt_pk_fp8_f32 v9, v6, v8 op_sel:[0,0,1]
	v_add_co_u32_e32 v6, vcc, 0xc000, v68
	s_nop 1
	v_addc_co_u32_e32 v7, vcc, 0, v69, vcc
	global_store_dword v[6:7], v9, off offset:64
.LBB0_1749:
	s_or_b64 exec, exec, s[12:13]
	v_mul_f32_e32 v4, v16, v4
	s_waitcnt lgkmcnt(0)
	s_nop 1
	v_mov_b32_dpp v6, v4 quad_perm:[1,0,3,2] row_mask:0xf bank_mask:0xf
	s_nop 1
	v_mov_b32_dpp v5, v4 quad_perm:[2,3,0,1] row_mask:0xf bank_mask:0xf
	s_waitcnt lgkmcnt(0)
	s_nop 1
	v_mov_b32_dpp v7, v6 quad_perm:[2,3,0,1] row_mask:0xf bank_mask:0xf
	s_and_saveexec_b64 s[12:13], s[6:7]
	s_cbranch_execz .LBB0_1751
	v_mov_b32_e32 v8, v3
	v_cvt_pk_fp8_f32 v8, v4, v6
	v_add_co_u32_e32 v4, vcc, 0xc000, v68
	s_waitcnt lgkmcnt(0)
	v_cvt_pk_fp8_f32 v8, v5, v7 op_sel:[0,0,1]
	v_addc_co_u32_e32 v5, vcc, 0, v69, vcc
	global_store_dword v[4:5], v8, off offset:96
.LBB0_1751:
	s_or_b64 exec, exec, s[12:13]
	ds_read_b32 v4, v173 offset:100
	s_waitcnt lgkmcnt(0)
	v_rcp_f32_e32 v4, v4
	s_nop 0
	v_mul_f32_e32 v4, 0x41800000, v4
	v_mul_f32_e32 v5, v65, v4
	s_nop 1
	v_mov_b32_dpp v7, v5 quad_perm:[1,0,3,2] row_mask:0xf bank_mask:0xf
	s_nop 1
	v_mov_b32_dpp v6, v5 quad_perm:[2,3,0,1] row_mask:0xf bank_mask:0xf
	s_waitcnt lgkmcnt(0)
	s_nop 1
	v_mov_b32_dpp v8, v7 quad_perm:[2,3,0,1] row_mask:0xf bank_mask:0xf
	s_and_saveexec_b64 s[12:13], s[6:7]
	s_cbranch_execz .LBB0_1753
	v_mov_b32_e32 v9, v3
	v_cvt_pk_fp8_f32 v9, v5, v7
	s_waitcnt lgkmcnt(0)
	v_cvt_pk_fp8_f32 v9, v6, v8 op_sel:[0,0,1]
	v_add_co_u32_e32 v6, vcc, 0xc000, v68
	s_nop 1
	v_addc_co_u32_e32 v7, vcc, 0, v69, vcc
	global_store_dword v[6:7], v9, off offset:2048
.LBB0_1753:
	s_or_b64 exec, exec, s[12:13]
	v_mul_f32_e32 v5, v49, v4
	s_nop 1
	v_mov_b32_dpp v7, v5 quad_perm:[1,0,3,2] row_mask:0xf bank_mask:0xf
	s_waitcnt lgkmcnt(0)
	s_nop 1
	v_mov_b32_dpp v6, v5 quad_perm:[2,3,0,1] row_mask:0xf bank_mask:0xf
	s_waitcnt lgkmcnt(0)
	s_nop 1
	v_mov_b32_dpp v8, v7 quad_perm:[2,3,0,1] row_mask:0xf bank_mask:0xf
	s_and_saveexec_b64 s[12:13], s[6:7]
	s_cbranch_execz .LBB0_1755
	v_mov_b32_e32 v9, v3
	v_cvt_pk_fp8_f32 v9, v5, v7
	s_waitcnt lgkmcnt(0)
	v_cvt_pk_fp8_f32 v9, v6, v8 op_sel:[0,0,1]
	v_add_co_u32_e32 v6, vcc, 0xc000, v68
	s_nop 1
	v_addc_co_u32_e32 v7, vcc, 0, v69, vcc
	global_store_dword v[6:7], v9, off offset:2080
.LBB0_1755:
	s_or_b64 exec, exec, s[12:13]
	v_mul_f32_e32 v5, v33, v4
	s_nop 1
	v_mov_b32_dpp v7, v5 quad_perm:[1,0,3,2] row_mask:0xf bank_mask:0xf
	s_waitcnt lgkmcnt(0)
	s_nop 1
	v_mov_b32_dpp v6, v5 quad_perm:[2,3,0,1] row_mask:0xf bank_mask:0xf
	s_waitcnt lgkmcnt(0)
	s_nop 1
	v_mov_b32_dpp v8, v7 quad_perm:[2,3,0,1] row_mask:0xf bank_mask:0xf
	s_and_saveexec_b64 s[12:13], s[6:7]
	s_cbranch_execz .LBB0_1757
	v_mov_b32_e32 v9, v3
	v_cvt_pk_fp8_f32 v9, v5, v7
	s_waitcnt lgkmcnt(0)
	v_cvt_pk_fp8_f32 v9, v6, v8 op_sel:[0,0,1]
	v_add_co_u32_e32 v6, vcc, 0xc000, v68
	s_nop 1
	v_addc_co_u32_e32 v7, vcc, 0, v69, vcc
	global_store_dword v[6:7], v9, off offset:2112
.LBB0_1757:
	s_or_b64 exec, exec, s[12:13]
	v_mul_f32_e32 v4, v17, v4
	s_waitcnt lgkmcnt(0)
	s_nop 1
	v_mov_b32_dpp v6, v4 quad_perm:[1,0,3,2] row_mask:0xf bank_mask:0xf
	s_nop 1
	v_mov_b32_dpp v5, v4 quad_perm:[2,3,0,1] row_mask:0xf bank_mask:0xf
	s_waitcnt lgkmcnt(0)
	s_nop 1
	v_mov_b32_dpp v7, v6 quad_perm:[2,3,0,1] row_mask:0xf bank_mask:0xf
	s_and_saveexec_b64 s[12:13], s[6:7]
	s_cbranch_execz .LBB0_1759
	v_mov_b32_e32 v8, v3
	v_cvt_pk_fp8_f32 v8, v4, v6
	v_add_co_u32_e32 v4, vcc, 0xc000, v68
	s_waitcnt lgkmcnt(0)
	v_cvt_pk_fp8_f32 v8, v5, v7 op_sel:[0,0,1]
	v_addc_co_u32_e32 v5, vcc, 0, v69, vcc
	global_store_dword v[4:5], v8, off offset:2144
; __device__ __forceinline__ unsigned cvt4_fp8(float a, float b, float c, float d) { int w = 0; w = __builtin_amdgcn_cvt_pk_fp8_f32(a, b, w, false); w = __builtin_amdgcn_cvt_pk_fp8_f32(c, d, w, true); return (unsigned)w; }
; template <bool MLA>
; __device__ __forceinline__ void attn_unit(char* lds, int h, int qb, const bf16_t* Qp, int ldq, const bf16_t* Kp, int ldk, const bf16_t* KRp, const bf16_t* Vp, int ldv,
;                                           unsigned char* Op, int ldo, const float* KMp, const float* rel_bias) {
;     ...
;     for (int r = 0; r < 16; ++r) { const int orow = CROWC(r) + 4 * hi; const float rl = 16.0f * __builtin_amdgcn_rcpf(li_h[CROWC(r)]);
; #pragma unroll
;         for (int d0 = 0; d0 < 4; ++d0) { const float v = o[d0][r] * rl; const float v1 = __shfl_xor(v, 1), v2 = __shfl_xor(v, 2), v3 = __shfl_xor(v1, 2);
;             if ((r32 & 3) == 0) *(unsigned*)(Ow + (size_t)orow * ldo + d0 * 32 + r32) = cvt4_fp8(v, v1, v2, v3); } }
.LBB0_1759:
	s_or_b64 exec, exec, s[12:13]
	ds_read_b32 v4, v173 offset:104
	s_waitcnt lgkmcnt(0)
	v_rcp_f32_e32 v4, v4
	s_nop 0
	v_mul_f32_e32 v4, 0x41800000, v4
	v_mul_f32_e32 v5, v66, v4
	s_nop 1
	v_mov_b32_dpp v7, v5 quad_perm:[1,0,3,2] row_mask:0xf bank_mask:0xf
	s_nop 1
	v_mov_b32_dpp v6, v5 quad_perm:[2,3,0,1] row_mask:0xf bank_mask:0xf
	s_waitcnt lgkmcnt(0)
	s_nop 1
	v_mov_b32_dpp v8, v7 quad_perm:[2,3,0,1] row_mask:0xf bank_mask:0xf
	s_and_saveexec_b64 s[12:13], s[6:7]
	s_cbranch_execz .LBB0_1761
	v_mov_b32_e32 v9, v3
	v_cvt_pk_fp8_f32 v9, v5, v7
	s_waitcnt lgkmcnt(0)
	v_cvt_pk_fp8_f32 v9, v6, v8 op_sel:[0,0,1]
	v_add_co_u32_e32 v6, vcc, 0xd000, v68
	s_nop 1
	v_addc_co_u32_e32 v7, vcc, 0, v69, vcc
	global_store_dword v[6:7], v9, off
.LBB0_1761:
	s_or_b64 exec, exec, s[12:13]
	v_mul_f32_e32 v5, v50, v4
	s_nop 1
	v_mov_b32_dpp v7, v5 quad_perm:[1,0,3,2] row_mask:0xf bank_mask:0xf
	s_waitcnt lgkmcnt(0)
	s_nop 1
	v_mov_b32_dpp v6, v5 quad_perm:[2,3,0,1] row_mask:0xf bank_mask:0xf
	s_waitcnt lgkmcnt(0)
	s_nop 1
	v_mov_b32_dpp v8, v7 quad_perm:[2,3,0,1] row_mask:0xf bank_mask:0xf
	s_and_saveexec_b64 s[12:13], s[6:7]
	s_cbranch_execz .LBB0_1763
	v_mov_b32_e32 v9, v3
	v_cvt_pk_fp8_f32 v9, v5, v7
	s_waitcnt lgkmcnt(0)
	v_cvt_pk_fp8_f32 v9, v6, v8 op_sel:[0,0,1]
	v_add_co_u32_e32 v6, vcc, 0xd000, v68
	s_nop 1
	v_addc_co_u32_e32 v7, vcc, 0, v69, vcc
	global_store_dword v[6:7], v9, off offset:32
.LBB0_1763:
	s_or_b64 exec, exec, s[12:13]
	v_mul_f32_e32 v5, v34, v4
	s_nop 1
	v_mov_b32_dpp v7, v5 quad_perm:[1,0,3,2] row_mask:0xf bank_mask:0xf
	s_waitcnt lgkmcnt(0)
	s_nop 1
	v_mov_b32_dpp v6, v5 quad_perm:[2,3,0,1] row_mask:0xf bank_mask:0xf
	s_waitcnt lgkmcnt(0)
	s_nop 1
	v_mov_b32_dpp v8, v7 quad_perm:[2,3,0,1] row_mask:0xf bank_mask:0xf
	s_and_saveexec_b64 s[12:13], s[6:7]
	s_cbranch_execz .LBB0_1765
	v_mov_b32_e32 v9, v3
	v_cvt_pk_fp8_f32 v9, v5, v7
	s_waitcnt lgkmcnt(0)
	v_cvt_pk_fp8_f32 v9, v6, v8 op_sel:[0,0,1]
	v_add_co_u32_e32 v6, vcc, 0xd000, v68
	s_nop 1
	v_addc_co_u32_e32 v7, vcc, 0, v69, vcc
	global_store_dword v[6:7], v9, off offset:64
.LBB0_1765:
	s_or_b64 exec, exec, s[12:13]
	v_mul_f32_e32 v4, v18, v4
	s_waitcnt lgkmcnt(0)
	s_nop 1
	v_mov_b32_dpp v6, v4 quad_perm:[1,0,3,2] row_mask:0xf bank_mask:0xf
	s_nop 1
	v_mov_b32_dpp v5, v4 quad_perm:[2,3,0,1] row_mask:0xf bank_mask:0xf
	s_waitcnt lgkmcnt(0)
	s_nop 1
	v_mov_b32_dpp v7, v6 quad_perm:[2,3,0,1] row_mask:0xf bank_mask:0xf
	s_and_saveexec_b64 s[12:13], s[6:7]
	s_cbranch_execz .LBB0_1767
	v_mov_b32_e32 v8, v3
	v_cvt_pk_fp8_f32 v8, v4, v6
	v_add_co_u32_e32 v4, vcc, 0xd000, v68
	s_waitcnt lgkmcnt(0)
	v_cvt_pk_fp8_f32 v8, v5, v7 op_sel:[0,0,1]
	v_addc_co_u32_e32 v5, vcc, 0, v69, vcc
	global_store_dword v[4:5], v8, off offset:96
.LBB0_1767:
	s_or_b64 exec, exec, s[12:13]
	ds_read_b32 v4, v173 offset:108
	s_waitcnt lgkmcnt(0)
	v_rcp_f32_e32 v4, v4
	s_nop 0
	v_mul_f32_e32 v4, 0x41800000, v4
	v_mul_f32_e32 v5, v67, v4
	s_nop 1
	v_mov_b32_dpp v7, v5 quad_perm:[1,0,3,2] row_mask:0xf bank_mask:0xf
	s_nop 1
	v_mov_b32_dpp v6, v5 quad_perm:[2,3,0,1] row_mask:0xf bank_mask:0xf
	s_waitcnt lgkmcnt(0)
	s_nop 1
	v_mov_b32_dpp v8, v7 quad_perm:[2,3,0,1] row_mask:0xf bank_mask:0xf
	s_and_saveexec_b64 s[12:13], s[6:7]
	s_cbranch_execz .LBB0_1769
	v_mov_b32_e32 v9, v3
	v_cvt_pk_fp8_f32 v9, v5, v7
	s_waitcnt lgkmcnt(0)
	v_cvt_pk_fp8_f32 v9, v6, v8 op_sel:[0,0,1]
	v_add_co_u32_e32 v6, vcc, 0xd000, v68
	s_nop 1
	v_addc_co_u32_e32 v7, vcc, 0, v69, vcc
	global_store_dword v[6:7], v9, off offset:2048
.LBB0_1769:
	s_or_b64 exec, exec, s[12:13]
	v_mul_f32_e32 v5, v51, v4
	s_nop 1
	v_mov_b32_dpp v7, v5 quad_perm:[1,0,3,2] row_mask:0xf bank_mask:0xf
	s_waitcnt lgkmcnt(0)
	s_nop 1
	v_mov_b32_dpp v6, v5 quad_perm:[2,3,0,1] row_mask:0xf bank_mask:0xf
	s_waitcnt lgkmcnt(0)
	s_nop 1
	v_mov_b32_dpp v8, v7 quad_perm:[2,3,0,1] row_mask:0xf bank_mask:0xf
	s_and_saveexec_b64 s[12:13], s[6:7]
	s_cbranch_execz .LBB0_1771
	v_mov_b32_e32 v9, v3
	v_cvt_pk_fp8_f32 v9, v5, v7
	s_waitcnt lgkmcnt(0)
	v_cvt_pk_fp8_f32 v9, v6, v8 op_sel:[0,0,1]
	v_add_co_u32_e32 v6, vcc, 0xd000, v68
	s_nop 1
	v_addc_co_u32_e32 v7, vcc, 0, v69, vcc
	global_store_dword v[6:7], v9, off offset:2080
.LBB0_1771:
	s_or_b64 exec, exec, s[12:13]
	v_mul_f32_e32 v5, v35, v4
	s_nop 1
	v_mov_b32_dpp v7, v5 quad_perm:[1,0,3,2] row_mask:0xf bank_mask:0xf
	s_waitcnt lgkmcnt(0)
	s_nop 1
	v_mov_b32_dpp v6, v5 quad_perm:[2,3,0,1] row_mask:0xf bank_mask:0xf
	s_waitcnt lgkmcnt(0)
	s_nop 1
	v_mov_b32_dpp v8, v7 quad_perm:[2,3,0,1] row_mask:0xf bank_mask:0xf
	s_and_saveexec_b64 s[12:13], s[6:7]
	s_cbranch_execz .LBB0_1773
	v_mov_b32_e32 v9, v3
	v_cvt_pk_fp8_f32 v9, v5, v7
	s_waitcnt lgkmcnt(0)
	v_cvt_pk_fp8_f32 v9, v6, v8 op_sel:[0,0,1]
	v_add_co_u32_e32 v6, vcc, 0xd000, v68
	s_nop 1
	v_addc_co_u32_e32 v7, vcc, 0, v69, vcc
	global_store_dword v[6:7], v9, off offset:2112
.LBB0_1773:
	s_or_b64 exec, exec, s[12:13]
	v_mul_f32_e32 v4, v19, v4
	s_nop 1
	v_mov_b32_dpp v5, v4 quad_perm:[1,0,3,2] row_mask:0xf bank_mask:0xf
	s_nop 1
	v_mov_b32_dpp v2, v4 quad_perm:[2,3,0,1] row_mask:0xf bank_mask:0xf
	s_waitcnt lgkmcnt(0)
	s_nop 1
	v_mov_b32_dpp v6, v5 quad_perm:[2,3,0,1] row_mask:0xf bank_mask:0xf
	s_and_saveexec_b64 s[12:13], s[6:7]
	s_cbranch_execz .LBB0_1525
	v_mov_b32_e32 v7, v3
	v_cvt_pk_fp8_f32 v7, v4, v5
	v_add_co_u32_e32 v4, vcc, 0xd000, v68
	s_waitcnt lgkmcnt(0)
	v_cvt_pk_fp8_f32 v7, v2, v6 op_sel:[0,0,1]
	v_addc_co_u32_e32 v5, vcc, 0, v69, vcc
	global_store_dword v[4:5], v7, off offset:2144
	s_branch .LBB0_1525
